# GEMM load segments: the s_nop separators between consecutive LDS-DMA wrappers removed (128 sites), on top of v144
# speedup vs baseline: 1.0016x; 1.0016x over previous
.LBB0_143:
	ds_read_b128 v[148:151], v142
	ds_read_b128 v[152:155], v142 offset:1024
	ds_read_b128 v[156:159], v142 offset:2048
	ds_read_b128 v[160:163], v142 offset:3072
	ds_read_b128 v[164:167], v143
	ds_read_b128 v[174:177], v143 offset:1024
	ds_read_b128 v[178:181], v143 offset:2048
	ds_read_b128 v[182:185], v143 offset:3072
	s_add_u32 s40, s22, 0x100
	s_addc_u32 s41, s23, 0
	s_cmp_eq_u32 s82, 12
	s_cselect_b32 s58, s33, s40
	s_cselect_b32 s59, s13, s41
	s_cselect_b32 s56, s79, s80
	s_cselect_b32 s57, s15, s81
	s_add_u32 s54, s58, 0x80
	s_addc_u32 s55, s59, 0
	ds_read_b128 v[186:189], v144
	ds_read_b128 v[190:193], v144 offset:1024
	ds_read_b128 v[194:197], v144 offset:2048
	ds_read_b128 v[198:201], v144 offset:3072
	ds_read_b128 v[202:205], v144 offset:4096
	ds_read_b128 v[206:209], v144 offset:5120
	ds_read_b128 v[210:213], v144 offset:6144
	ds_read_b128 v[214:217], v144 offset:7168
	s_add_u32 s22, s22, 0x40080
	s_addc_u32 s23, s23, 0
	s_mov_b32 s83, m0
	s_mov_b32 m0, s67
	s_nop 2
	global_load_lds_dwordx4 v136, s[22:23]
	s_mov_b32 m0, s83
	s_mov_b32 s83, m0
	s_mov_b32 m0, s76
	s_nop 2
	global_load_lds_dwordx4 v138, s[22:23]
	s_mov_b32 m0, s83
	s_waitcnt vmcnt(8)
	s_waitcnt lgkmcnt(0)
	s_barrier
	s_setprio 1
	v_mfma_f32_16x16x32_bf16 v[126:129], v[148:151], v[186:189], v[126:129]
	v_mfma_f32_16x16x32_bf16 v[122:125], v[156:159], v[186:189], v[122:125]
	v_mfma_f32_16x16x32_bf16 v[110:113], v[148:151], v[194:197], v[110:113]
	v_mfma_f32_16x16x32_bf16 v[106:109], v[156:159], v[194:197], v[106:109]
	v_mfma_f32_16x16x32_bf16 v[94:97], v[148:151], v[202:205], v[94:97]
	v_mfma_f32_16x16x32_bf16 v[90:93], v[156:159], v[202:205], v[90:93]
	v_mfma_f32_16x16x32_bf16 v[78:81], v[148:151], v[210:213], v[78:81]
	v_mfma_f32_16x16x32_bf16 v[74:77], v[156:159], v[210:213], v[74:77]
	v_mfma_f32_16x16x32_bf16 v[126:129], v[152:155], v[190:193], v[126:129]
	v_mfma_f32_16x16x32_bf16 v[122:125], v[160:163], v[190:193], v[122:125]
	v_mfma_f32_16x16x32_bf16 v[110:113], v[152:155], v[198:201], v[110:113]
	v_mfma_f32_16x16x32_bf16 v[106:109], v[160:163], v[198:201], v[106:109]
	v_mfma_f32_16x16x32_bf16 v[94:97], v[152:155], v[206:209], v[94:97]
	v_mfma_f32_16x16x32_bf16 v[90:93], v[160:163], v[206:209], v[90:93]
	v_mfma_f32_16x16x32_bf16 v[78:81], v[152:155], v[214:217], v[78:81]
	v_mfma_f32_16x16x32_bf16 v[74:77], v[160:163], v[214:217], v[74:77]
	v_mfma_f32_16x16x32_bf16 v[118:121], v[164:167], v[186:189], v[118:121]
	v_mfma_f32_16x16x32_bf16 v[114:117], v[178:181], v[186:189], v[114:117]
	v_mfma_f32_16x16x32_bf16 v[102:105], v[164:167], v[194:197], v[102:105]
	v_mfma_f32_16x16x32_bf16 v[98:101], v[178:181], v[194:197], v[98:101]
	v_mfma_f32_16x16x32_bf16 v[86:89], v[164:167], v[202:205], v[86:89]
	v_mfma_f32_16x16x32_bf16 v[82:85], v[178:181], v[202:205], v[82:85]
	v_mfma_f32_16x16x32_bf16 v[70:73], v[164:167], v[210:213], v[70:73]
	v_mfma_f32_16x16x32_bf16 v[66:69], v[178:181], v[210:213], v[66:69]
	v_mfma_f32_16x16x32_bf16 v[118:121], v[174:177], v[190:193], v[118:121]
	v_mfma_f32_16x16x32_bf16 v[114:117], v[182:185], v[190:193], v[114:117]
	v_mfma_f32_16x16x32_bf16 v[102:105], v[174:177], v[198:201], v[102:105]
	v_mfma_f32_16x16x32_bf16 v[98:101], v[182:185], v[198:201], v[98:101]
	v_mfma_f32_16x16x32_bf16 v[86:89], v[174:177], v[206:209], v[86:89]
	v_mfma_f32_16x16x32_bf16 v[82:85], v[182:185], v[206:209], v[82:85]
	v_mfma_f32_16x16x32_bf16 v[70:73], v[174:177], v[214:217], v[70:73]
	v_mfma_f32_16x16x32_bf16 v[66:69], v[182:185], v[214:217], v[66:69]
	s_setprio 0
	s_barrier
	ds_read_b128 v[186:189], v144 offset:16384
	ds_read_b128 v[190:193], v144 offset:17408
	ds_read_b128 v[194:197], v144 offset:18432
	ds_read_b128 v[198:201], v144 offset:19456
	ds_read_b128 v[202:205], v144 offset:20480
	ds_read_b128 v[206:209], v144 offset:21504
	ds_read_b128 v[210:213], v144 offset:22528
	ds_read_b128 v[214:217], v144 offset:23552
	s_mov_b32 s22, m0
	s_mov_b32 m0, s30
	s_nop 2
	global_load_lds_dwordx4 v137, s[56:57]
	s_mov_b32 m0, s22
	s_mov_b32 s22, m0
	s_mov_b32 m0, s31
	s_nop 2
	global_load_lds_dwordx4 v139, s[56:57]
	s_mov_b32 m0, s22
	s_add_u32 s22, s56, 0x40000
	s_addc_u32 s23, s57, 0
	s_mov_b32 s83, m0
	s_mov_b32 m0, s34
	s_nop 2
	global_load_lds_dwordx4 v137, s[22:23]
	s_mov_b32 m0, s83
	s_mov_b32 s83, m0
	s_mov_b32 m0, s35
	s_nop 2
	global_load_lds_dwordx4 v139, s[22:23]
	s_mov_b32 m0, s83
	s_mov_b32 s22, m0
	s_mov_b32 m0, s21
	s_nop 2
	global_load_lds_dwordx4 v136, s[58:59]
	s_mov_b32 m0, s22
	s_mov_b32 s22, m0
	s_mov_b32 m0, s36
	s_nop 2
	global_load_lds_dwordx4 v138, s[58:59]
	s_mov_b32 m0, s22
	s_waitcnt vmcnt(8)
	s_waitcnt lgkmcnt(0)
	s_barrier
	s_setprio 1
	v_mfma_f32_16x16x32_bf16 v[62:65], v[148:151], v[186:189], v[62:65]
	v_mfma_f32_16x16x32_bf16 v[58:61], v[156:159], v[186:189], v[58:61]
	v_mfma_f32_16x16x32_bf16 v[46:49], v[148:151], v[194:197], v[46:49]
	v_mfma_f32_16x16x32_bf16 v[42:45], v[156:159], v[194:197], v[42:45]
	v_mfma_f32_16x16x32_bf16 v[30:33], v[148:151], v[202:205], v[30:33]
	v_mfma_f32_16x16x32_bf16 v[26:29], v[156:159], v[202:205], v[26:29]
	v_mfma_f32_16x16x32_bf16 v[14:17], v[148:151], v[210:213], v[14:17]
	v_mfma_f32_16x16x32_bf16 v[10:13], v[156:159], v[210:213], v[10:13]
	v_mfma_f32_16x16x32_bf16 v[62:65], v[152:155], v[190:193], v[62:65]
	v_mfma_f32_16x16x32_bf16 v[58:61], v[160:163], v[190:193], v[58:61]
	v_mfma_f32_16x16x32_bf16 v[46:49], v[152:155], v[198:201], v[46:49]
	v_mfma_f32_16x16x32_bf16 v[42:45], v[160:163], v[198:201], v[42:45]
	v_mfma_f32_16x16x32_bf16 v[30:33], v[152:155], v[206:209], v[30:33]
	v_mfma_f32_16x16x32_bf16 v[26:29], v[160:163], v[206:209], v[26:29]
	v_mfma_f32_16x16x32_bf16 v[14:17], v[152:155], v[214:217], v[14:17]
	v_mfma_f32_16x16x32_bf16 v[10:13], v[160:163], v[214:217], v[10:13]
	v_mfma_f32_16x16x32_bf16 v[54:57], v[164:167], v[186:189], v[54:57]
	v_mfma_f32_16x16x32_bf16 v[50:53], v[178:181], v[186:189], v[50:53]
	v_mfma_f32_16x16x32_bf16 v[38:41], v[164:167], v[194:197], v[38:41]
	v_mfma_f32_16x16x32_bf16 v[34:37], v[178:181], v[194:197], v[34:37]
	v_mfma_f32_16x16x32_bf16 v[22:25], v[164:167], v[202:205], v[22:25]
	v_mfma_f32_16x16x32_bf16 v[18:21], v[178:181], v[202:205], v[18:21]
	v_mfma_f32_16x16x32_bf16 v[6:9], v[164:167], v[210:213], v[6:9]
	v_mfma_f32_16x16x32_bf16 v[2:5], v[178:181], v[210:213], v[2:5]
	v_mfma_f32_16x16x32_bf16 v[54:57], v[174:177], v[190:193], v[54:57]
	v_mfma_f32_16x16x32_bf16 v[50:53], v[182:185], v[190:193], v[50:53]
	v_mfma_f32_16x16x32_bf16 v[38:41], v[174:177], v[198:201], v[38:41]
	v_mfma_f32_16x16x32_bf16 v[34:37], v[182:185], v[198:201], v[34:37]
	v_mfma_f32_16x16x32_bf16 v[22:25], v[174:177], v[206:209], v[22:25]
	v_mfma_f32_16x16x32_bf16 v[18:21], v[182:185], v[206:209], v[18:21]
	v_mfma_f32_16x16x32_bf16 v[6:9], v[174:177], v[214:217], v[6:9]
	v_mfma_f32_16x16x32_bf16 v[2:5], v[182:185], v[214:217], v[2:5]
	s_setprio 0
	s_barrier
	ds_read_b128 v[148:151], v145
	ds_read_b128 v[152:155], v145 offset:1024
	ds_read_b128 v[156:159], v145 offset:2048
	ds_read_b128 v[160:163], v145 offset:3072
	ds_read_b128 v[164:167], v146
	ds_read_b128 v[174:177], v146 offset:1024
	ds_read_b128 v[178:181], v146 offset:2048
	ds_read_b128 v[182:185], v146 offset:3072
	ds_read_b128 v[186:189], v144 offset:32768
	ds_read_b128 v[190:193], v144 offset:33792
	ds_read_b128 v[194:197], v144 offset:34816
	ds_read_b128 v[198:201], v144 offset:35840
	ds_read_b128 v[202:205], v144 offset:36864
	ds_read_b128 v[206:209], v144 offset:37888
	ds_read_b128 v[210:213], v144 offset:38912
	ds_read_b128 v[214:217], v144 offset:39936
	s_add_u32 s22, s58, 0x40000
	s_addc_u32 s23, s59, 0
	s_mov_b32 s58, m0
	s_mov_b32 m0, s37
	s_nop 2
	global_load_lds_dwordx4 v136, s[22:23]
	s_mov_b32 m0, s58
	s_mov_b32 s58, m0
	s_mov_b32 m0, s52
	s_nop 2
	global_load_lds_dwordx4 v138, s[22:23]
	s_mov_b32 m0, s58
	s_waitcnt vmcnt(8)
	s_waitcnt lgkmcnt(0)
	s_barrier
	s_setprio 1
	v_mfma_f32_16x16x32_bf16 v[126:129], v[148:151], v[186:189], v[126:129]
	v_mfma_f32_16x16x32_bf16 v[122:125], v[156:159], v[186:189], v[122:125]
	v_mfma_f32_16x16x32_bf16 v[110:113], v[148:151], v[194:197], v[110:113]
	v_mfma_f32_16x16x32_bf16 v[106:109], v[156:159], v[194:197], v[106:109]
	v_mfma_f32_16x16x32_bf16 v[94:97], v[148:151], v[202:205], v[94:97]
	v_mfma_f32_16x16x32_bf16 v[90:93], v[156:159], v[202:205], v[90:93]
	v_mfma_f32_16x16x32_bf16 v[78:81], v[148:151], v[210:213], v[78:81]
	v_mfma_f32_16x16x32_bf16 v[74:77], v[156:159], v[210:213], v[74:77]
	v_mfma_f32_16x16x32_bf16 v[126:129], v[152:155], v[190:193], v[126:129]
	v_mfma_f32_16x16x32_bf16 v[122:125], v[160:163], v[190:193], v[122:125]
	v_mfma_f32_16x16x32_bf16 v[110:113], v[152:155], v[198:201], v[110:113]
	v_mfma_f32_16x16x32_bf16 v[106:109], v[160:163], v[198:201], v[106:109]
	v_mfma_f32_16x16x32_bf16 v[94:97], v[152:155], v[206:209], v[94:97]
	v_mfma_f32_16x16x32_bf16 v[90:93], v[160:163], v[206:209], v[90:93]
	v_mfma_f32_16x16x32_bf16 v[78:81], v[152:155], v[214:217], v[78:81]
	v_mfma_f32_16x16x32_bf16 v[74:77], v[160:163], v[214:217], v[74:77]
	v_mfma_f32_16x16x32_bf16 v[118:121], v[164:167], v[186:189], v[118:121]
	v_mfma_f32_16x16x32_bf16 v[114:117], v[178:181], v[186:189], v[114:117]
	v_mfma_f32_16x16x32_bf16 v[102:105], v[164:167], v[194:197], v[102:105]
	v_mfma_f32_16x16x32_bf16 v[98:101], v[178:181], v[194:197], v[98:101]
	v_mfma_f32_16x16x32_bf16 v[86:89], v[164:167], v[202:205], v[86:89]
	v_mfma_f32_16x16x32_bf16 v[82:85], v[178:181], v[202:205], v[82:85]
	v_mfma_f32_16x16x32_bf16 v[70:73], v[164:167], v[210:213], v[70:73]
	v_mfma_f32_16x16x32_bf16 v[66:69], v[178:181], v[210:213], v[66:69]
	v_mfma_f32_16x16x32_bf16 v[118:121], v[174:177], v[190:193], v[118:121]
	v_mfma_f32_16x16x32_bf16 v[114:117], v[182:185], v[190:193], v[114:117]
	v_mfma_f32_16x16x32_bf16 v[102:105], v[174:177], v[198:201], v[102:105]
	v_mfma_f32_16x16x32_bf16 v[98:101], v[182:185], v[198:201], v[98:101]
	v_mfma_f32_16x16x32_bf16 v[86:89], v[174:177], v[206:209], v[86:89]
	v_mfma_f32_16x16x32_bf16 v[82:85], v[182:185], v[206:209], v[82:85]
	v_mfma_f32_16x16x32_bf16 v[70:73], v[174:177], v[214:217], v[70:73]
	v_mfma_f32_16x16x32_bf16 v[66:69], v[182:185], v[214:217], v[66:69]
	s_setprio 0
	s_barrier
	ds_read_b128 v[186:189], v144 offset:49152
	ds_read_b128 v[190:193], v144 offset:50176
	ds_read_b128 v[194:197], v144 offset:51200
	ds_read_b128 v[198:201], v144 offset:52224
	ds_read_b128 v[202:205], v144 offset:53248
	ds_read_b128 v[206:209], v144 offset:54272
	ds_read_b128 v[210:213], v144 offset:55296
	ds_read_b128 v[214:217], v144 offset:56320
	s_add_u32 s22, s56, 0x80
	s_addc_u32 s23, s57, 0
	s_mov_b32 s58, m0
	s_mov_b32 m0, s61
	s_nop 2
	global_load_lds_dwordx4 v137, s[22:23]
	s_mov_b32 m0, s58
	s_mov_b32 s58, m0
	s_mov_b32 m0, s62
	s_nop 2
	global_load_lds_dwordx4 v139, s[22:23]
	s_mov_b32 m0, s58
	s_add_u32 s22, s56, 0x40080
	s_addc_u32 s23, s57, 0
	s_mov_b32 s56, m0
	s_mov_b32 m0, s65
	s_nop 2
	global_load_lds_dwordx4 v137, s[22:23]
	s_mov_b32 m0, s56
	s_mov_b32 s56, m0
	s_mov_b32 m0, s66
	s_nop 2
	global_load_lds_dwordx4 v139, s[22:23]
	s_mov_b32 m0, s56
	s_mov_b32 s22, m0
	s_mov_b32 m0, s63
	s_nop 2
	global_load_lds_dwordx4 v136, s[54:55]
	s_mov_b32 m0, s22
	s_mov_b32 s22, m0
	s_mov_b32 m0, s64
	s_nop 2
	global_load_lds_dwordx4 v138, s[54:55]
	s_mov_b32 m0, s22
	s_waitcnt vmcnt(8)
	s_waitcnt lgkmcnt(0)
	s_barrier
	s_setprio 1
	v_mfma_f32_16x16x32_bf16 v[62:65], v[148:151], v[186:189], v[62:65]
	v_mfma_f32_16x16x32_bf16 v[58:61], v[156:159], v[186:189], v[58:61]
	v_mfma_f32_16x16x32_bf16 v[46:49], v[148:151], v[194:197], v[46:49]
	v_mfma_f32_16x16x32_bf16 v[42:45], v[156:159], v[194:197], v[42:45]
	v_mfma_f32_16x16x32_bf16 v[30:33], v[148:151], v[202:205], v[30:33]
	v_mfma_f32_16x16x32_bf16 v[26:29], v[156:159], v[202:205], v[26:29]
	v_mfma_f32_16x16x32_bf16 v[14:17], v[148:151], v[210:213], v[14:17]
	v_mfma_f32_16x16x32_bf16 v[10:13], v[156:159], v[210:213], v[10:13]
	v_mfma_f32_16x16x32_bf16 v[62:65], v[152:155], v[190:193], v[62:65]
	v_mfma_f32_16x16x32_bf16 v[58:61], v[160:163], v[190:193], v[58:61]
	v_mfma_f32_16x16x32_bf16 v[46:49], v[152:155], v[198:201], v[46:49]
	v_mfma_f32_16x16x32_bf16 v[42:45], v[160:163], v[198:201], v[42:45]
	v_mfma_f32_16x16x32_bf16 v[30:33], v[152:155], v[206:209], v[30:33]
	v_mfma_f32_16x16x32_bf16 v[26:29], v[160:163], v[206:209], v[26:29]
	v_mfma_f32_16x16x32_bf16 v[14:17], v[152:155], v[214:217], v[14:17]
	v_mfma_f32_16x16x32_bf16 v[10:13], v[160:163], v[214:217], v[10:13]
	v_mfma_f32_16x16x32_bf16 v[54:57], v[164:167], v[186:189], v[54:57]
	v_mfma_f32_16x16x32_bf16 v[50:53], v[178:181], v[186:189], v[50:53]
	v_mfma_f32_16x16x32_bf16 v[38:41], v[164:167], v[194:197], v[38:41]
	v_mfma_f32_16x16x32_bf16 v[34:37], v[178:181], v[194:197], v[34:37]
	v_mfma_f32_16x16x32_bf16 v[22:25], v[164:167], v[202:205], v[22:25]
	v_mfma_f32_16x16x32_bf16 v[18:21], v[178:181], v[202:205], v[18:21]
	v_mfma_f32_16x16x32_bf16 v[6:9], v[164:167], v[210:213], v[6:9]
	v_mfma_f32_16x16x32_bf16 v[2:5], v[178:181], v[210:213], v[2:5]
	v_mfma_f32_16x16x32_bf16 v[54:57], v[174:177], v[190:193], v[54:57]
	v_mfma_f32_16x16x32_bf16 v[50:53], v[182:185], v[190:193], v[50:53]
	v_mfma_f32_16x16x32_bf16 v[38:41], v[174:177], v[198:201], v[38:41]
	v_mfma_f32_16x16x32_bf16 v[34:37], v[182:185], v[198:201], v[34:37]
	v_mfma_f32_16x16x32_bf16 v[22:25], v[174:177], v[206:209], v[22:25]
	v_mfma_f32_16x16x32_bf16 v[18:21], v[182:185], v[206:209], v[18:21]
	v_mfma_f32_16x16x32_bf16 v[6:9], v[174:177], v[214:217], v[6:9]
	v_mfma_f32_16x16x32_bf16 v[2:5], v[182:185], v[214:217], v[2:5]
	s_setprio 0
	s_barrier
	s_add_i32 s82, s82, 2
	s_add_u32 s80, s80, 0x100
	s_addc_u32 s81, s81, 0
	s_cmp_gt_u32 s82, 13
	s_mov_b64 s[22:23], s[40:41]
	s_cbranch_scc0 .LBB0_143
	s_and_b64 vcc, exec, s[10:11]
	s_cbranch_vccz .LBB0_146
	s_barrier

.Lpeel170:
	ds_read_b128 v[142:145], v136
	ds_read_b128 v[146:149], v136 offset:1024
	ds_read_b128 v[150:153], v136 offset:2048
	ds_read_b128 v[154:157], v136 offset:3072
	ds_read_b128 v[158:161], v137
	ds_read_b128 v[162:165], v137 offset:1024
	ds_read_b128 v[166:169], v137 offset:2048
	ds_read_b128 v[174:177], v137 offset:3072
	s_add_u32 s14, s12, 0x100
	s_addc_u32 s15, s13, 0
	s_cmp_eq_u32 s56, 12
	s_cselect_b32 s20, s10, s14
	s_cselect_b32 s21, s11, s15
	s_cselect_b32 s18, s8, s54
	s_cselect_b32 s19, s9, s55
	s_add_u32 s16, s20, 0x80
	s_addc_u32 s17, s21, 0
	ds_read_b128 v[178:181], v138
	ds_read_b128 v[182:185], v138 offset:1024
	ds_read_b128 v[186:189], v138 offset:2048
	ds_read_b128 v[190:193], v138 offset:3072
	ds_read_b128 v[194:197], v138 offset:4096
	ds_read_b128 v[198:201], v138 offset:5120
	ds_read_b128 v[202:205], v138 offset:6144
	ds_read_b128 v[206:209], v138 offset:7168
	s_add_u32 s12, s12, 0x40080
	s_addc_u32 s13, s13, 0
	s_mov_b32 s57, m0
	s_mov_b32 m0, s52
	s_nop 2
	global_load_lds_dwordx4 v132, s[12:13]
	s_mov_b32 m0, s57
	s_mov_b32 s57, m0
	s_mov_b32 m0, s53
	s_nop 2
	global_load_lds_dwordx4 v134, s[12:13]
	s_mov_b32 m0, s57
	s_waitcnt vmcnt(8)
	s_waitcnt lgkmcnt(0)
	s_barrier
	s_setprio 1
	v_mfma_f32_16x16x32_bf16 v[126:129], v[142:145], v[178:181], 0
	v_mfma_f32_16x16x32_bf16 v[122:125], v[150:153], v[178:181], 0
	v_mfma_f32_16x16x32_bf16 v[110:113], v[142:145], v[186:189], 0
	v_mfma_f32_16x16x32_bf16 v[106:109], v[150:153], v[186:189], 0
	v_mfma_f32_16x16x32_bf16 v[94:97], v[142:145], v[194:197], 0
	v_mfma_f32_16x16x32_bf16 v[90:93], v[150:153], v[194:197], 0
	v_mfma_f32_16x16x32_bf16 v[78:81], v[142:145], v[202:205], 0
	v_mfma_f32_16x16x32_bf16 v[74:77], v[150:153], v[202:205], 0
	v_mfma_f32_16x16x32_bf16 v[126:129], v[146:149], v[182:185], v[126:129]
	v_mfma_f32_16x16x32_bf16 v[122:125], v[154:157], v[182:185], v[122:125]
	v_mfma_f32_16x16x32_bf16 v[110:113], v[146:149], v[190:193], v[110:113]
	v_mfma_f32_16x16x32_bf16 v[106:109], v[154:157], v[190:193], v[106:109]
	v_mfma_f32_16x16x32_bf16 v[94:97], v[146:149], v[198:201], v[94:97]
	v_mfma_f32_16x16x32_bf16 v[90:93], v[154:157], v[198:201], v[90:93]
	v_mfma_f32_16x16x32_bf16 v[78:81], v[146:149], v[206:209], v[78:81]
	v_mfma_f32_16x16x32_bf16 v[74:77], v[154:157], v[206:209], v[74:77]
	v_mfma_f32_16x16x32_bf16 v[118:121], v[158:161], v[178:181], 0
	v_mfma_f32_16x16x32_bf16 v[114:117], v[166:169], v[178:181], 0
	v_mfma_f32_16x16x32_bf16 v[102:105], v[158:161], v[186:189], 0
	v_mfma_f32_16x16x32_bf16 v[98:101], v[166:169], v[186:189], 0
	v_mfma_f32_16x16x32_bf16 v[86:89], v[158:161], v[194:197], 0
	v_mfma_f32_16x16x32_bf16 v[82:85], v[166:169], v[194:197], 0
	v_mfma_f32_16x16x32_bf16 v[70:73], v[158:161], v[202:205], 0
	v_mfma_f32_16x16x32_bf16 v[66:69], v[166:169], v[202:205], 0
	v_mfma_f32_16x16x32_bf16 v[118:121], v[162:165], v[182:185], v[118:121]
	v_mfma_f32_16x16x32_bf16 v[114:117], v[174:177], v[182:185], v[114:117]
	v_mfma_f32_16x16x32_bf16 v[102:105], v[162:165], v[190:193], v[102:105]
	v_mfma_f32_16x16x32_bf16 v[98:101], v[174:177], v[190:193], v[98:101]
	v_mfma_f32_16x16x32_bf16 v[86:89], v[162:165], v[198:201], v[86:89]
	v_mfma_f32_16x16x32_bf16 v[82:85], v[174:177], v[198:201], v[82:85]
	v_mfma_f32_16x16x32_bf16 v[70:73], v[162:165], v[206:209], v[70:73]
	v_mfma_f32_16x16x32_bf16 v[66:69], v[174:177], v[206:209], v[66:69]
	s_setprio 0
	s_barrier
	ds_read_b128 v[178:181], v138 offset:16384
	ds_read_b128 v[182:185], v138 offset:17408
	ds_read_b128 v[186:189], v138 offset:18432
	ds_read_b128 v[190:193], v138 offset:19456
	ds_read_b128 v[194:197], v138 offset:20480
	ds_read_b128 v[198:201], v138 offset:21504
	ds_read_b128 v[202:205], v138 offset:22528
	ds_read_b128 v[206:209], v138 offset:23552
	s_mov_b32 s12, m0
	s_mov_b32 m0, s24
	s_nop 2
	global_load_lds_dwordx4 v133, s[18:19]
	s_mov_b32 m0, s12
	s_mov_b32 s12, m0
	s_mov_b32 m0, s25
	s_nop 2
	global_load_lds_dwordx4 v135, s[18:19]
	s_mov_b32 m0, s12
	s_add_u32 s12, s18, 0x40000
	s_addc_u32 s13, s19, 0
	s_mov_b32 s57, m0
	s_mov_b32 m0, s28
	s_nop 2
	global_load_lds_dwordx4 v133, s[12:13]
	s_mov_b32 m0, s57
	s_mov_b32 s57, m0
	s_mov_b32 m0, s29
	s_nop 2
	global_load_lds_dwordx4 v135, s[12:13]
	s_mov_b32 m0, s57
	s_mov_b32 s12, m0
	s_mov_b32 m0, s5
	s_nop 2
	global_load_lds_dwordx4 v132, s[20:21]
	s_mov_b32 m0, s12
	s_mov_b32 s12, m0
	s_mov_b32 m0, s30
	s_nop 2
	global_load_lds_dwordx4 v134, s[20:21]
	s_mov_b32 m0, s12
	s_waitcnt vmcnt(8)
	s_waitcnt lgkmcnt(0)
	s_barrier
	s_setprio 1
	v_mfma_f32_16x16x32_bf16 v[62:65], v[142:145], v[178:181], 0
	v_mfma_f32_16x16x32_bf16 v[58:61], v[150:153], v[178:181], 0
	v_mfma_f32_16x16x32_bf16 v[46:49], v[142:145], v[186:189], 0
	v_mfma_f32_16x16x32_bf16 v[42:45], v[150:153], v[186:189], 0
	v_mfma_f32_16x16x32_bf16 v[30:33], v[142:145], v[194:197], 0
	v_mfma_f32_16x16x32_bf16 v[26:29], v[150:153], v[194:197], 0
	v_mfma_f32_16x16x32_bf16 v[14:17], v[142:145], v[202:205], 0
	v_mfma_f32_16x16x32_bf16 v[10:13], v[150:153], v[202:205], 0
	v_mfma_f32_16x16x32_bf16 v[62:65], v[146:149], v[182:185], v[62:65]
	v_mfma_f32_16x16x32_bf16 v[58:61], v[154:157], v[182:185], v[58:61]
	v_mfma_f32_16x16x32_bf16 v[46:49], v[146:149], v[190:193], v[46:49]
	v_mfma_f32_16x16x32_bf16 v[42:45], v[154:157], v[190:193], v[42:45]
	v_mfma_f32_16x16x32_bf16 v[30:33], v[146:149], v[198:201], v[30:33]
	v_mfma_f32_16x16x32_bf16 v[26:29], v[154:157], v[198:201], v[26:29]
	v_mfma_f32_16x16x32_bf16 v[14:17], v[146:149], v[206:209], v[14:17]
	v_mfma_f32_16x16x32_bf16 v[10:13], v[154:157], v[206:209], v[10:13]
	v_mfma_f32_16x16x32_bf16 v[54:57], v[158:161], v[178:181], 0
	v_mfma_f32_16x16x32_bf16 v[50:53], v[166:169], v[178:181], 0
	v_mfma_f32_16x16x32_bf16 v[38:41], v[158:161], v[186:189], 0
	v_mfma_f32_16x16x32_bf16 v[34:37], v[166:169], v[186:189], 0
	v_mfma_f32_16x16x32_bf16 v[22:25], v[158:161], v[194:197], 0
	v_mfma_f32_16x16x32_bf16 v[18:21], v[166:169], v[194:197], 0
	v_mfma_f32_16x16x32_bf16 v[6:9], v[158:161], v[202:205], 0
	v_mfma_f32_16x16x32_bf16 v[2:5], v[166:169], v[202:205], 0
	v_mfma_f32_16x16x32_bf16 v[54:57], v[162:165], v[182:185], v[54:57]
	v_mfma_f32_16x16x32_bf16 v[50:53], v[174:177], v[182:185], v[50:53]
	v_mfma_f32_16x16x32_bf16 v[38:41], v[162:165], v[190:193], v[38:41]
	v_mfma_f32_16x16x32_bf16 v[34:37], v[174:177], v[190:193], v[34:37]
	v_mfma_f32_16x16x32_bf16 v[22:25], v[162:165], v[198:201], v[22:25]
	v_mfma_f32_16x16x32_bf16 v[18:21], v[174:177], v[198:201], v[18:21]
	v_mfma_f32_16x16x32_bf16 v[6:9], v[162:165], v[206:209], v[6:9]
	v_mfma_f32_16x16x32_bf16 v[2:5], v[174:177], v[206:209], v[2:5]
	s_setprio 0
	s_barrier
	s_branch .Lmid170
.LBB0_170:
	ds_read_b128 v[142:145], v136
	ds_read_b128 v[146:149], v136 offset:1024
	ds_read_b128 v[150:153], v136 offset:2048
	ds_read_b128 v[154:157], v136 offset:3072
	ds_read_b128 v[158:161], v137
	ds_read_b128 v[162:165], v137 offset:1024
	ds_read_b128 v[166:169], v137 offset:2048
	ds_read_b128 v[174:177], v137 offset:3072
	s_add_u32 s14, s12, 0x100
	s_addc_u32 s15, s13, 0
	s_cmp_eq_u32 s56, 12
	s_cselect_b32 s20, s10, s14
	s_cselect_b32 s21, s11, s15
	s_cselect_b32 s18, s8, s54
	s_cselect_b32 s19, s9, s55
	s_add_u32 s16, s20, 0x80
	s_addc_u32 s17, s21, 0
	ds_read_b128 v[178:181], v138
	ds_read_b128 v[182:185], v138 offset:1024
	ds_read_b128 v[186:189], v138 offset:2048
	ds_read_b128 v[190:193], v138 offset:3072
	ds_read_b128 v[194:197], v138 offset:4096
	ds_read_b128 v[198:201], v138 offset:5120
	ds_read_b128 v[202:205], v138 offset:6144
	ds_read_b128 v[206:209], v138 offset:7168
	s_add_u32 s12, s12, 0x40080
	s_addc_u32 s13, s13, 0
	s_mov_b32 s57, m0
	s_mov_b32 m0, s52
	s_nop 2
	global_load_lds_dwordx4 v132, s[12:13]
	s_mov_b32 m0, s57
	s_mov_b32 s57, m0
	s_mov_b32 m0, s53
	s_nop 2
	global_load_lds_dwordx4 v134, s[12:13]
	s_mov_b32 m0, s57
	s_waitcnt vmcnt(8)
	s_waitcnt lgkmcnt(0)
	s_barrier
	s_setprio 1
	v_mfma_f32_16x16x32_bf16 v[126:129], v[142:145], v[178:181], v[126:129]
	v_mfma_f32_16x16x32_bf16 v[122:125], v[150:153], v[178:181], v[122:125]
	v_mfma_f32_16x16x32_bf16 v[110:113], v[142:145], v[186:189], v[110:113]
	v_mfma_f32_16x16x32_bf16 v[106:109], v[150:153], v[186:189], v[106:109]
	v_mfma_f32_16x16x32_bf16 v[94:97], v[142:145], v[194:197], v[94:97]
	v_mfma_f32_16x16x32_bf16 v[90:93], v[150:153], v[194:197], v[90:93]
	v_mfma_f32_16x16x32_bf16 v[78:81], v[142:145], v[202:205], v[78:81]
	v_mfma_f32_16x16x32_bf16 v[74:77], v[150:153], v[202:205], v[74:77]
	v_mfma_f32_16x16x32_bf16 v[126:129], v[146:149], v[182:185], v[126:129]
	v_mfma_f32_16x16x32_bf16 v[122:125], v[154:157], v[182:185], v[122:125]
	v_mfma_f32_16x16x32_bf16 v[110:113], v[146:149], v[190:193], v[110:113]
	v_mfma_f32_16x16x32_bf16 v[106:109], v[154:157], v[190:193], v[106:109]
	v_mfma_f32_16x16x32_bf16 v[94:97], v[146:149], v[198:201], v[94:97]
	v_mfma_f32_16x16x32_bf16 v[90:93], v[154:157], v[198:201], v[90:93]
	v_mfma_f32_16x16x32_bf16 v[78:81], v[146:149], v[206:209], v[78:81]
	v_mfma_f32_16x16x32_bf16 v[74:77], v[154:157], v[206:209], v[74:77]
	v_mfma_f32_16x16x32_bf16 v[118:121], v[158:161], v[178:181], v[118:121]
	v_mfma_f32_16x16x32_bf16 v[114:117], v[166:169], v[178:181], v[114:117]
	v_mfma_f32_16x16x32_bf16 v[102:105], v[158:161], v[186:189], v[102:105]
	v_mfma_f32_16x16x32_bf16 v[98:101], v[166:169], v[186:189], v[98:101]
	v_mfma_f32_16x16x32_bf16 v[86:89], v[158:161], v[194:197], v[86:89]
	v_mfma_f32_16x16x32_bf16 v[82:85], v[166:169], v[194:197], v[82:85]
	v_mfma_f32_16x16x32_bf16 v[70:73], v[158:161], v[202:205], v[70:73]
	v_mfma_f32_16x16x32_bf16 v[66:69], v[166:169], v[202:205], v[66:69]
	v_mfma_f32_16x16x32_bf16 v[118:121], v[162:165], v[182:185], v[118:121]
	v_mfma_f32_16x16x32_bf16 v[114:117], v[174:177], v[182:185], v[114:117]
	v_mfma_f32_16x16x32_bf16 v[102:105], v[162:165], v[190:193], v[102:105]
	v_mfma_f32_16x16x32_bf16 v[98:101], v[174:177], v[190:193], v[98:101]
	v_mfma_f32_16x16x32_bf16 v[86:89], v[162:165], v[198:201], v[86:89]
	v_mfma_f32_16x16x32_bf16 v[82:85], v[174:177], v[198:201], v[82:85]
	v_mfma_f32_16x16x32_bf16 v[70:73], v[162:165], v[206:209], v[70:73]
	v_mfma_f32_16x16x32_bf16 v[66:69], v[174:177], v[206:209], v[66:69]
	s_setprio 0
	s_barrier
	ds_read_b128 v[178:181], v138 offset:16384
	ds_read_b128 v[182:185], v138 offset:17408
	ds_read_b128 v[186:189], v138 offset:18432
	ds_read_b128 v[190:193], v138 offset:19456
	ds_read_b128 v[194:197], v138 offset:20480
	ds_read_b128 v[198:201], v138 offset:21504
	ds_read_b128 v[202:205], v138 offset:22528
	ds_read_b128 v[206:209], v138 offset:23552
	s_mov_b32 s12, m0
	s_mov_b32 m0, s24
	s_nop 2
	global_load_lds_dwordx4 v133, s[18:19]
	s_mov_b32 m0, s12
	s_mov_b32 s12, m0
	s_mov_b32 m0, s25
	s_nop 2
	global_load_lds_dwordx4 v135, s[18:19]
	s_mov_b32 m0, s12
	s_add_u32 s12, s18, 0x40000
	s_addc_u32 s13, s19, 0
	s_mov_b32 s57, m0
	s_mov_b32 m0, s28
	s_nop 2
	global_load_lds_dwordx4 v133, s[12:13]
	s_mov_b32 m0, s57
	s_mov_b32 s57, m0
	s_mov_b32 m0, s29
	s_nop 2
	global_load_lds_dwordx4 v135, s[12:13]
	s_mov_b32 m0, s57
	s_mov_b32 s12, m0
	s_mov_b32 m0, s5
	s_nop 2
	global_load_lds_dwordx4 v132, s[20:21]
	s_mov_b32 m0, s12
	s_mov_b32 s12, m0
	s_mov_b32 m0, s30
	s_nop 2
	global_load_lds_dwordx4 v134, s[20:21]
	s_mov_b32 m0, s12
	s_waitcnt vmcnt(8)
	s_waitcnt lgkmcnt(0)
	s_barrier
	s_setprio 1
	v_mfma_f32_16x16x32_bf16 v[62:65], v[142:145], v[178:181], v[62:65]
	v_mfma_f32_16x16x32_bf16 v[58:61], v[150:153], v[178:181], v[58:61]
	v_mfma_f32_16x16x32_bf16 v[46:49], v[142:145], v[186:189], v[46:49]
	v_mfma_f32_16x16x32_bf16 v[42:45], v[150:153], v[186:189], v[42:45]
	v_mfma_f32_16x16x32_bf16 v[30:33], v[142:145], v[194:197], v[30:33]
	v_mfma_f32_16x16x32_bf16 v[26:29], v[150:153], v[194:197], v[26:29]
	v_mfma_f32_16x16x32_bf16 v[14:17], v[142:145], v[202:205], v[14:17]
	v_mfma_f32_16x16x32_bf16 v[10:13], v[150:153], v[202:205], v[10:13]
	v_mfma_f32_16x16x32_bf16 v[62:65], v[146:149], v[182:185], v[62:65]
	v_mfma_f32_16x16x32_bf16 v[58:61], v[154:157], v[182:185], v[58:61]
	v_mfma_f32_16x16x32_bf16 v[46:49], v[146:149], v[190:193], v[46:49]
	v_mfma_f32_16x16x32_bf16 v[42:45], v[154:157], v[190:193], v[42:45]
	v_mfma_f32_16x16x32_bf16 v[30:33], v[146:149], v[198:201], v[30:33]
	v_mfma_f32_16x16x32_bf16 v[26:29], v[154:157], v[198:201], v[26:29]
	v_mfma_f32_16x16x32_bf16 v[14:17], v[146:149], v[206:209], v[14:17]
	v_mfma_f32_16x16x32_bf16 v[10:13], v[154:157], v[206:209], v[10:13]
	v_mfma_f32_16x16x32_bf16 v[54:57], v[158:161], v[178:181], v[54:57]
	v_mfma_f32_16x16x32_bf16 v[50:53], v[166:169], v[178:181], v[50:53]
	v_mfma_f32_16x16x32_bf16 v[38:41], v[158:161], v[186:189], v[38:41]
	v_mfma_f32_16x16x32_bf16 v[34:37], v[166:169], v[186:189], v[34:37]
	v_mfma_f32_16x16x32_bf16 v[22:25], v[158:161], v[194:197], v[22:25]
	v_mfma_f32_16x16x32_bf16 v[18:21], v[166:169], v[194:197], v[18:21]
	v_mfma_f32_16x16x32_bf16 v[6:9], v[158:161], v[202:205], v[6:9]
	v_mfma_f32_16x16x32_bf16 v[2:5], v[166:169], v[202:205], v[2:5]
	v_mfma_f32_16x16x32_bf16 v[54:57], v[162:165], v[182:185], v[54:57]
	v_mfma_f32_16x16x32_bf16 v[50:53], v[174:177], v[182:185], v[50:53]
	v_mfma_f32_16x16x32_bf16 v[38:41], v[162:165], v[190:193], v[38:41]
	v_mfma_f32_16x16x32_bf16 v[34:37], v[174:177], v[190:193], v[34:37]
	v_mfma_f32_16x16x32_bf16 v[22:25], v[162:165], v[198:201], v[22:25]
	v_mfma_f32_16x16x32_bf16 v[18:21], v[174:177], v[198:201], v[18:21]
	v_mfma_f32_16x16x32_bf16 v[6:9], v[162:165], v[206:209], v[6:9]
	v_mfma_f32_16x16x32_bf16 v[2:5], v[174:177], v[206:209], v[2:5]
	s_setprio 0
	s_barrier
.Lmid170:
	ds_read_b128 v[142:145], v139
	ds_read_b128 v[146:149], v139 offset:1024
	ds_read_b128 v[150:153], v139 offset:2048
	ds_read_b128 v[154:157], v139 offset:3072
	ds_read_b128 v[158:161], v140
	ds_read_b128 v[162:165], v140 offset:1024
	ds_read_b128 v[166:169], v140 offset:2048
	ds_read_b128 v[174:177], v140 offset:3072
	ds_read_b128 v[178:181], v138 offset:32768
	ds_read_b128 v[182:185], v138 offset:33792
	ds_read_b128 v[186:189], v138 offset:34816
	ds_read_b128 v[190:193], v138 offset:35840
	ds_read_b128 v[194:197], v138 offset:36864
	ds_read_b128 v[198:201], v138 offset:37888
	ds_read_b128 v[202:205], v138 offset:38912
	ds_read_b128 v[206:209], v138 offset:39936
	s_add_u32 s12, s20, 0x40000
	s_addc_u32 s13, s21, 0
	s_mov_b32 s20, m0
	s_mov_b32 m0, s31
	s_nop 2
	global_load_lds_dwordx4 v132, s[12:13]
	s_mov_b32 m0, s20
	s_mov_b32 s20, m0
	s_mov_b32 m0, s33
	s_nop 2
	global_load_lds_dwordx4 v134, s[12:13]
	s_mov_b32 m0, s20
	s_waitcnt vmcnt(8)
	s_waitcnt lgkmcnt(0)
	s_barrier
	s_setprio 1
	v_mfma_f32_16x16x32_bf16 v[126:129], v[142:145], v[178:181], v[126:129]
	v_mfma_f32_16x16x32_bf16 v[122:125], v[150:153], v[178:181], v[122:125]
	v_mfma_f32_16x16x32_bf16 v[110:113], v[142:145], v[186:189], v[110:113]
	v_mfma_f32_16x16x32_bf16 v[106:109], v[150:153], v[186:189], v[106:109]
	v_mfma_f32_16x16x32_bf16 v[94:97], v[142:145], v[194:197], v[94:97]
	v_mfma_f32_16x16x32_bf16 v[90:93], v[150:153], v[194:197], v[90:93]
	v_mfma_f32_16x16x32_bf16 v[78:81], v[142:145], v[202:205], v[78:81]
	v_mfma_f32_16x16x32_bf16 v[74:77], v[150:153], v[202:205], v[74:77]
	v_mfma_f32_16x16x32_bf16 v[126:129], v[146:149], v[182:185], v[126:129]
	v_mfma_f32_16x16x32_bf16 v[122:125], v[154:157], v[182:185], v[122:125]
	v_mfma_f32_16x16x32_bf16 v[110:113], v[146:149], v[190:193], v[110:113]
	v_mfma_f32_16x16x32_bf16 v[106:109], v[154:157], v[190:193], v[106:109]
	v_mfma_f32_16x16x32_bf16 v[94:97], v[146:149], v[198:201], v[94:97]
	v_mfma_f32_16x16x32_bf16 v[90:93], v[154:157], v[198:201], v[90:93]
	v_mfma_f32_16x16x32_bf16 v[78:81], v[146:149], v[206:209], v[78:81]
	v_mfma_f32_16x16x32_bf16 v[74:77], v[154:157], v[206:209], v[74:77]
	v_mfma_f32_16x16x32_bf16 v[118:121], v[158:161], v[178:181], v[118:121]
	v_mfma_f32_16x16x32_bf16 v[114:117], v[166:169], v[178:181], v[114:117]
	v_mfma_f32_16x16x32_bf16 v[102:105], v[158:161], v[186:189], v[102:105]
	v_mfma_f32_16x16x32_bf16 v[98:101], v[166:169], v[186:189], v[98:101]
	v_mfma_f32_16x16x32_bf16 v[86:89], v[158:161], v[194:197], v[86:89]
	v_mfma_f32_16x16x32_bf16 v[82:85], v[166:169], v[194:197], v[82:85]
	v_mfma_f32_16x16x32_bf16 v[70:73], v[158:161], v[202:205], v[70:73]
	v_mfma_f32_16x16x32_bf16 v[66:69], v[166:169], v[202:205], v[66:69]
	v_mfma_f32_16x16x32_bf16 v[118:121], v[162:165], v[182:185], v[118:121]
	v_mfma_f32_16x16x32_bf16 v[114:117], v[174:177], v[182:185], v[114:117]
	v_mfma_f32_16x16x32_bf16 v[102:105], v[162:165], v[190:193], v[102:105]
	v_mfma_f32_16x16x32_bf16 v[98:101], v[174:177], v[190:193], v[98:101]
	v_mfma_f32_16x16x32_bf16 v[86:89], v[162:165], v[198:201], v[86:89]
	v_mfma_f32_16x16x32_bf16 v[82:85], v[174:177], v[198:201], v[82:85]
	v_mfma_f32_16x16x32_bf16 v[70:73], v[162:165], v[206:209], v[70:73]
	v_mfma_f32_16x16x32_bf16 v[66:69], v[174:177], v[206:209], v[66:69]
	s_setprio 0
	s_barrier
	ds_read_b128 v[178:181], v138 offset:49152
	ds_read_b128 v[182:185], v138 offset:50176
	ds_read_b128 v[186:189], v138 offset:51200
	ds_read_b128 v[190:193], v138 offset:52224
	ds_read_b128 v[194:197], v138 offset:53248
	ds_read_b128 v[198:201], v138 offset:54272
	ds_read_b128 v[202:205], v138 offset:55296
	ds_read_b128 v[206:209], v138 offset:56320
	s_add_u32 s12, s18, 0x80
	s_addc_u32 s13, s19, 0
	s_mov_b32 s20, m0
	s_mov_b32 m0, s34
	s_nop 2
	global_load_lds_dwordx4 v133, s[12:13]
	s_mov_b32 m0, s20
	s_mov_b32 s20, m0
	s_mov_b32 m0, s35
	s_nop 2
	global_load_lds_dwordx4 v135, s[12:13]
	s_mov_b32 m0, s20
	s_add_u32 s12, s18, 0x40080
	s_addc_u32 s13, s19, 0
	s_mov_b32 s18, m0
	s_mov_b32 m0, s40
	s_nop 2
	global_load_lds_dwordx4 v133, s[12:13]
	s_mov_b32 m0, s18
	s_mov_b32 s18, m0
	s_mov_b32 m0, s41
	s_nop 2
	global_load_lds_dwordx4 v135, s[12:13]
	s_mov_b32 m0, s18
	s_mov_b32 s12, m0
	s_mov_b32 m0, s36
	s_nop 2
	global_load_lds_dwordx4 v132, s[16:17]
	s_mov_b32 m0, s12
	s_mov_b32 s12, m0
	s_mov_b32 m0, s37
	s_nop 2
	global_load_lds_dwordx4 v134, s[16:17]
	s_mov_b32 m0, s12
	s_waitcnt vmcnt(8)
	s_waitcnt lgkmcnt(0)
	s_barrier
	s_setprio 1
	v_mfma_f32_16x16x32_bf16 v[62:65], v[142:145], v[178:181], v[62:65]
	v_mfma_f32_16x16x32_bf16 v[58:61], v[150:153], v[178:181], v[58:61]
	v_mfma_f32_16x16x32_bf16 v[46:49], v[142:145], v[186:189], v[46:49]
	v_mfma_f32_16x16x32_bf16 v[42:45], v[150:153], v[186:189], v[42:45]
	v_mfma_f32_16x16x32_bf16 v[30:33], v[142:145], v[194:197], v[30:33]
	v_mfma_f32_16x16x32_bf16 v[26:29], v[150:153], v[194:197], v[26:29]
	v_mfma_f32_16x16x32_bf16 v[14:17], v[142:145], v[202:205], v[14:17]
	v_mfma_f32_16x16x32_bf16 v[10:13], v[150:153], v[202:205], v[10:13]
	v_mfma_f32_16x16x32_bf16 v[62:65], v[146:149], v[182:185], v[62:65]
	v_mfma_f32_16x16x32_bf16 v[58:61], v[154:157], v[182:185], v[58:61]
	v_mfma_f32_16x16x32_bf16 v[46:49], v[146:149], v[190:193], v[46:49]
	v_mfma_f32_16x16x32_bf16 v[42:45], v[154:157], v[190:193], v[42:45]
	v_mfma_f32_16x16x32_bf16 v[30:33], v[146:149], v[198:201], v[30:33]
	v_mfma_f32_16x16x32_bf16 v[26:29], v[154:157], v[198:201], v[26:29]
	v_mfma_f32_16x16x32_bf16 v[14:17], v[146:149], v[206:209], v[14:17]
	v_mfma_f32_16x16x32_bf16 v[10:13], v[154:157], v[206:209], v[10:13]
	v_mfma_f32_16x16x32_bf16 v[54:57], v[158:161], v[178:181], v[54:57]
	v_mfma_f32_16x16x32_bf16 v[50:53], v[166:169], v[178:181], v[50:53]
	v_mfma_f32_16x16x32_bf16 v[38:41], v[158:161], v[186:189], v[38:41]
	v_mfma_f32_16x16x32_bf16 v[34:37], v[166:169], v[186:189], v[34:37]
	v_mfma_f32_16x16x32_bf16 v[22:25], v[158:161], v[194:197], v[22:25]
	v_mfma_f32_16x16x32_bf16 v[18:21], v[166:169], v[194:197], v[18:21]
	v_mfma_f32_16x16x32_bf16 v[6:9], v[158:161], v[202:205], v[6:9]
	v_mfma_f32_16x16x32_bf16 v[2:5], v[166:169], v[202:205], v[2:5]
	v_mfma_f32_16x16x32_bf16 v[54:57], v[162:165], v[182:185], v[54:57]
	v_mfma_f32_16x16x32_bf16 v[50:53], v[174:177], v[182:185], v[50:53]
	v_mfma_f32_16x16x32_bf16 v[38:41], v[162:165], v[190:193], v[38:41]
	v_mfma_f32_16x16x32_bf16 v[34:37], v[174:177], v[190:193], v[34:37]
	v_mfma_f32_16x16x32_bf16 v[22:25], v[162:165], v[198:201], v[22:25]
	v_mfma_f32_16x16x32_bf16 v[18:21], v[174:177], v[198:201], v[18:21]
	v_mfma_f32_16x16x32_bf16 v[6:9], v[162:165], v[206:209], v[6:9]
	v_mfma_f32_16x16x32_bf16 v[2:5], v[174:177], v[206:209], v[2:5]
	s_setprio 0
	s_barrier
	s_add_i32 s56, s56, 2
	s_add_u32 s54, s54, 0x100
	s_addc_u32 s55, s55, 0
	s_cmp_gt_u32 s56, 13
	s_mov_b64 s[12:13], s[14:15]
	s_cbranch_scc0 .LBB0_170
	s_cmpk_lt_u32 s23, 0x100
	s_cbranch_scc0 .LBB0_173
	s_barrier

.LBB0_190:
	ds_read_b128 v[18:21], v174
	ds_read_b128 v[22:25], v174 offset:1024
	ds_read_b128 v[26:29], v174 offset:2048
	ds_read_b128 v[30:33], v174 offset:3072
	ds_read_b128 v[2:5], v175
	ds_read_b128 v[6:9], v175 offset:1024
	ds_read_b128 v[10:13], v175 offset:2048
	ds_read_b128 v[14:17], v175 offset:3072
	s_add_u32 s76, s78, 0x100
	s_addc_u32 s77, s79, 0
	s_cmp_eq_u32 s33, 4
	s_cselect_b32 s84, s59, s76
	s_cselect_b32 s85, s7, s77
	s_cselect_b32 s82, s67, vcc_lo
	s_cselect_b32 s83, s57, vcc_hi
	s_add_u32 s80, s84, 0x80
	s_addc_u32 s81, s85, 0
	ds_read_b128 v[180:183], v176
	ds_read_b128 v[184:187], v176 offset:1024
	ds_read_b128 v[188:191], v176 offset:2048
	ds_read_b128 v[192:195], v176 offset:3072
	ds_read_b128 v[196:199], v176 offset:4096
	ds_read_b128 v[200:203], v176 offset:5120
	ds_read_b128 v[204:207], v176 offset:6144
	ds_read_b128 v[208:211], v176 offset:7168
	s_add_u32 s78, s78, 0x20080
	s_addc_u32 s79, s79, 0
	s_mov_b32 s88, m0
	s_mov_b32 m0, s96
	s_nop 2
	global_load_lds_dwordx4 v166, s[78:79]
	s_mov_b32 m0, s88
	s_mov_b32 s88, m0
	s_mov_b32 m0, s92
	s_nop 2
	global_load_lds_dwordx4 v168, s[78:79]
	s_mov_b32 m0, s88
	s_waitcnt vmcnt(8)
	s_waitcnt lgkmcnt(0)
	s_barrier
	s_setprio 1
	v_mfma_f32_16x16x128_f8f6f4 v[158:161], v[18:25], v[180:187], v[158:161]
	v_mfma_f32_16x16x128_f8f6f4 v[154:157], v[26:33], v[180:187], v[154:157]
	v_mfma_f32_16x16x128_f8f6f4 v[146:149], v[18:25], v[188:195], v[146:149]
	v_mfma_f32_16x16x128_f8f6f4 v[138:141], v[26:33], v[188:195], v[138:141]
	v_mfma_f32_16x16x128_f8f6f4 v[130:133], v[18:25], v[196:203], v[130:133]
	v_mfma_f32_16x16x128_f8f6f4 v[122:125], v[26:33], v[196:203], v[122:125]
	v_mfma_f32_16x16x128_f8f6f4 v[114:117], v[18:25], v[204:211], v[114:117]
	v_mfma_f32_16x16x128_f8f6f4 v[106:109], v[26:33], v[204:211], v[106:109]
	v_mfma_f32_16x16x128_f8f6f4 v[150:153], v[2:9], v[180:187], v[150:153]
	v_mfma_f32_16x16x128_f8f6f4 v[142:145], v[10:17], v[180:187], v[142:145]
	v_mfma_f32_16x16x128_f8f6f4 v[134:137], v[2:9], v[188:195], v[134:137]
	v_mfma_f32_16x16x128_f8f6f4 v[126:129], v[10:17], v[188:195], v[126:129]
	v_mfma_f32_16x16x128_f8f6f4 v[118:121], v[2:9], v[196:203], v[118:121]
	v_mfma_f32_16x16x128_f8f6f4 v[110:113], v[10:17], v[196:203], v[110:113]
	v_mfma_f32_16x16x128_f8f6f4 v[102:105], v[2:9], v[204:211], v[102:105]
	v_mfma_f32_16x16x128_f8f6f4 v[98:101], v[10:17], v[204:211], v[98:101]
	s_setprio 0
	s_barrier
	ds_read_b128 v[180:183], v176 offset:16384
	ds_read_b128 v[184:187], v176 offset:17408
	ds_read_b128 v[188:191], v176 offset:18432
	ds_read_b128 v[192:195], v176 offset:19456
	ds_read_b128 v[196:199], v176 offset:20480
	ds_read_b128 v[200:203], v176 offset:21504
	ds_read_b128 v[204:207], v176 offset:22528
	ds_read_b128 v[208:211], v176 offset:23552
	s_mov_b32 s78, m0
	s_mov_b32 m0, s36
	s_nop 2
	global_load_lds_dwordx4 v167, s[82:83]
	s_mov_b32 m0, s78
	s_mov_b32 s78, m0
	s_mov_b32 m0, s37
	s_nop 2
	global_load_lds_dwordx4 v169, s[82:83]
	s_mov_b32 m0, s78
	s_add_u32 s78, s82, 0x20000
	s_addc_u32 s79, s83, 0
	s_mov_b32 s88, m0
	s_mov_b32 m0, s55
	s_nop 2
	global_load_lds_dwordx4 v167, s[78:79]
	s_mov_b32 m0, s88
	s_mov_b32 s88, m0
	s_mov_b32 m0, s86
	s_nop 2
	global_load_lds_dwordx4 v169, s[78:79]
	s_mov_b32 m0, s88
	s_mov_b32 s78, m0
	s_mov_b32 m0, s35
	s_nop 2
	global_load_lds_dwordx4 v166, s[84:85]
	s_mov_b32 m0, s78
	s_mov_b32 s78, m0
	s_mov_b32 m0, s87
	s_nop 2
	global_load_lds_dwordx4 v168, s[84:85]
	s_mov_b32 m0, s78
	s_waitcnt vmcnt(8)
	s_waitcnt lgkmcnt(0)
	s_barrier
	s_setprio 1
	v_mfma_f32_16x16x128_f8f6f4 v[94:97], v[18:25], v[180:187], v[94:97]
	v_mfma_f32_16x16x128_f8f6f4 v[90:93], v[26:33], v[180:187], v[90:93]
	v_mfma_f32_16x16x128_f8f6f4 v[82:85], v[18:25], v[188:195], v[82:85]
	v_mfma_f32_16x16x128_f8f6f4 v[74:77], v[26:33], v[188:195], v[74:77]
	v_mfma_f32_16x16x128_f8f6f4 v[66:69], v[18:25], v[196:203], v[66:69]
	v_mfma_f32_16x16x128_f8f6f4 v[58:61], v[26:33], v[196:203], v[58:61]
	v_mfma_f32_16x16x128_f8f6f4 v[50:53], v[18:25], v[204:211], v[50:53]
	v_mfma_f32_16x16x128_f8f6f4 v[42:45], v[26:33], v[204:211], v[42:45]
	v_mfma_f32_16x16x128_f8f6f4 v[86:89], v[2:9], v[180:187], v[86:89]
	v_mfma_f32_16x16x128_f8f6f4 v[78:81], v[10:17], v[180:187], v[78:81]
	v_mfma_f32_16x16x128_f8f6f4 v[70:73], v[2:9], v[188:195], v[70:73]
	v_mfma_f32_16x16x128_f8f6f4 v[62:65], v[10:17], v[188:195], v[62:65]
	v_mfma_f32_16x16x128_f8f6f4 v[54:57], v[2:9], v[196:203], v[54:57]
	v_mfma_f32_16x16x128_f8f6f4 v[46:49], v[10:17], v[196:203], v[46:49]
	v_mfma_f32_16x16x128_f8f6f4 v[38:41], v[2:9], v[204:211], v[38:41]
	v_mfma_f32_16x16x128_f8f6f4 v[34:37], v[10:17], v[204:211], v[34:37]
	s_setprio 0
	s_barrier
	ds_read_b128 v[2:5], v177
	ds_read_b128 v[6:9], v177 offset:1024
	ds_read_b128 v[10:13], v177 offset:2048
	ds_read_b128 v[14:17], v177 offset:3072
	ds_read_b128 v[18:21], v178
	ds_read_b128 v[22:25], v178 offset:1024
	ds_read_b128 v[26:29], v178 offset:2048
	ds_read_b128 v[30:33], v178 offset:3072
	ds_read_b128 v[180:183], v176 offset:32768
	ds_read_b128 v[184:187], v176 offset:33792
	ds_read_b128 v[188:191], v176 offset:34816
	ds_read_b128 v[192:195], v176 offset:35840
	ds_read_b128 v[196:199], v176 offset:36864
	ds_read_b128 v[200:203], v176 offset:37888
	ds_read_b128 v[204:207], v176 offset:38912
	ds_read_b128 v[208:211], v176 offset:39936
	s_add_u32 s78, s84, 0x20000
	s_addc_u32 s79, s85, 0
	s_mov_b32 s84, m0
	s_mov_b32 m0, s89
	s_nop 2
	global_load_lds_dwordx4 v166, s[78:79]
	s_mov_b32 m0, s84
	s_mov_b32 s84, m0
	s_mov_b32 m0, s3
	s_nop 2
	global_load_lds_dwordx4 v168, s[78:79]
	s_mov_b32 m0, s84
	s_waitcnt vmcnt(8)
	s_waitcnt lgkmcnt(0)
	s_barrier
	s_setprio 1
	v_mfma_f32_16x16x128_f8f6f4 v[158:161], v[2:9], v[180:187], v[158:161]
	v_mfma_f32_16x16x128_f8f6f4 v[154:157], v[10:17], v[180:187], v[154:157]
	v_mfma_f32_16x16x128_f8f6f4 v[146:149], v[2:9], v[188:195], v[146:149]
	v_mfma_f32_16x16x128_f8f6f4 v[138:141], v[10:17], v[188:195], v[138:141]
	v_mfma_f32_16x16x128_f8f6f4 v[130:133], v[2:9], v[196:203], v[130:133]
	v_mfma_f32_16x16x128_f8f6f4 v[122:125], v[10:17], v[196:203], v[122:125]
	v_mfma_f32_16x16x128_f8f6f4 v[114:117], v[2:9], v[204:211], v[114:117]
	v_mfma_f32_16x16x128_f8f6f4 v[106:109], v[10:17], v[204:211], v[106:109]
	v_mfma_f32_16x16x128_f8f6f4 v[150:153], v[18:25], v[180:187], v[150:153]
	v_mfma_f32_16x16x128_f8f6f4 v[142:145], v[26:33], v[180:187], v[142:145]
	v_mfma_f32_16x16x128_f8f6f4 v[134:137], v[18:25], v[188:195], v[134:137]
	v_mfma_f32_16x16x128_f8f6f4 v[126:129], v[26:33], v[188:195], v[126:129]
	v_mfma_f32_16x16x128_f8f6f4 v[118:121], v[18:25], v[196:203], v[118:121]
	v_mfma_f32_16x16x128_f8f6f4 v[110:113], v[26:33], v[196:203], v[110:113]
	v_mfma_f32_16x16x128_f8f6f4 v[102:105], v[18:25], v[204:211], v[102:105]
	v_mfma_f32_16x16x128_f8f6f4 v[98:101], v[26:33], v[204:211], v[98:101]
	s_setprio 0
	s_barrier
	ds_read_b128 v[180:183], v176 offset:49152
	ds_read_b128 v[184:187], v176 offset:50176
	ds_read_b128 v[188:191], v176 offset:51200
	ds_read_b128 v[192:195], v176 offset:52224
	ds_read_b128 v[196:199], v176 offset:53248
	ds_read_b128 v[200:203], v176 offset:54272
	ds_read_b128 v[204:207], v176 offset:55296
	ds_read_b128 v[208:211], v176 offset:56320
	s_add_u32 s78, s82, 0x80
	s_addc_u32 s79, s83, 0
	s_mov_b32 s84, m0
	s_mov_b32 m0, s90
	s_nop 2
	global_load_lds_dwordx4 v167, s[78:79]
	s_mov_b32 m0, s84
	s_mov_b32 s84, m0
	s_mov_b32 m0, s28
	s_nop 2
	global_load_lds_dwordx4 v169, s[78:79]
	s_mov_b32 m0, s84
	s_add_u32 s78, s82, 0x20080
	s_addc_u32 s79, s83, 0
	s_mov_b32 s82, m0
	s_mov_b32 m0, s94
	s_nop 2
	global_load_lds_dwordx4 v167, s[78:79]
	s_mov_b32 m0, s82
	s_mov_b32 s82, m0
	s_mov_b32 m0, s95
	s_nop 2
	global_load_lds_dwordx4 v169, s[78:79]
	s_mov_b32 m0, s82
	s_mov_b32 s78, m0
	s_mov_b32 m0, s93
	s_nop 2
	global_load_lds_dwordx4 v166, s[80:81]
	s_mov_b32 m0, s78
	s_mov_b32 s78, m0
	s_mov_b32 m0, s2
	s_nop 2
	global_load_lds_dwordx4 v168, s[80:81]
	s_mov_b32 m0, s78
	s_waitcnt vmcnt(8)
	s_waitcnt lgkmcnt(0)
	s_barrier
	s_setprio 1
	v_mfma_f32_16x16x128_f8f6f4 v[94:97], v[2:9], v[180:187], v[94:97]
	v_mfma_f32_16x16x128_f8f6f4 v[90:93], v[10:17], v[180:187], v[90:93]
	v_mfma_f32_16x16x128_f8f6f4 v[82:85], v[2:9], v[188:195], v[82:85]
	v_mfma_f32_16x16x128_f8f6f4 v[74:77], v[10:17], v[188:195], v[74:77]
	v_mfma_f32_16x16x128_f8f6f4 v[66:69], v[2:9], v[196:203], v[66:69]
	v_mfma_f32_16x16x128_f8f6f4 v[58:61], v[10:17], v[196:203], v[58:61]
	v_mfma_f32_16x16x128_f8f6f4 v[50:53], v[2:9], v[204:211], v[50:53]
	v_mfma_f32_16x16x128_f8f6f4 v[42:45], v[10:17], v[204:211], v[42:45]
	v_mfma_f32_16x16x128_f8f6f4 v[86:89], v[18:25], v[180:187], v[86:89]
	v_mfma_f32_16x16x128_f8f6f4 v[78:81], v[26:33], v[180:187], v[78:81]
	v_mfma_f32_16x16x128_f8f6f4 v[70:73], v[18:25], v[188:195], v[70:73]
	v_mfma_f32_16x16x128_f8f6f4 v[62:65], v[26:33], v[188:195], v[62:65]
	v_mfma_f32_16x16x128_f8f6f4 v[54:57], v[18:25], v[196:203], v[54:57]
	v_mfma_f32_16x16x128_f8f6f4 v[46:49], v[26:33], v[196:203], v[46:49]
	v_mfma_f32_16x16x128_f8f6f4 v[38:41], v[18:25], v[204:211], v[38:41]
	v_mfma_f32_16x16x128_f8f6f4 v[34:37], v[26:33], v[204:211], v[34:37]
	s_setprio 0
	s_barrier
	s_add_i32 s33, s33, 2
	s_add_u32 vcc_lo, vcc_lo, 0x100
	s_addc_u32 vcc_hi, vcc_hi, 0
	s_cmp_gt_u32 s33, 5
	s_mov_b64 s[78:79], s[76:77]
	s_cbranch_scc0 .LBB0_190
	s_and_b64 vcc, exec, s[10:11]
	s_cbranch_vccz .LBB0_193
	s_barrier

.LBB0_217:
	s_cmp_lt_i32 s33, 0
	s_cbranch_scc1 .Lpeel1
	ds_read_b128 v[18:21], v168
	ds_read_b128 v[22:25], v168 offset:1024
	ds_read_b128 v[26:29], v168 offset:2048
	ds_read_b128 v[30:33], v168 offset:3072
	ds_read_b128 v[2:5], v169
	ds_read_b128 v[6:9], v169 offset:1024
	ds_read_b128 v[10:13], v169 offset:2048
	ds_read_b128 v[14:17], v169 offset:3072
	s_add_u32 s78, s80, 0x100
	s_addc_u32 s79, s81, 0
	s_cmp_eq_u32 s33, 4
	s_cselect_b32 s86, s57, s78
	s_cselect_b32 s87, s7, s79
	s_cselect_b32 s84, vcc_lo, vcc_hi
	s_cselect_b32 s85, s59, s89
	s_add_u32 s82, s86, 0x80
	s_addc_u32 s83, s87, 0
	ds_read_b128 v[176:179], v170
	ds_read_b128 v[180:183], v170 offset:1024
	ds_read_b128 v[184:187], v170 offset:2048
	ds_read_b128 v[188:191], v170 offset:3072
	ds_read_b128 v[192:195], v170 offset:4096
	ds_read_b128 v[196:199], v170 offset:5120
	ds_read_b128 v[200:203], v170 offset:6144
	ds_read_b128 v[204:207], v170 offset:7168
	s_add_u32 s80, s80, 0x20080
	s_addc_u32 s81, s81, 0
	s_mov_b32 s29, m0
	s_mov_b32 m0, s91
	s_nop 2
	global_load_lds_dwordx4 v162, s[80:81]
	s_mov_b32 m0, s29
	s_mov_b32 s29, m0
	s_mov_b32 m0, s92
	s_nop 2
	global_load_lds_dwordx4 v164, s[80:81]
	s_mov_b32 m0, s29
	s_waitcnt vmcnt(8)
	s_waitcnt lgkmcnt(0)
	s_barrier
	s_setprio 1
	v_mfma_f32_16x16x128_f8f6f4 v[158:161], v[18:25], v[176:183], v[158:161]
	v_mfma_f32_16x16x128_f8f6f4 v[154:157], v[26:33], v[176:183], v[154:157]
	v_mfma_f32_16x16x128_f8f6f4 v[146:149], v[18:25], v[184:191], v[146:149]
	v_mfma_f32_16x16x128_f8f6f4 v[138:141], v[26:33], v[184:191], v[138:141]
	v_mfma_f32_16x16x128_f8f6f4 v[130:133], v[18:25], v[192:199], v[130:133]
	v_mfma_f32_16x16x128_f8f6f4 v[122:125], v[26:33], v[192:199], v[122:125]
	v_mfma_f32_16x16x128_f8f6f4 v[114:117], v[18:25], v[200:207], v[114:117]
	v_mfma_f32_16x16x128_f8f6f4 v[106:109], v[26:33], v[200:207], v[106:109]
	v_mfma_f32_16x16x128_f8f6f4 v[150:153], v[2:9], v[176:183], v[150:153]
	v_mfma_f32_16x16x128_f8f6f4 v[142:145], v[10:17], v[176:183], v[142:145]
	v_mfma_f32_16x16x128_f8f6f4 v[134:137], v[2:9], v[184:191], v[134:137]
	v_mfma_f32_16x16x128_f8f6f4 v[126:129], v[10:17], v[184:191], v[126:129]
	v_mfma_f32_16x16x128_f8f6f4 v[118:121], v[2:9], v[192:199], v[118:121]
	v_mfma_f32_16x16x128_f8f6f4 v[110:113], v[10:17], v[192:199], v[110:113]
	v_mfma_f32_16x16x128_f8f6f4 v[102:105], v[2:9], v[200:207], v[102:105]
	v_mfma_f32_16x16x128_f8f6f4 v[98:101], v[10:17], v[200:207], v[98:101]
	s_setprio 0
	s_barrier
	ds_read_b128 v[176:179], v170 offset:16384
	ds_read_b128 v[180:183], v170 offset:17408
	ds_read_b128 v[184:187], v170 offset:18432
	ds_read_b128 v[188:191], v170 offset:19456
	ds_read_b128 v[192:195], v170 offset:20480
	ds_read_b128 v[196:199], v170 offset:21504
	ds_read_b128 v[200:203], v170 offset:22528
	ds_read_b128 v[204:207], v170 offset:23552
	s_mov_b32 s29, m0
	s_mov_b32 m0, s36
	s_nop 2
	global_load_lds_dwordx4 v163, s[84:85]
	s_mov_b32 m0, s29
	s_add_u32 s80, s84, 0x20000
	s_mov_b32 s29, m0
	s_mov_b32 m0, s37
	s_nop 2
	global_load_lds_dwordx4 v165, s[84:85]
	s_mov_b32 m0, s29
	s_addc_u32 s81, s85, 0
	s_mov_b32 s29, m0
	s_mov_b32 m0, s55
	s_nop 2
	global_load_lds_dwordx4 v163, s[80:81]
	s_mov_b32 m0, s29
	s_mov_b32 s29, m0
	s_mov_b32 m0, s77
	s_nop 2
	global_load_lds_dwordx4 v165, s[80:81]
	s_mov_b32 m0, s29
	s_mov_b32 s29, m0
	s_mov_b32 m0, s35
	s_nop 2
	global_load_lds_dwordx4 v162, s[86:87]
	s_mov_b32 m0, s29
	s_mov_b32 s29, m0
	s_mov_b32 m0, s88
	s_nop 2
	global_load_lds_dwordx4 v164, s[86:87]
	s_mov_b32 m0, s29
	s_waitcnt vmcnt(8)
	s_waitcnt lgkmcnt(0)
	s_barrier
	s_setprio 1
	v_mfma_f32_16x16x128_f8f6f4 v[94:97], v[18:25], v[176:183], v[94:97]
	v_mfma_f32_16x16x128_f8f6f4 v[90:93], v[26:33], v[176:183], v[90:93]
	v_mfma_f32_16x16x128_f8f6f4 v[82:85], v[18:25], v[184:191], v[82:85]
	v_mfma_f32_16x16x128_f8f6f4 v[74:77], v[26:33], v[184:191], v[74:77]
	v_mfma_f32_16x16x128_f8f6f4 v[66:69], v[18:25], v[192:199], v[66:69]
	v_mfma_f32_16x16x128_f8f6f4 v[58:61], v[26:33], v[192:199], v[58:61]
	v_mfma_f32_16x16x128_f8f6f4 v[50:53], v[18:25], v[200:207], v[50:53]
	v_mfma_f32_16x16x128_f8f6f4 v[42:45], v[26:33], v[200:207], v[42:45]
	v_mfma_f32_16x16x128_f8f6f4 v[86:89], v[2:9], v[176:183], v[86:89]
	v_mfma_f32_16x16x128_f8f6f4 v[78:81], v[10:17], v[176:183], v[78:81]
	v_mfma_f32_16x16x128_f8f6f4 v[70:73], v[2:9], v[184:191], v[70:73]
	v_mfma_f32_16x16x128_f8f6f4 v[62:65], v[10:17], v[184:191], v[62:65]
	v_mfma_f32_16x16x128_f8f6f4 v[54:57], v[2:9], v[192:199], v[54:57]
	v_mfma_f32_16x16x128_f8f6f4 v[46:49], v[10:17], v[192:199], v[46:49]
	v_mfma_f32_16x16x128_f8f6f4 v[38:41], v[2:9], v[200:207], v[38:41]
	v_mfma_f32_16x16x128_f8f6f4 v[34:37], v[10:17], v[200:207], v[34:37]
	s_setprio 0
	s_barrier
.Lmid1:
	ds_read_b128 v[2:5], v172
	ds_read_b128 v[6:9], v172 offset:1024
	ds_read_b128 v[10:13], v172 offset:2048
	ds_read_b128 v[14:17], v172 offset:3072
	ds_read_b128 v[18:21], v174
	ds_read_b128 v[22:25], v174 offset:1024
	ds_read_b128 v[26:29], v174 offset:2048
	ds_read_b128 v[30:33], v174 offset:3072
	ds_read_b128 v[176:179], v170 offset:32768
	ds_read_b128 v[180:183], v170 offset:33792
	ds_read_b128 v[184:187], v170 offset:34816
	ds_read_b128 v[188:191], v170 offset:35840
	ds_read_b128 v[192:195], v170 offset:36864
	ds_read_b128 v[196:199], v170 offset:37888
	ds_read_b128 v[200:203], v170 offset:38912
	ds_read_b128 v[204:207], v170 offset:39936
	s_add_u32 s80, s86, 0x20000
	s_addc_u32 s81, s87, 0
	s_mov_b32 s29, m0
	s_mov_b32 m0, s97
	s_nop 2
	global_load_lds_dwordx4 v162, s[80:81]
	s_mov_b32 m0, s29
	s_mov_b32 s29, m0
	s_mov_b32 m0, s3
	s_nop 2
	global_load_lds_dwordx4 v164, s[80:81]
	s_mov_b32 m0, s29
	s_waitcnt vmcnt(8)
	s_waitcnt lgkmcnt(0)
	s_barrier
	s_setprio 1
	v_mfma_f32_16x16x128_f8f6f4 v[158:161], v[2:9], v[176:183], v[158:161]
	v_mfma_f32_16x16x128_f8f6f4 v[154:157], v[10:17], v[176:183], v[154:157]
	v_mfma_f32_16x16x128_f8f6f4 v[146:149], v[2:9], v[184:191], v[146:149]
	v_mfma_f32_16x16x128_f8f6f4 v[138:141], v[10:17], v[184:191], v[138:141]
	v_mfma_f32_16x16x128_f8f6f4 v[130:133], v[2:9], v[192:199], v[130:133]
	v_mfma_f32_16x16x128_f8f6f4 v[122:125], v[10:17], v[192:199], v[122:125]
	v_mfma_f32_16x16x128_f8f6f4 v[114:117], v[2:9], v[200:207], v[114:117]
	v_mfma_f32_16x16x128_f8f6f4 v[106:109], v[10:17], v[200:207], v[106:109]
	v_mfma_f32_16x16x128_f8f6f4 v[150:153], v[18:25], v[176:183], v[150:153]
	v_mfma_f32_16x16x128_f8f6f4 v[142:145], v[26:33], v[176:183], v[142:145]
	v_mfma_f32_16x16x128_f8f6f4 v[134:137], v[18:25], v[184:191], v[134:137]
	v_mfma_f32_16x16x128_f8f6f4 v[126:129], v[26:33], v[184:191], v[126:129]
	v_mfma_f32_16x16x128_f8f6f4 v[118:121], v[18:25], v[192:199], v[118:121]
	v_mfma_f32_16x16x128_f8f6f4 v[110:113], v[26:33], v[192:199], v[110:113]
	v_mfma_f32_16x16x128_f8f6f4 v[102:105], v[18:25], v[200:207], v[102:105]
	v_mfma_f32_16x16x128_f8f6f4 v[98:101], v[26:33], v[200:207], v[98:101]
	s_setprio 0
	s_barrier
	ds_read_b128 v[176:179], v170 offset:49152
	ds_read_b128 v[180:183], v170 offset:50176
	ds_read_b128 v[184:187], v170 offset:51200
	ds_read_b128 v[188:191], v170 offset:52224
	ds_read_b128 v[192:195], v170 offset:53248
	ds_read_b128 v[196:199], v170 offset:54272
	ds_read_b128 v[200:203], v170 offset:55296
	ds_read_b128 v[204:207], v170 offset:56320
	s_add_u32 s80, s84, 0x80
	s_addc_u32 s81, s85, 0
	s_mov_b32 s29, m0
	s_mov_b32 m0, s90
	s_nop 2
	global_load_lds_dwordx4 v163, s[80:81]
	s_mov_b32 m0, s29
	s_mov_b32 s29, m0
	s_mov_b32 m0, s28
	s_nop 2
	global_load_lds_dwordx4 v165, s[80:81]
	s_mov_b32 m0, s29
	s_add_u32 s80, s84, 0x20080
	s_addc_u32 s81, s85, 0
	s_mov_b32 s29, m0
	s_mov_b32 m0, s94
	s_nop 2
	global_load_lds_dwordx4 v163, s[80:81]
	s_mov_b32 m0, s29
	s_mov_b32 s29, m0
	s_mov_b32 m0, s95
	s_nop 2
	global_load_lds_dwordx4 v165, s[80:81]
	s_mov_b32 m0, s29
	s_mov_b32 s29, m0
	s_mov_b32 m0, s93
	s_nop 2
	global_load_lds_dwordx4 v162, s[82:83]
	s_mov_b32 m0, s29
	s_mov_b32 s29, m0
	s_mov_b32 m0, s2
	s_nop 2
	global_load_lds_dwordx4 v164, s[82:83]
	s_mov_b32 m0, s29
	s_waitcnt vmcnt(8)
	s_waitcnt lgkmcnt(0)
	s_barrier
	s_setprio 1
	v_mfma_f32_16x16x128_f8f6f4 v[94:97], v[2:9], v[176:183], v[94:97]
	v_mfma_f32_16x16x128_f8f6f4 v[90:93], v[10:17], v[176:183], v[90:93]
	v_mfma_f32_16x16x128_f8f6f4 v[82:85], v[2:9], v[184:191], v[82:85]
	v_mfma_f32_16x16x128_f8f6f4 v[74:77], v[10:17], v[184:191], v[74:77]
	v_mfma_f32_16x16x128_f8f6f4 v[66:69], v[2:9], v[192:199], v[66:69]
	v_mfma_f32_16x16x128_f8f6f4 v[58:61], v[10:17], v[192:199], v[58:61]
	v_mfma_f32_16x16x128_f8f6f4 v[50:53], v[2:9], v[200:207], v[50:53]
	v_mfma_f32_16x16x128_f8f6f4 v[42:45], v[10:17], v[200:207], v[42:45]
	v_mfma_f32_16x16x128_f8f6f4 v[86:89], v[18:25], v[176:183], v[86:89]
	v_mfma_f32_16x16x128_f8f6f4 v[78:81], v[26:33], v[176:183], v[78:81]
	v_mfma_f32_16x16x128_f8f6f4 v[70:73], v[18:25], v[184:191], v[70:73]
	v_mfma_f32_16x16x128_f8f6f4 v[62:65], v[26:33], v[184:191], v[62:65]
	v_mfma_f32_16x16x128_f8f6f4 v[54:57], v[18:25], v[192:199], v[54:57]
	v_mfma_f32_16x16x128_f8f6f4 v[46:49], v[26:33], v[192:199], v[46:49]
	v_mfma_f32_16x16x128_f8f6f4 v[38:41], v[18:25], v[200:207], v[38:41]
	v_mfma_f32_16x16x128_f8f6f4 v[34:37], v[26:33], v[200:207], v[34:37]
	s_setprio 0
	s_cmp_lt_i32 s33, 4
	s_cbranch_scc1 .Lkb1_do
	s_cmp_lg_u64 s[10:11], 0
	s_cbranch_scc0 .Lkb1_skip

.Lpeel1:
	ds_read_b128 v[18:21], v168
	ds_read_b128 v[22:25], v168 offset:1024
	ds_read_b128 v[26:29], v168 offset:2048
	ds_read_b128 v[30:33], v168 offset:3072
	ds_read_b128 v[2:5], v169
	ds_read_b128 v[6:9], v169 offset:1024
	ds_read_b128 v[10:13], v169 offset:2048
	ds_read_b128 v[14:17], v169 offset:3072
	s_add_u32 s78, s80, 0x100
	s_addc_u32 s79, s81, 0
	s_cmp_eq_u32 s33, 4
	s_cselect_b32 s86, s57, s78
	s_cselect_b32 s87, s7, s79
	s_cselect_b32 s84, vcc_lo, vcc_hi
	s_cselect_b32 s85, s59, s89
	s_add_u32 s82, s86, 0x80
	s_addc_u32 s83, s87, 0
	ds_read_b128 v[176:179], v170
	ds_read_b128 v[180:183], v170 offset:1024
	ds_read_b128 v[184:187], v170 offset:2048
	ds_read_b128 v[188:191], v170 offset:3072
	ds_read_b128 v[192:195], v170 offset:4096
	ds_read_b128 v[196:199], v170 offset:5120
	ds_read_b128 v[200:203], v170 offset:6144
	ds_read_b128 v[204:207], v170 offset:7168
	s_add_u32 s80, s80, 0x20080
	s_addc_u32 s81, s81, 0
	s_mov_b32 s29, m0
	s_mov_b32 m0, s91
	s_nop 2
	global_load_lds_dwordx4 v162, s[80:81]
	s_mov_b32 m0, s29
	s_mov_b32 s29, m0
	s_mov_b32 m0, s92
	s_nop 2
	global_load_lds_dwordx4 v164, s[80:81]
	s_mov_b32 m0, s29
	s_waitcnt vmcnt(8)
	s_waitcnt lgkmcnt(0)
	s_barrier
	s_setprio 1
	v_mfma_f32_16x16x128_f8f6f4 v[158:161], v[18:25], v[176:183], 0
	v_mfma_f32_16x16x128_f8f6f4 v[154:157], v[26:33], v[176:183], 0
	v_mfma_f32_16x16x128_f8f6f4 v[146:149], v[18:25], v[184:191], 0
	v_mfma_f32_16x16x128_f8f6f4 v[138:141], v[26:33], v[184:191], 0
	v_mfma_f32_16x16x128_f8f6f4 v[130:133], v[18:25], v[192:199], 0
	v_mfma_f32_16x16x128_f8f6f4 v[122:125], v[26:33], v[192:199], 0
	v_mfma_f32_16x16x128_f8f6f4 v[114:117], v[18:25], v[200:207], 0
	v_mfma_f32_16x16x128_f8f6f4 v[106:109], v[26:33], v[200:207], 0
	v_mfma_f32_16x16x128_f8f6f4 v[150:153], v[2:9], v[176:183], 0
	v_mfma_f32_16x16x128_f8f6f4 v[142:145], v[10:17], v[176:183], 0
	v_mfma_f32_16x16x128_f8f6f4 v[134:137], v[2:9], v[184:191], 0
	v_mfma_f32_16x16x128_f8f6f4 v[126:129], v[10:17], v[184:191], 0
	v_mfma_f32_16x16x128_f8f6f4 v[118:121], v[2:9], v[192:199], 0
	v_mfma_f32_16x16x128_f8f6f4 v[110:113], v[10:17], v[192:199], 0
	v_mfma_f32_16x16x128_f8f6f4 v[102:105], v[2:9], v[200:207], 0
	v_mfma_f32_16x16x128_f8f6f4 v[98:101], v[10:17], v[200:207], 0
	s_setprio 0
	s_barrier
	ds_read_b128 v[176:179], v170 offset:16384
	ds_read_b128 v[180:183], v170 offset:17408
	ds_read_b128 v[184:187], v170 offset:18432
	ds_read_b128 v[188:191], v170 offset:19456
	ds_read_b128 v[192:195], v170 offset:20480
	ds_read_b128 v[196:199], v170 offset:21504
	ds_read_b128 v[200:203], v170 offset:22528
	ds_read_b128 v[204:207], v170 offset:23552
	s_mov_b32 s29, m0
	s_mov_b32 m0, s36
	s_nop 2
	global_load_lds_dwordx4 v163, s[84:85]
	s_mov_b32 m0, s29
	s_add_u32 s80, s84, 0x20000
	s_mov_b32 s29, m0
	s_mov_b32 m0, s37
	s_nop 2
	global_load_lds_dwordx4 v165, s[84:85]
	s_mov_b32 m0, s29
	s_addc_u32 s81, s85, 0
	s_mov_b32 s29, m0
	s_mov_b32 m0, s55
	s_nop 2
	global_load_lds_dwordx4 v163, s[80:81]
	s_mov_b32 m0, s29
	s_mov_b32 s29, m0
	s_mov_b32 m0, s77
	s_nop 2
	global_load_lds_dwordx4 v165, s[80:81]
	s_mov_b32 m0, s29
	s_mov_b32 s29, m0
	s_mov_b32 m0, s35
	s_nop 2
	global_load_lds_dwordx4 v162, s[86:87]
	s_mov_b32 m0, s29
	s_mov_b32 s29, m0
	s_mov_b32 m0, s88
	s_nop 2
	global_load_lds_dwordx4 v164, s[86:87]
	s_mov_b32 m0, s29
	s_waitcnt vmcnt(8)
	s_waitcnt lgkmcnt(0)
	s_barrier
	s_setprio 1
	v_mfma_f32_16x16x128_f8f6f4 v[94:97], v[18:25], v[176:183], 0
	v_mfma_f32_16x16x128_f8f6f4 v[90:93], v[26:33], v[176:183], 0
	v_mfma_f32_16x16x128_f8f6f4 v[82:85], v[18:25], v[184:191], 0
	v_mfma_f32_16x16x128_f8f6f4 v[74:77], v[26:33], v[184:191], 0
	v_mfma_f32_16x16x128_f8f6f4 v[66:69], v[18:25], v[192:199], 0
	v_mfma_f32_16x16x128_f8f6f4 v[58:61], v[26:33], v[192:199], 0
	v_mfma_f32_16x16x128_f8f6f4 v[50:53], v[18:25], v[200:207], 0
	v_mfma_f32_16x16x128_f8f6f4 v[42:45], v[26:33], v[200:207], 0
	v_mfma_f32_16x16x128_f8f6f4 v[86:89], v[2:9], v[176:183], 0
	v_mfma_f32_16x16x128_f8f6f4 v[78:81], v[10:17], v[176:183], 0
	v_mfma_f32_16x16x128_f8f6f4 v[70:73], v[2:9], v[184:191], 0
	v_mfma_f32_16x16x128_f8f6f4 v[62:65], v[10:17], v[184:191], 0
	v_mfma_f32_16x16x128_f8f6f4 v[54:57], v[2:9], v[192:199], 0
	v_mfma_f32_16x16x128_f8f6f4 v[46:49], v[10:17], v[192:199], 0
	v_mfma_f32_16x16x128_f8f6f4 v[38:41], v[2:9], v[200:207], 0
	v_mfma_f32_16x16x128_f8f6f4 v[34:37], v[10:17], v[200:207], 0
	s_setprio 0
	s_barrier
	s_branch .Lmid1

.Lpeel1046:
	ds_read_b128 v[136:139], v172
	ds_read_b128 v[140:143], v172 offset:1024
	ds_read_b128 v[144:147], v172 offset:2048
	ds_read_b128 v[148:151], v172 offset:3072
	ds_read_b128 v[152:155], v173
	ds_read_b128 v[156:159], v173 offset:1024
	ds_read_b128 v[160:163], v173 offset:2048
	ds_read_b128 v[178:181], v173 offset:3072
	s_add_u32 s25, s64, s56
	s_addc_u32 s33, s65, s57
	s_add_u32 s66, s25, 0x100
	s_addc_u32 s67, s33, 0
	s_add_u32 s23, s62, s56
	s_addc_u32 s24, s63, s57
	s_add_u32 s28, s23, 0x100
	s_addc_u32 s29, s24, 0
	s_add_u32 s58, s25, 0x180
	s_addc_u32 s59, s33, 0
	ds_read_b128 v[182:185], v174
	ds_read_b128 v[186:189], v174 offset:1024
	ds_read_b128 v[190:193], v174 offset:2048
	ds_read_b128 v[194:197], v174 offset:3072
	ds_read_b128 v[198:201], v174 offset:4096
	ds_read_b128 v[202:205], v174 offset:5120
	ds_read_b128 v[206:209], v174 offset:6144
	ds_read_b128 v[210:213], v174 offset:7168
	s_add_u32 s30, s25, 0x40080
	s_addc_u32 s31, s33, 0
	s_mov_b32 s36, m0
	s_mov_b32 m0, s26
	s_nop 2
	global_load_lds_dwordx4 v165, s[30:31]
	s_mov_b32 m0, s36
	s_mov_b32 s36, m0
	s_mov_b32 m0, s27
	s_nop 2
	global_load_lds_dwordx4 v167, s[30:31]
	s_mov_b32 m0, s36
	s_waitcnt vmcnt(8)
	s_waitcnt lgkmcnt(0)
	s_barrier
	s_setprio 1
	v_mfma_f32_16x16x32_bf16 v[26:29], v[136:139], v[182:185], 0
	v_mfma_f32_16x16x32_bf16 v[30:33], v[144:147], v[182:185], 0
	v_mfma_f32_16x16x32_bf16 v[50:53], v[136:139], v[190:193], 0
	v_mfma_f32_16x16x32_bf16 v[54:57], v[144:147], v[190:193], 0
	v_mfma_f32_16x16x32_bf16 v[74:77], v[136:139], v[198:201], 0
	v_mfma_f32_16x16x32_bf16 v[78:81], v[144:147], v[198:201], 0
	v_mfma_f32_16x16x32_bf16 v[94:97], v[136:139], v[206:209], 0
	v_mfma_f32_16x16x32_bf16 v[102:105], v[144:147], v[206:209], 0
	v_mfma_f32_16x16x32_bf16 v[26:29], v[140:143], v[186:189], v[26:29]
	v_mfma_f32_16x16x32_bf16 v[30:33], v[148:151], v[186:189], v[30:33]
	v_mfma_f32_16x16x32_bf16 v[50:53], v[140:143], v[194:197], v[50:53]
	v_mfma_f32_16x16x32_bf16 v[54:57], v[148:151], v[194:197], v[54:57]
	v_mfma_f32_16x16x32_bf16 v[74:77], v[140:143], v[202:205], v[74:77]
	v_mfma_f32_16x16x32_bf16 v[78:81], v[148:151], v[202:205], v[78:81]
	v_mfma_f32_16x16x32_bf16 v[94:97], v[140:143], v[210:213], v[94:97]
	v_mfma_f32_16x16x32_bf16 v[102:105], v[148:151], v[210:213], v[102:105]
	v_mfma_f32_16x16x32_bf16 v[38:41], v[152:155], v[182:185], 0
	v_mfma_f32_16x16x32_bf16 v[42:45], v[160:163], v[182:185], 0
	v_mfma_f32_16x16x32_bf16 v[62:65], v[152:155], v[190:193], 0
	v_mfma_f32_16x16x32_bf16 v[66:69], v[160:163], v[190:193], 0
	v_mfma_f32_16x16x32_bf16 v[82:85], v[152:155], v[198:201], 0
	v_mfma_f32_16x16x32_bf16 v[90:93], v[160:163], v[198:201], 0
	v_mfma_f32_16x16x32_bf16 v[106:109], v[152:155], v[206:209], 0
	v_mfma_f32_16x16x32_bf16 v[114:117], v[160:163], v[206:209], 0
	v_mfma_f32_16x16x32_bf16 v[38:41], v[156:159], v[186:189], v[38:41]
	v_mfma_f32_16x16x32_bf16 v[42:45], v[178:181], v[186:189], v[42:45]
	v_mfma_f32_16x16x32_bf16 v[62:65], v[156:159], v[194:197], v[62:65]
	v_mfma_f32_16x16x32_bf16 v[66:69], v[178:181], v[194:197], v[66:69]
	v_mfma_f32_16x16x32_bf16 v[82:85], v[156:159], v[202:205], v[82:85]
	v_mfma_f32_16x16x32_bf16 v[90:93], v[178:181], v[202:205], v[90:93]
	v_mfma_f32_16x16x32_bf16 v[106:109], v[156:159], v[210:213], v[106:109]
	v_mfma_f32_16x16x32_bf16 v[114:117], v[178:181], v[210:213], v[114:117]
	s_setprio 0
	s_barrier
	ds_read_b128 v[182:185], v174 offset:16384
	ds_read_b128 v[186:189], v174 offset:17408
	ds_read_b128 v[190:193], v174 offset:18432
	ds_read_b128 v[194:197], v174 offset:19456
	ds_read_b128 v[198:201], v174 offset:20480
	ds_read_b128 v[202:205], v174 offset:21504
	ds_read_b128 v[206:209], v174 offset:22528
	ds_read_b128 v[210:213], v174 offset:23552
	s_mov_b32 s30, m0
	s_mov_b32 m0, s80
	s_nop 2
	global_load_lds_dwordx4 v166, s[28:29]
	s_mov_b32 m0, s30
	s_mov_b32 s30, m0
	s_mov_b32 m0, s81
	s_nop 2
	global_load_lds_dwordx4 v168, s[28:29]
	s_mov_b32 m0, s30
	s_add_u32 s28, s23, 0x40100
	s_addc_u32 s29, s24, 0
	s_mov_b32 s30, m0
	s_mov_b32 m0, s82
	s_nop 2
	global_load_lds_dwordx4 v166, s[28:29]
	s_mov_b32 m0, s30
	s_mov_b32 s30, m0
	s_mov_b32 m0, s83
	s_nop 2
	global_load_lds_dwordx4 v168, s[28:29]
	s_mov_b32 m0, s30
	s_mov_b32 s28, m0
	s_mov_b32 m0, s79
	s_nop 2
	global_load_lds_dwordx4 v165, s[66:67]
	s_mov_b32 m0, s28
	s_mov_b32 s28, m0
	s_mov_b32 m0, s84
	s_nop 2
	global_load_lds_dwordx4 v167, s[66:67]
	s_mov_b32 m0, s28
	s_waitcnt vmcnt(8)
	s_waitcnt lgkmcnt(0)
	s_barrier
	s_setprio 1
	v_mfma_f32_16x16x32_bf16 v[118:121], v[136:139], v[182:185], 0
	v_mfma_f32_16x16x32_bf16 v[126:129], v[144:147], v[182:185], 0
	v_mfma_f32_16x16x32_bf16 v[98:101], v[136:139], v[190:193], 0
	v_mfma_f32_16x16x32_bf16 v[86:89], v[144:147], v[190:193], 0
	v_mfma_f32_16x16x32_bf16 v[46:49], v[136:139], v[198:201], 0
	v_mfma_f32_16x16x32_bf16 v[34:37], v[144:147], v[198:201], 0
	v_mfma_f32_16x16x32_bf16 v[14:17], v[136:139], v[206:209], 0
	v_mfma_f32_16x16x32_bf16 v[10:13], v[144:147], v[206:209], 0
	v_mfma_f32_16x16x32_bf16 v[118:121], v[140:143], v[186:189], v[118:121]
	v_mfma_f32_16x16x32_bf16 v[126:129], v[148:151], v[186:189], v[126:129]
	v_mfma_f32_16x16x32_bf16 v[98:101], v[140:143], v[194:197], v[98:101]
	v_mfma_f32_16x16x32_bf16 v[86:89], v[148:151], v[194:197], v[86:89]
	v_mfma_f32_16x16x32_bf16 v[46:49], v[140:143], v[202:205], v[46:49]
	v_mfma_f32_16x16x32_bf16 v[34:37], v[148:151], v[202:205], v[34:37]
	v_mfma_f32_16x16x32_bf16 v[14:17], v[140:143], v[210:213], v[14:17]
	v_mfma_f32_16x16x32_bf16 v[10:13], v[148:151], v[210:213], v[10:13]
	v_mfma_f32_16x16x32_bf16 v[122:125], v[152:155], v[182:185], 0
	v_mfma_f32_16x16x32_bf16 v[110:113], v[160:163], v[182:185], 0
	v_mfma_f32_16x16x32_bf16 v[70:73], v[152:155], v[190:193], 0
	v_mfma_f32_16x16x32_bf16 v[58:61], v[160:163], v[190:193], 0
	v_mfma_f32_16x16x32_bf16 v[22:25], v[152:155], v[198:201], 0
	v_mfma_f32_16x16x32_bf16 v[18:21], v[160:163], v[198:201], 0
	v_mfma_f32_16x16x32_bf16 v[6:9], v[152:155], v[206:209], 0
	v_mfma_f32_16x16x32_bf16 v[2:5], v[160:163], v[206:209], 0
	v_mfma_f32_16x16x32_bf16 v[122:125], v[156:159], v[186:189], v[122:125]
	v_mfma_f32_16x16x32_bf16 v[110:113], v[178:181], v[186:189], v[110:113]
	v_mfma_f32_16x16x32_bf16 v[70:73], v[156:159], v[194:197], v[70:73]
	v_mfma_f32_16x16x32_bf16 v[58:61], v[178:181], v[194:197], v[58:61]
	v_mfma_f32_16x16x32_bf16 v[22:25], v[156:159], v[202:205], v[22:25]
	v_mfma_f32_16x16x32_bf16 v[18:21], v[178:181], v[202:205], v[18:21]
	v_mfma_f32_16x16x32_bf16 v[6:9], v[156:159], v[210:213], v[6:9]
	v_mfma_f32_16x16x32_bf16 v[2:5], v[178:181], v[210:213], v[2:5]
	s_setprio 0
	s_barrier
	s_branch .Lmid1046
.LBB0_1046:
	ds_read_b128 v[136:139], v172
	ds_read_b128 v[140:143], v172 offset:1024
	ds_read_b128 v[144:147], v172 offset:2048
	ds_read_b128 v[148:151], v172 offset:3072
	ds_read_b128 v[152:155], v173
	ds_read_b128 v[156:159], v173 offset:1024
	ds_read_b128 v[160:163], v173 offset:2048
	ds_read_b128 v[178:181], v173 offset:3072
	s_add_u32 s25, s64, s56
	s_addc_u32 s33, s65, s57
	s_add_u32 s66, s25, 0x100
	s_addc_u32 s67, s33, 0
	s_add_u32 s23, s62, s56
	s_addc_u32 s24, s63, s57
	s_add_u32 s28, s23, 0x100
	s_addc_u32 s29, s24, 0
	s_add_u32 s58, s25, 0x180
	s_addc_u32 s59, s33, 0
	ds_read_b128 v[182:185], v174
	ds_read_b128 v[186:189], v174 offset:1024
	ds_read_b128 v[190:193], v174 offset:2048
	ds_read_b128 v[194:197], v174 offset:3072
	ds_read_b128 v[198:201], v174 offset:4096
	ds_read_b128 v[202:205], v174 offset:5120
	ds_read_b128 v[206:209], v174 offset:6144
	ds_read_b128 v[210:213], v174 offset:7168
	s_add_u32 s30, s25, 0x40080
	s_addc_u32 s31, s33, 0
	s_mov_b32 s36, m0
	s_mov_b32 m0, s26
	s_nop 2
	global_load_lds_dwordx4 v165, s[30:31]
	s_mov_b32 m0, s36
	s_mov_b32 s36, m0
	s_mov_b32 m0, s27
	s_nop 2
	global_load_lds_dwordx4 v167, s[30:31]
	s_mov_b32 m0, s36
	s_waitcnt vmcnt(8)
	s_waitcnt lgkmcnt(0)
	s_barrier
	s_setprio 1
	v_mfma_f32_16x16x32_bf16 v[26:29], v[136:139], v[182:185], v[26:29]
	v_mfma_f32_16x16x32_bf16 v[30:33], v[144:147], v[182:185], v[30:33]
	v_mfma_f32_16x16x32_bf16 v[50:53], v[136:139], v[190:193], v[50:53]
	v_mfma_f32_16x16x32_bf16 v[54:57], v[144:147], v[190:193], v[54:57]
	v_mfma_f32_16x16x32_bf16 v[74:77], v[136:139], v[198:201], v[74:77]
	v_mfma_f32_16x16x32_bf16 v[78:81], v[144:147], v[198:201], v[78:81]
	v_mfma_f32_16x16x32_bf16 v[94:97], v[136:139], v[206:209], v[94:97]
	v_mfma_f32_16x16x32_bf16 v[102:105], v[144:147], v[206:209], v[102:105]
	v_mfma_f32_16x16x32_bf16 v[26:29], v[140:143], v[186:189], v[26:29]
	v_mfma_f32_16x16x32_bf16 v[30:33], v[148:151], v[186:189], v[30:33]
	v_mfma_f32_16x16x32_bf16 v[50:53], v[140:143], v[194:197], v[50:53]
	v_mfma_f32_16x16x32_bf16 v[54:57], v[148:151], v[194:197], v[54:57]
	v_mfma_f32_16x16x32_bf16 v[74:77], v[140:143], v[202:205], v[74:77]
	v_mfma_f32_16x16x32_bf16 v[78:81], v[148:151], v[202:205], v[78:81]
	v_mfma_f32_16x16x32_bf16 v[94:97], v[140:143], v[210:213], v[94:97]
	v_mfma_f32_16x16x32_bf16 v[102:105], v[148:151], v[210:213], v[102:105]
	v_mfma_f32_16x16x32_bf16 v[38:41], v[152:155], v[182:185], v[38:41]
	v_mfma_f32_16x16x32_bf16 v[42:45], v[160:163], v[182:185], v[42:45]
	v_mfma_f32_16x16x32_bf16 v[62:65], v[152:155], v[190:193], v[62:65]
	v_mfma_f32_16x16x32_bf16 v[66:69], v[160:163], v[190:193], v[66:69]
	v_mfma_f32_16x16x32_bf16 v[82:85], v[152:155], v[198:201], v[82:85]
	v_mfma_f32_16x16x32_bf16 v[90:93], v[160:163], v[198:201], v[90:93]
	v_mfma_f32_16x16x32_bf16 v[106:109], v[152:155], v[206:209], v[106:109]
	v_mfma_f32_16x16x32_bf16 v[114:117], v[160:163], v[206:209], v[114:117]
	v_mfma_f32_16x16x32_bf16 v[38:41], v[156:159], v[186:189], v[38:41]
	v_mfma_f32_16x16x32_bf16 v[42:45], v[178:181], v[186:189], v[42:45]
	v_mfma_f32_16x16x32_bf16 v[62:65], v[156:159], v[194:197], v[62:65]
	v_mfma_f32_16x16x32_bf16 v[66:69], v[178:181], v[194:197], v[66:69]
	v_mfma_f32_16x16x32_bf16 v[82:85], v[156:159], v[202:205], v[82:85]
	v_mfma_f32_16x16x32_bf16 v[90:93], v[178:181], v[202:205], v[90:93]
	v_mfma_f32_16x16x32_bf16 v[106:109], v[156:159], v[210:213], v[106:109]
	v_mfma_f32_16x16x32_bf16 v[114:117], v[178:181], v[210:213], v[114:117]
	s_setprio 0
	s_barrier
	ds_read_b128 v[182:185], v174 offset:16384
	ds_read_b128 v[186:189], v174 offset:17408
	ds_read_b128 v[190:193], v174 offset:18432
	ds_read_b128 v[194:197], v174 offset:19456
	ds_read_b128 v[198:201], v174 offset:20480
	ds_read_b128 v[202:205], v174 offset:21504
	ds_read_b128 v[206:209], v174 offset:22528
	ds_read_b128 v[210:213], v174 offset:23552
	s_mov_b32 s30, m0
	s_mov_b32 m0, s80
	s_nop 2
	global_load_lds_dwordx4 v166, s[28:29]
	s_mov_b32 m0, s30
	s_mov_b32 s30, m0
	s_mov_b32 m0, s81
	s_nop 2
	global_load_lds_dwordx4 v168, s[28:29]
	s_mov_b32 m0, s30
	s_add_u32 s28, s23, 0x40100
	s_addc_u32 s29, s24, 0
	s_mov_b32 s30, m0
	s_mov_b32 m0, s82
	s_nop 2
	global_load_lds_dwordx4 v166, s[28:29]
	s_mov_b32 m0, s30
	s_mov_b32 s30, m0
	s_mov_b32 m0, s83
	s_nop 2
	global_load_lds_dwordx4 v168, s[28:29]
	s_mov_b32 m0, s30
	s_mov_b32 s28, m0
	s_mov_b32 m0, s79
	s_nop 2
	global_load_lds_dwordx4 v165, s[66:67]
	s_mov_b32 m0, s28
	s_mov_b32 s28, m0
	s_mov_b32 m0, s84
	s_nop 2
	global_load_lds_dwordx4 v167, s[66:67]
	s_mov_b32 m0, s28
	s_waitcnt vmcnt(8)
	s_waitcnt lgkmcnt(0)
	s_barrier
	s_setprio 1
	v_mfma_f32_16x16x32_bf16 v[118:121], v[136:139], v[182:185], v[118:121]
	v_mfma_f32_16x16x32_bf16 v[126:129], v[144:147], v[182:185], v[126:129]
	v_mfma_f32_16x16x32_bf16 v[98:101], v[136:139], v[190:193], v[98:101]
	v_mfma_f32_16x16x32_bf16 v[86:89], v[144:147], v[190:193], v[86:89]
	v_mfma_f32_16x16x32_bf16 v[46:49], v[136:139], v[198:201], v[46:49]
	v_mfma_f32_16x16x32_bf16 v[34:37], v[144:147], v[198:201], v[34:37]
	v_mfma_f32_16x16x32_bf16 v[14:17], v[136:139], v[206:209], v[14:17]
	v_mfma_f32_16x16x32_bf16 v[10:13], v[144:147], v[206:209], v[10:13]
	v_mfma_f32_16x16x32_bf16 v[118:121], v[140:143], v[186:189], v[118:121]
	v_mfma_f32_16x16x32_bf16 v[126:129], v[148:151], v[186:189], v[126:129]
	v_mfma_f32_16x16x32_bf16 v[98:101], v[140:143], v[194:197], v[98:101]
	v_mfma_f32_16x16x32_bf16 v[86:89], v[148:151], v[194:197], v[86:89]
	v_mfma_f32_16x16x32_bf16 v[46:49], v[140:143], v[202:205], v[46:49]
	v_mfma_f32_16x16x32_bf16 v[34:37], v[148:151], v[202:205], v[34:37]
	v_mfma_f32_16x16x32_bf16 v[14:17], v[140:143], v[210:213], v[14:17]
	v_mfma_f32_16x16x32_bf16 v[10:13], v[148:151], v[210:213], v[10:13]
	v_mfma_f32_16x16x32_bf16 v[122:125], v[152:155], v[182:185], v[122:125]
	v_mfma_f32_16x16x32_bf16 v[110:113], v[160:163], v[182:185], v[110:113]
	v_mfma_f32_16x16x32_bf16 v[70:73], v[152:155], v[190:193], v[70:73]
	v_mfma_f32_16x16x32_bf16 v[58:61], v[160:163], v[190:193], v[58:61]
	v_mfma_f32_16x16x32_bf16 v[22:25], v[152:155], v[198:201], v[22:25]
	v_mfma_f32_16x16x32_bf16 v[18:21], v[160:163], v[198:201], v[18:21]
	v_mfma_f32_16x16x32_bf16 v[6:9], v[152:155], v[206:209], v[6:9]
	v_mfma_f32_16x16x32_bf16 v[2:5], v[160:163], v[206:209], v[2:5]
	v_mfma_f32_16x16x32_bf16 v[122:125], v[156:159], v[186:189], v[122:125]
	v_mfma_f32_16x16x32_bf16 v[110:113], v[178:181], v[186:189], v[110:113]
	v_mfma_f32_16x16x32_bf16 v[70:73], v[156:159], v[194:197], v[70:73]
	v_mfma_f32_16x16x32_bf16 v[58:61], v[178:181], v[194:197], v[58:61]
	v_mfma_f32_16x16x32_bf16 v[22:25], v[156:159], v[202:205], v[22:25]
	v_mfma_f32_16x16x32_bf16 v[18:21], v[178:181], v[202:205], v[18:21]
	v_mfma_f32_16x16x32_bf16 v[6:9], v[156:159], v[210:213], v[6:9]
	v_mfma_f32_16x16x32_bf16 v[2:5], v[178:181], v[210:213], v[2:5]
	s_setprio 0
	s_barrier
.Lmid1046:
	ds_read_b128 v[136:139], v175
	ds_read_b128 v[140:143], v175 offset:1024
	ds_read_b128 v[144:147], v175 offset:2048
	ds_read_b128 v[148:151], v175 offset:3072
	ds_read_b128 v[152:155], v176
	ds_read_b128 v[156:159], v176 offset:1024
	ds_read_b128 v[160:163], v176 offset:2048
	ds_read_b128 v[178:181], v176 offset:3072
	ds_read_b128 v[182:185], v174 offset:32768
	ds_read_b128 v[186:189], v174 offset:33792
	ds_read_b128 v[190:193], v174 offset:34816
	ds_read_b128 v[194:197], v174 offset:35840
	ds_read_b128 v[198:201], v174 offset:36864
	ds_read_b128 v[202:205], v174 offset:37888
	ds_read_b128 v[206:209], v174 offset:38912
	ds_read_b128 v[210:213], v174 offset:39936
	s_add_u32 s28, s25, 0x40100
	s_addc_u32 s29, s33, 0
	s_mov_b32 s25, m0
	s_mov_b32 m0, s85
	s_nop 2
	global_load_lds_dwordx4 v165, s[28:29]
	s_mov_b32 m0, s25
	s_mov_b32 s25, m0
	s_mov_b32 m0, s86
	s_nop 2
	global_load_lds_dwordx4 v167, s[28:29]
	s_mov_b32 m0, s25
	s_waitcnt vmcnt(8)
	s_waitcnt lgkmcnt(0)
	s_barrier
	s_setprio 1
	v_mfma_f32_16x16x32_bf16 v[26:29], v[136:139], v[182:185], v[26:29]
	v_mfma_f32_16x16x32_bf16 v[30:33], v[144:147], v[182:185], v[30:33]
	v_mfma_f32_16x16x32_bf16 v[50:53], v[136:139], v[190:193], v[50:53]
	v_mfma_f32_16x16x32_bf16 v[54:57], v[144:147], v[190:193], v[54:57]
	v_mfma_f32_16x16x32_bf16 v[74:77], v[136:139], v[198:201], v[74:77]
	v_mfma_f32_16x16x32_bf16 v[78:81], v[144:147], v[198:201], v[78:81]
	v_mfma_f32_16x16x32_bf16 v[94:97], v[136:139], v[206:209], v[94:97]
	v_mfma_f32_16x16x32_bf16 v[102:105], v[144:147], v[206:209], v[102:105]
	v_mfma_f32_16x16x32_bf16 v[26:29], v[140:143], v[186:189], v[26:29]
	v_mfma_f32_16x16x32_bf16 v[30:33], v[148:151], v[186:189], v[30:33]
	v_mfma_f32_16x16x32_bf16 v[50:53], v[140:143], v[194:197], v[50:53]
	v_mfma_f32_16x16x32_bf16 v[54:57], v[148:151], v[194:197], v[54:57]
	v_mfma_f32_16x16x32_bf16 v[74:77], v[140:143], v[202:205], v[74:77]
	v_mfma_f32_16x16x32_bf16 v[78:81], v[148:151], v[202:205], v[78:81]
	v_mfma_f32_16x16x32_bf16 v[94:97], v[140:143], v[210:213], v[94:97]
	v_mfma_f32_16x16x32_bf16 v[102:105], v[148:151], v[210:213], v[102:105]
	v_mfma_f32_16x16x32_bf16 v[38:41], v[152:155], v[182:185], v[38:41]
	v_mfma_f32_16x16x32_bf16 v[42:45], v[160:163], v[182:185], v[42:45]
	v_mfma_f32_16x16x32_bf16 v[62:65], v[152:155], v[190:193], v[62:65]
	v_mfma_f32_16x16x32_bf16 v[66:69], v[160:163], v[190:193], v[66:69]
	v_mfma_f32_16x16x32_bf16 v[82:85], v[152:155], v[198:201], v[82:85]
	v_mfma_f32_16x16x32_bf16 v[90:93], v[160:163], v[198:201], v[90:93]
	v_mfma_f32_16x16x32_bf16 v[106:109], v[152:155], v[206:209], v[106:109]
	v_mfma_f32_16x16x32_bf16 v[114:117], v[160:163], v[206:209], v[114:117]
	v_mfma_f32_16x16x32_bf16 v[38:41], v[156:159], v[186:189], v[38:41]
	v_mfma_f32_16x16x32_bf16 v[42:45], v[178:181], v[186:189], v[42:45]
	v_mfma_f32_16x16x32_bf16 v[62:65], v[156:159], v[194:197], v[62:65]
	v_mfma_f32_16x16x32_bf16 v[66:69], v[178:181], v[194:197], v[66:69]
	v_mfma_f32_16x16x32_bf16 v[82:85], v[156:159], v[202:205], v[82:85]
	v_mfma_f32_16x16x32_bf16 v[90:93], v[178:181], v[202:205], v[90:93]
	v_mfma_f32_16x16x32_bf16 v[106:109], v[156:159], v[210:213], v[106:109]
	v_mfma_f32_16x16x32_bf16 v[114:117], v[178:181], v[210:213], v[114:117]
	s_setprio 0
	s_barrier
	ds_read_b128 v[182:185], v174 offset:49152
	ds_read_b128 v[186:189], v174 offset:50176
	ds_read_b128 v[190:193], v174 offset:51200
	ds_read_b128 v[194:197], v174 offset:52224
	ds_read_b128 v[198:201], v174 offset:53248
	ds_read_b128 v[202:205], v174 offset:54272
	ds_read_b128 v[206:209], v174 offset:55296
	ds_read_b128 v[210:213], v174 offset:56320
	s_add_u32 s28, s23, 0x180
	s_addc_u32 s29, s24, 0
	s_mov_b32 s25, m0
	s_mov_b32 m0, s92
	s_nop 2
	global_load_lds_dwordx4 v166, s[28:29]
	s_mov_b32 m0, s25
	s_mov_b32 s25, m0
	s_mov_b32 m0, s93
	s_nop 2
	global_load_lds_dwordx4 v168, s[28:29]
	s_mov_b32 m0, s25
	s_add_u32 s28, s23, 0x40180
	s_addc_u32 s29, s24, 0
	s_mov_b32 s23, m0
	s_mov_b32 m0, s96
	s_nop 2
	global_load_lds_dwordx4 v166, s[28:29]
	s_mov_b32 m0, s23
	s_mov_b32 s23, m0
	s_mov_b32 m0, s97
	s_nop 2
	global_load_lds_dwordx4 v168, s[28:29]
	s_mov_b32 m0, s23
	s_mov_b32 s23, m0
	s_mov_b32 m0, s94
	s_nop 2
	global_load_lds_dwordx4 v165, s[58:59]
	s_mov_b32 m0, s23
	s_mov_b32 s23, m0
	s_mov_b32 m0, s95
	s_nop 2
	global_load_lds_dwordx4 v167, s[58:59]
	s_mov_b32 m0, s23
	s_waitcnt vmcnt(8)
	s_waitcnt lgkmcnt(0)
	s_barrier
	s_setprio 1
	v_mfma_f32_16x16x32_bf16 v[118:121], v[136:139], v[182:185], v[118:121]
	v_mfma_f32_16x16x32_bf16 v[126:129], v[144:147], v[182:185], v[126:129]
	v_mfma_f32_16x16x32_bf16 v[98:101], v[136:139], v[190:193], v[98:101]
	v_mfma_f32_16x16x32_bf16 v[86:89], v[144:147], v[190:193], v[86:89]
	v_mfma_f32_16x16x32_bf16 v[46:49], v[136:139], v[198:201], v[46:49]
	v_mfma_f32_16x16x32_bf16 v[34:37], v[144:147], v[198:201], v[34:37]
	v_mfma_f32_16x16x32_bf16 v[14:17], v[136:139], v[206:209], v[14:17]
	v_mfma_f32_16x16x32_bf16 v[10:13], v[144:147], v[206:209], v[10:13]
	v_mfma_f32_16x16x32_bf16 v[118:121], v[140:143], v[186:189], v[118:121]
	v_mfma_f32_16x16x32_bf16 v[126:129], v[148:151], v[186:189], v[126:129]
	v_mfma_f32_16x16x32_bf16 v[98:101], v[140:143], v[194:197], v[98:101]
	v_mfma_f32_16x16x32_bf16 v[86:89], v[148:151], v[194:197], v[86:89]
	v_mfma_f32_16x16x32_bf16 v[46:49], v[140:143], v[202:205], v[46:49]
	v_mfma_f32_16x16x32_bf16 v[34:37], v[148:151], v[202:205], v[34:37]
	v_mfma_f32_16x16x32_bf16 v[14:17], v[140:143], v[210:213], v[14:17]
	v_mfma_f32_16x16x32_bf16 v[10:13], v[148:151], v[210:213], v[10:13]
	v_mfma_f32_16x16x32_bf16 v[122:125], v[152:155], v[182:185], v[122:125]
	v_mfma_f32_16x16x32_bf16 v[110:113], v[160:163], v[182:185], v[110:113]
	v_mfma_f32_16x16x32_bf16 v[70:73], v[152:155], v[190:193], v[70:73]
	v_mfma_f32_16x16x32_bf16 v[58:61], v[160:163], v[190:193], v[58:61]
	v_mfma_f32_16x16x32_bf16 v[22:25], v[152:155], v[198:201], v[22:25]
	v_mfma_f32_16x16x32_bf16 v[18:21], v[160:163], v[198:201], v[18:21]
	v_mfma_f32_16x16x32_bf16 v[6:9], v[152:155], v[206:209], v[6:9]
	v_mfma_f32_16x16x32_bf16 v[2:5], v[160:163], v[206:209], v[2:5]
	v_mfma_f32_16x16x32_bf16 v[122:125], v[156:159], v[186:189], v[122:125]
	v_mfma_f32_16x16x32_bf16 v[110:113], v[178:181], v[186:189], v[110:113]
	v_mfma_f32_16x16x32_bf16 v[70:73], v[156:159], v[194:197], v[70:73]
	v_mfma_f32_16x16x32_bf16 v[58:61], v[178:181], v[194:197], v[58:61]
	v_mfma_f32_16x16x32_bf16 v[22:25], v[156:159], v[202:205], v[22:25]
	v_mfma_f32_16x16x32_bf16 v[18:21], v[178:181], v[202:205], v[18:21]
	v_mfma_f32_16x16x32_bf16 v[6:9], v[156:159], v[210:213], v[6:9]
	v_mfma_f32_16x16x32_bf16 v[2:5], v[178:181], v[210:213], v[2:5]
	s_setprio 0
	s_barrier
	s_add_i32 s3, s3, 2
	s_add_u32 s56, s56, 0x100
	s_addc_u32 s57, s57, 0
	s_cmp_gt_u32 s3, 5
	s_cbranch_scc0 .LBB0_1046
	s_ashr_i32 s55, s54, 31
	s_lshl_b64 s[24:25], s[54:55], 19
	s_add_u32 s56, s69, s24
	s_addc_u32 s57, s76, s25
	s_ashr_i32 s23, s22, 31
	s_lshl_b64 s[24:25], s[22:23], 19
	s_add_u32 s58, s77, s24
	s_addc_u32 s59, s78, s25
	s_lshl_b32 s3, s60, 18
	s_lshl_b32 s23, s2, 8
	s_lshl_b32 s32, s2, 16
	s_add_i32 s2, s32, s3
	v_lshrrev_b32_e32 v214, 6, v0
	v_lshlrev_b32_e32 v214, 13, v214
	v_and_b32_e32 v215, 63, v0
	v_lshl_add_u32 v214, v215, 3, v214
	v_add_u32_e32 v134, s2, v214
	s_cmp_lg_u32 s37, 0
	s_cbranch_scc1 .Lmpf_have
	global_load_dwordx2 v[162:163], v134, s[14:15]
	global_load_dwordx2 v[178:179], v134, s[16:17]
	v_or_b32_e32 v136, 0x200, v134
	v_add_u32_e32 v137, 0x400, v134
	v_add_u32_e32 v138, 0x600, v134
	v_add_u32_e32 v139, 0x800, v134
	v_add_u32_e32 v140, 0xa00, v134
	v_add_u32_e32 v141, 0xc00, v134
	v_add_u32_e32 v161, 0xe00, v134
	global_load_dwordx2 v[180:181], v136, s[14:15]
	global_load_dwordx2 v[182:183], v136, s[16:17]
	global_load_dwordx2 v[158:159], v137, s[14:15]
	global_load_dwordx2 v[156:157], v137, s[16:17]
	global_load_dwordx2 v[154:155], v138, s[14:15]
	global_load_dwordx2 v[152:153], v138, s[16:17]
	global_load_dwordx2 v[150:151], v139, s[14:15]
	global_load_dwordx2 v[148:149], v139, s[16:17]
	global_load_dwordx2 v[146:147], v140, s[14:15]
	global_load_dwordx2 v[144:145], v140, s[16:17]
	global_load_dwordx2 v[142:143], v141, s[14:15]
	s_nop 0
	global_load_dwordx2 v[140:141], v141, s[16:17]
	s_nop 0
	global_load_dwordx2 v[138:139], v161, s[14:15]
	global_load_dwordx2 v[136:137], v161, s[16:17]
	s_branch .Lmpf_join

.LBB0_1048:
	ds_read_b128 v[136:139], v172
	ds_read_b128 v[140:143], v172 offset:1024
	ds_read_b128 v[144:147], v172 offset:2048
	ds_read_b128 v[148:151], v172 offset:3072
	ds_read_b128 v[152:155], v173
	ds_read_b128 v[156:159], v173 offset:1024
	ds_read_b128 v[160:163], v173 offset:2048
	ds_read_b128 v[178:181], v173 offset:3072
	s_cmp_eq_u32 s33, 12
	s_cselect_b32 s66, s3, s28
	s_cselect_b32 s67, s2, s29
	s_cselect_b32 s64, s25, s30
	s_cselect_b32 s65, s24, s31
	s_add_u32 s62, s66, 0x80
	s_addc_u32 s63, s67, 0
	ds_read_b128 v[182:185], v174
	ds_read_b128 v[186:189], v174 offset:1024
	ds_read_b128 v[190:193], v174 offset:2048
	ds_read_b128 v[194:197], v174 offset:3072
	ds_read_b128 v[198:201], v174 offset:4096
	ds_read_b128 v[202:205], v174 offset:5120
	ds_read_b128 v[206:209], v174 offset:6144
	ds_read_b128 v[210:213], v174 offset:7168
	s_add_u32 s36, s28, 0x3ff80
	s_addc_u32 s37, s29, 0
	s_mov_b32 s52, m0
	s_mov_b32 m0, s26
	s_nop 2
	global_load_lds_dwordx4 v165, s[36:37]
	s_mov_b32 m0, s52
	s_mov_b32 s52, m0
	s_mov_b32 m0, s27
	s_nop 2
	global_load_lds_dwordx4 v167, s[36:37]
	s_mov_b32 m0, s52
	s_waitcnt vmcnt(8)
	s_waitcnt lgkmcnt(0)
	s_barrier
	s_setprio 1
	v_mfma_f32_16x16x32_bf16 v[26:29], v[136:139], v[182:185], v[26:29]
	v_mfma_f32_16x16x32_bf16 v[30:33], v[144:147], v[182:185], v[30:33]
	v_mfma_f32_16x16x32_bf16 v[50:53], v[136:139], v[190:193], v[50:53]
	v_mfma_f32_16x16x32_bf16 v[54:57], v[144:147], v[190:193], v[54:57]
	v_mfma_f32_16x16x32_bf16 v[74:77], v[136:139], v[198:201], v[74:77]
	v_mfma_f32_16x16x32_bf16 v[78:81], v[144:147], v[198:201], v[78:81]
	v_mfma_f32_16x16x32_bf16 v[94:97], v[136:139], v[206:209], v[94:97]
	v_mfma_f32_16x16x32_bf16 v[102:105], v[144:147], v[206:209], v[102:105]
	v_mfma_f32_16x16x32_bf16 v[26:29], v[140:143], v[186:189], v[26:29]
	v_mfma_f32_16x16x32_bf16 v[30:33], v[148:151], v[186:189], v[30:33]
	v_mfma_f32_16x16x32_bf16 v[50:53], v[140:143], v[194:197], v[50:53]
	v_mfma_f32_16x16x32_bf16 v[54:57], v[148:151], v[194:197], v[54:57]
	v_mfma_f32_16x16x32_bf16 v[74:77], v[140:143], v[202:205], v[74:77]
	v_mfma_f32_16x16x32_bf16 v[78:81], v[148:151], v[202:205], v[78:81]
	v_mfma_f32_16x16x32_bf16 v[94:97], v[140:143], v[210:213], v[94:97]
	v_mfma_f32_16x16x32_bf16 v[102:105], v[148:151], v[210:213], v[102:105]
	v_mfma_f32_16x16x32_bf16 v[38:41], v[152:155], v[182:185], v[38:41]
	v_mfma_f32_16x16x32_bf16 v[42:45], v[160:163], v[182:185], v[42:45]
	v_mfma_f32_16x16x32_bf16 v[62:65], v[152:155], v[190:193], v[62:65]
	v_mfma_f32_16x16x32_bf16 v[66:69], v[160:163], v[190:193], v[66:69]
	v_mfma_f32_16x16x32_bf16 v[82:85], v[152:155], v[198:201], v[82:85]
	v_mfma_f32_16x16x32_bf16 v[90:93], v[160:163], v[198:201], v[90:93]
	v_mfma_f32_16x16x32_bf16 v[106:109], v[152:155], v[206:209], v[106:109]
	v_mfma_f32_16x16x32_bf16 v[114:117], v[160:163], v[206:209], v[114:117]
	v_mfma_f32_16x16x32_bf16 v[38:41], v[156:159], v[186:189], v[38:41]
	v_mfma_f32_16x16x32_bf16 v[42:45], v[178:181], v[186:189], v[42:45]
	v_mfma_f32_16x16x32_bf16 v[62:65], v[156:159], v[194:197], v[62:65]
	v_mfma_f32_16x16x32_bf16 v[66:69], v[178:181], v[194:197], v[66:69]
	v_mfma_f32_16x16x32_bf16 v[82:85], v[156:159], v[202:205], v[82:85]
	v_mfma_f32_16x16x32_bf16 v[90:93], v[178:181], v[202:205], v[90:93]
	v_mfma_f32_16x16x32_bf16 v[106:109], v[156:159], v[210:213], v[106:109]
	v_mfma_f32_16x16x32_bf16 v[114:117], v[178:181], v[210:213], v[114:117]
	s_setprio 0
	s_barrier
	ds_read_b128 v[182:185], v174 offset:16384
	ds_read_b128 v[186:189], v174 offset:17408
	ds_read_b128 v[190:193], v174 offset:18432
	ds_read_b128 v[194:197], v174 offset:19456
	ds_read_b128 v[198:201], v174 offset:20480
	ds_read_b128 v[202:205], v174 offset:21504
	ds_read_b128 v[206:209], v174 offset:22528
	ds_read_b128 v[210:213], v174 offset:23552
	s_mov_b32 s36, m0
	s_mov_b32 m0, s80
	s_nop 2
	global_load_lds_dwordx4 v166, s[64:65]
	s_mov_b32 m0, s36
	s_mov_b32 s36, m0
	s_mov_b32 m0, s81
	s_nop 2
	global_load_lds_dwordx4 v168, s[64:65]
	s_mov_b32 m0, s36
	s_add_u32 s36, s64, 0x40000
	s_addc_u32 s37, s65, 0
	s_mov_b32 s52, m0
	s_mov_b32 m0, s82
	s_nop 2
	global_load_lds_dwordx4 v166, s[36:37]
	s_mov_b32 m0, s52
	s_mov_b32 s52, m0
	s_mov_b32 m0, s83
	s_nop 2
	global_load_lds_dwordx4 v168, s[36:37]
	s_mov_b32 m0, s52
	s_mov_b32 s36, m0
	s_mov_b32 m0, s79
	s_nop 2
	global_load_lds_dwordx4 v165, s[66:67]
	s_mov_b32 m0, s36
	s_mov_b32 s36, m0
	s_mov_b32 m0, s84
	s_nop 2
	global_load_lds_dwordx4 v167, s[66:67]
	s_mov_b32 m0, s36
	s_waitcnt vmcnt(8)
	s_waitcnt lgkmcnt(0)
	s_barrier
	s_setprio 1
	v_mfma_f32_16x16x32_bf16 v[118:121], v[136:139], v[182:185], v[118:121]
	v_mfma_f32_16x16x32_bf16 v[126:129], v[144:147], v[182:185], v[126:129]
	v_mfma_f32_16x16x32_bf16 v[98:101], v[136:139], v[190:193], v[98:101]
	v_mfma_f32_16x16x32_bf16 v[86:89], v[144:147], v[190:193], v[86:89]
	v_mfma_f32_16x16x32_bf16 v[46:49], v[136:139], v[198:201], v[46:49]
	v_mfma_f32_16x16x32_bf16 v[34:37], v[144:147], v[198:201], v[34:37]
	v_mfma_f32_16x16x32_bf16 v[14:17], v[136:139], v[206:209], v[14:17]
	v_mfma_f32_16x16x32_bf16 v[10:13], v[144:147], v[206:209], v[10:13]
	v_mfma_f32_16x16x32_bf16 v[118:121], v[140:143], v[186:189], v[118:121]
	v_mfma_f32_16x16x32_bf16 v[126:129], v[148:151], v[186:189], v[126:129]
	v_mfma_f32_16x16x32_bf16 v[98:101], v[140:143], v[194:197], v[98:101]
	v_mfma_f32_16x16x32_bf16 v[86:89], v[148:151], v[194:197], v[86:89]
	v_mfma_f32_16x16x32_bf16 v[46:49], v[140:143], v[202:205], v[46:49]
	v_mfma_f32_16x16x32_bf16 v[34:37], v[148:151], v[202:205], v[34:37]
	v_mfma_f32_16x16x32_bf16 v[14:17], v[140:143], v[210:213], v[14:17]
	v_mfma_f32_16x16x32_bf16 v[10:13], v[148:151], v[210:213], v[10:13]
	v_mfma_f32_16x16x32_bf16 v[122:125], v[152:155], v[182:185], v[122:125]
	v_mfma_f32_16x16x32_bf16 v[110:113], v[160:163], v[182:185], v[110:113]
	v_mfma_f32_16x16x32_bf16 v[70:73], v[152:155], v[190:193], v[70:73]
	v_mfma_f32_16x16x32_bf16 v[58:61], v[160:163], v[190:193], v[58:61]
	v_mfma_f32_16x16x32_bf16 v[22:25], v[152:155], v[198:201], v[22:25]
	v_mfma_f32_16x16x32_bf16 v[18:21], v[160:163], v[198:201], v[18:21]
	v_mfma_f32_16x16x32_bf16 v[6:9], v[152:155], v[206:209], v[6:9]
	v_mfma_f32_16x16x32_bf16 v[2:5], v[160:163], v[206:209], v[2:5]
	v_mfma_f32_16x16x32_bf16 v[122:125], v[156:159], v[186:189], v[122:125]
	v_mfma_f32_16x16x32_bf16 v[110:113], v[178:181], v[186:189], v[110:113]
	v_mfma_f32_16x16x32_bf16 v[70:73], v[156:159], v[194:197], v[70:73]
	v_mfma_f32_16x16x32_bf16 v[58:61], v[178:181], v[194:197], v[58:61]
	v_mfma_f32_16x16x32_bf16 v[22:25], v[156:159], v[202:205], v[22:25]
	v_mfma_f32_16x16x32_bf16 v[18:21], v[178:181], v[202:205], v[18:21]
	v_mfma_f32_16x16x32_bf16 v[6:9], v[156:159], v[210:213], v[6:9]
	v_mfma_f32_16x16x32_bf16 v[2:5], v[178:181], v[210:213], v[2:5]
	s_setprio 0
	s_barrier
	ds_read_b128 v[136:139], v175
	ds_read_b128 v[140:143], v175 offset:1024
	ds_read_b128 v[144:147], v175 offset:2048
	ds_read_b128 v[148:151], v175 offset:3072
	ds_read_b128 v[152:155], v176
	ds_read_b128 v[156:159], v176 offset:1024
	ds_read_b128 v[160:163], v176 offset:2048
	ds_read_b128 v[178:181], v176 offset:3072
	ds_read_b128 v[182:185], v174 offset:32768
	ds_read_b128 v[186:189], v174 offset:33792
	ds_read_b128 v[190:193], v174 offset:34816
	ds_read_b128 v[194:197], v174 offset:35840
	ds_read_b128 v[198:201], v174 offset:36864
	ds_read_b128 v[202:205], v174 offset:37888
	ds_read_b128 v[206:209], v174 offset:38912
	ds_read_b128 v[210:213], v174 offset:39936
	s_add_u32 s36, s66, 0x40000
	s_addc_u32 s37, s67, 0
	s_mov_b32 s52, m0
	s_mov_b32 m0, s85
	s_nop 2
	global_load_lds_dwordx4 v165, s[36:37]
	s_mov_b32 m0, s52
	s_mov_b32 s52, m0
	s_mov_b32 m0, s86
	s_nop 2
	global_load_lds_dwordx4 v167, s[36:37]
	s_mov_b32 m0, s52
	s_waitcnt vmcnt(8)
	s_waitcnt lgkmcnt(0)
	s_barrier
	s_setprio 1
	v_mfma_f32_16x16x32_bf16 v[26:29], v[136:139], v[182:185], v[26:29]
	v_mfma_f32_16x16x32_bf16 v[30:33], v[144:147], v[182:185], v[30:33]
	v_mfma_f32_16x16x32_bf16 v[50:53], v[136:139], v[190:193], v[50:53]
	v_mfma_f32_16x16x32_bf16 v[54:57], v[144:147], v[190:193], v[54:57]
	v_mfma_f32_16x16x32_bf16 v[74:77], v[136:139], v[198:201], v[74:77]
	v_mfma_f32_16x16x32_bf16 v[78:81], v[144:147], v[198:201], v[78:81]
	v_mfma_f32_16x16x32_bf16 v[94:97], v[136:139], v[206:209], v[94:97]
	v_mfma_f32_16x16x32_bf16 v[102:105], v[144:147], v[206:209], v[102:105]
	v_mfma_f32_16x16x32_bf16 v[26:29], v[140:143], v[186:189], v[26:29]
	v_mfma_f32_16x16x32_bf16 v[30:33], v[148:151], v[186:189], v[30:33]
	v_mfma_f32_16x16x32_bf16 v[50:53], v[140:143], v[194:197], v[50:53]
	v_mfma_f32_16x16x32_bf16 v[54:57], v[148:151], v[194:197], v[54:57]
	v_mfma_f32_16x16x32_bf16 v[74:77], v[140:143], v[202:205], v[74:77]
	v_mfma_f32_16x16x32_bf16 v[78:81], v[148:151], v[202:205], v[78:81]
	v_mfma_f32_16x16x32_bf16 v[94:97], v[140:143], v[210:213], v[94:97]
	v_mfma_f32_16x16x32_bf16 v[102:105], v[148:151], v[210:213], v[102:105]
	v_mfma_f32_16x16x32_bf16 v[38:41], v[152:155], v[182:185], v[38:41]
	v_mfma_f32_16x16x32_bf16 v[42:45], v[160:163], v[182:185], v[42:45]
	v_mfma_f32_16x16x32_bf16 v[62:65], v[152:155], v[190:193], v[62:65]
	v_mfma_f32_16x16x32_bf16 v[66:69], v[160:163], v[190:193], v[66:69]
	v_mfma_f32_16x16x32_bf16 v[82:85], v[152:155], v[198:201], v[82:85]
	v_mfma_f32_16x16x32_bf16 v[90:93], v[160:163], v[198:201], v[90:93]
	v_mfma_f32_16x16x32_bf16 v[106:109], v[152:155], v[206:209], v[106:109]
	v_mfma_f32_16x16x32_bf16 v[114:117], v[160:163], v[206:209], v[114:117]
	v_mfma_f32_16x16x32_bf16 v[38:41], v[156:159], v[186:189], v[38:41]
	v_mfma_f32_16x16x32_bf16 v[42:45], v[178:181], v[186:189], v[42:45]
	v_mfma_f32_16x16x32_bf16 v[62:65], v[156:159], v[194:197], v[62:65]
	v_mfma_f32_16x16x32_bf16 v[66:69], v[178:181], v[194:197], v[66:69]
	v_mfma_f32_16x16x32_bf16 v[82:85], v[156:159], v[202:205], v[82:85]
	v_mfma_f32_16x16x32_bf16 v[90:93], v[178:181], v[202:205], v[90:93]
	v_mfma_f32_16x16x32_bf16 v[106:109], v[156:159], v[210:213], v[106:109]
	v_mfma_f32_16x16x32_bf16 v[114:117], v[178:181], v[210:213], v[114:117]
	s_setprio 0
	s_barrier
	ds_read_b128 v[182:185], v174 offset:49152
	ds_read_b128 v[186:189], v174 offset:50176
	ds_read_b128 v[190:193], v174 offset:51200
	ds_read_b128 v[194:197], v174 offset:52224
	ds_read_b128 v[198:201], v174 offset:53248
	ds_read_b128 v[202:205], v174 offset:54272
	ds_read_b128 v[206:209], v174 offset:55296
	ds_read_b128 v[210:213], v174 offset:56320
	s_add_u32 s36, s64, 0x80
	s_addc_u32 s37, s65, 0
	s_mov_b32 s52, m0
	s_mov_b32 m0, s92
	s_nop 2
	global_load_lds_dwordx4 v166, s[36:37]
	s_mov_b32 m0, s52
	s_mov_b32 s52, m0
	s_mov_b32 m0, s93
	s_nop 2
	global_load_lds_dwordx4 v168, s[36:37]
	s_mov_b32 m0, s52
	s_add_u32 s36, s64, 0x40080
	s_addc_u32 s37, s65, 0
	s_mov_b32 s52, m0
	s_mov_b32 m0, s96
	s_nop 2
	global_load_lds_dwordx4 v166, s[36:37]
	s_mov_b32 m0, s52
	s_mov_b32 s52, m0
	s_mov_b32 m0, s97
	s_nop 2
	global_load_lds_dwordx4 v168, s[36:37]
	s_mov_b32 m0, s52
	s_mov_b32 s36, m0
	s_mov_b32 m0, s94
	s_nop 2
	global_load_lds_dwordx4 v165, s[62:63]
	s_mov_b32 m0, s36
	s_mov_b32 s36, m0
	s_mov_b32 m0, s95
	s_nop 2
	global_load_lds_dwordx4 v167, s[62:63]
	s_mov_b32 m0, s36
	s_waitcnt vmcnt(8)
	s_waitcnt lgkmcnt(0)
	s_barrier
	s_setprio 1
	v_mfma_f32_16x16x32_bf16 v[118:121], v[136:139], v[182:185], v[118:121]
	v_mfma_f32_16x16x32_bf16 v[126:129], v[144:147], v[182:185], v[126:129]
	v_mfma_f32_16x16x32_bf16 v[98:101], v[136:139], v[190:193], v[98:101]
	v_mfma_f32_16x16x32_bf16 v[86:89], v[144:147], v[190:193], v[86:89]
	v_mfma_f32_16x16x32_bf16 v[46:49], v[136:139], v[198:201], v[46:49]
	v_mfma_f32_16x16x32_bf16 v[34:37], v[144:147], v[198:201], v[34:37]
	v_mfma_f32_16x16x32_bf16 v[14:17], v[136:139], v[206:209], v[14:17]
	v_mfma_f32_16x16x32_bf16 v[10:13], v[144:147], v[206:209], v[10:13]
	v_mfma_f32_16x16x32_bf16 v[118:121], v[140:143], v[186:189], v[118:121]
	v_mfma_f32_16x16x32_bf16 v[126:129], v[148:151], v[186:189], v[126:129]
	v_mfma_f32_16x16x32_bf16 v[98:101], v[140:143], v[194:197], v[98:101]
	v_mfma_f32_16x16x32_bf16 v[86:89], v[148:151], v[194:197], v[86:89]
	v_mfma_f32_16x16x32_bf16 v[46:49], v[140:143], v[202:205], v[46:49]
	v_mfma_f32_16x16x32_bf16 v[34:37], v[148:151], v[202:205], v[34:37]
	v_mfma_f32_16x16x32_bf16 v[14:17], v[140:143], v[210:213], v[14:17]
	v_mfma_f32_16x16x32_bf16 v[10:13], v[148:151], v[210:213], v[10:13]
	v_mfma_f32_16x16x32_bf16 v[122:125], v[152:155], v[182:185], v[122:125]
	v_mfma_f32_16x16x32_bf16 v[110:113], v[160:163], v[182:185], v[110:113]
	v_mfma_f32_16x16x32_bf16 v[70:73], v[152:155], v[190:193], v[70:73]
	v_mfma_f32_16x16x32_bf16 v[58:61], v[160:163], v[190:193], v[58:61]
	v_mfma_f32_16x16x32_bf16 v[22:25], v[152:155], v[198:201], v[22:25]
	v_mfma_f32_16x16x32_bf16 v[18:21], v[160:163], v[198:201], v[18:21]
	v_mfma_f32_16x16x32_bf16 v[6:9], v[152:155], v[206:209], v[6:9]
	v_mfma_f32_16x16x32_bf16 v[2:5], v[160:163], v[206:209], v[2:5]
	v_mfma_f32_16x16x32_bf16 v[122:125], v[156:159], v[186:189], v[122:125]
	v_mfma_f32_16x16x32_bf16 v[110:113], v[178:181], v[186:189], v[110:113]
	v_mfma_f32_16x16x32_bf16 v[70:73], v[156:159], v[194:197], v[70:73]
	v_mfma_f32_16x16x32_bf16 v[58:61], v[178:181], v[194:197], v[58:61]
	v_mfma_f32_16x16x32_bf16 v[22:25], v[156:159], v[202:205], v[22:25]
	v_mfma_f32_16x16x32_bf16 v[18:21], v[178:181], v[202:205], v[18:21]
	v_mfma_f32_16x16x32_bf16 v[6:9], v[156:159], v[210:213], v[6:9]
	v_mfma_f32_16x16x32_bf16 v[2:5], v[178:181], v[210:213], v[2:5]
	s_setprio 0
	s_barrier
	s_add_i32 s33, s33, 2
	s_add_u32 s28, s28, 0x100
	s_addc_u32 s29, s29, 0
	s_add_u32 s30, s30, 0x100
	s_addc_u32 s31, s31, 0
	s_cmp_lt_u32 s33, 14
	s_cbranch_scc1 .LBB0_1048
	s_and_b64 vcc, exec, s[20:21]
	s_cbranch_vccz .LBB0_1051
	s_barrier

.Lpeel1440:
	ds_read_b128 v[130:133], v234
	ds_read_b128 v[134:137], v234 offset:1024
	ds_read_b128 v[138:141], v234 offset:2048
	ds_read_b128 v[142:145], v234 offset:3072
	ds_read_b128 v[146:149], v235
	ds_read_b128 v[150:153], v235 offset:1024
	ds_read_b128 v[154:157], v235 offset:2048
	ds_read_b128 v[158:161], v235 offset:3072
	s_add_u32 s60, s58, 0x100
	s_addc_u32 s61, s59, 0
	s_cmp_eq_u32 s87, 12
	s_cselect_b32 s66, s33, s60
	s_cselect_b32 s67, s21, s61
	s_cselect_b32 s64, s84, s85
	s_cselect_b32 s65, s19, s86
	s_add_u32 s62, s66, 0x80
	s_addc_u32 s63, s67, 0
	ds_read_b128 v[162:165], v236
	ds_read_b128 v[166:169], v236 offset:1024
	ds_read_b128 v[170:173], v236 offset:2048
	ds_read_b128 v[174:177], v236 offset:3072
	ds_read_b128 v[178:181], v236 offset:4096
	ds_read_b128 v[182:185], v236 offset:5120
	ds_read_b128 v[186:189], v236 offset:6144
	ds_read_b128 v[190:193], v236 offset:7168
	s_add_u32 s58, s58, 0x40080
	s_addc_u32 s59, s59, 0
	s_mov_b32 s88, m0
	s_mov_b32 m0, s80
	s_nop 2
	global_load_lds_dwordx4 v228, s[58:59]
	s_mov_b32 m0, s88
	s_mov_b32 s88, m0
	s_mov_b32 m0, s81
	s_nop 2
	global_load_lds_dwordx4 v230, s[58:59]
	s_mov_b32 m0, s88
	s_waitcnt vmcnt(8)
	s_waitcnt lgkmcnt(0)
	s_barrier
	s_setprio 1
	v_mfma_f32_16x16x32_bf16 v[126:129], v[130:133], v[162:165], 0
	v_mfma_f32_16x16x32_bf16 v[122:125], v[138:141], v[162:165], 0
	v_mfma_f32_16x16x32_bf16 v[114:117], v[130:133], v[170:173], 0
	v_mfma_f32_16x16x32_bf16 v[106:109], v[138:141], v[170:173], 0
	v_mfma_f32_16x16x32_bf16 v[94:97], v[130:133], v[178:181], 0
	v_mfma_f32_16x16x32_bf16 v[90:93], v[138:141], v[178:181], 0
	v_mfma_f32_16x16x32_bf16 v[86:89], v[130:133], v[186:189], 0
	v_mfma_f32_16x16x32_bf16 v[78:81], v[138:141], v[186:189], 0
	v_mfma_f32_16x16x32_bf16 v[126:129], v[134:137], v[166:169], v[126:129]
	v_mfma_f32_16x16x32_bf16 v[122:125], v[142:145], v[166:169], v[122:125]
	v_mfma_f32_16x16x32_bf16 v[114:117], v[134:137], v[174:177], v[114:117]
	v_mfma_f32_16x16x32_bf16 v[106:109], v[142:145], v[174:177], v[106:109]
	v_mfma_f32_16x16x32_bf16 v[94:97], v[134:137], v[182:185], v[94:97]
	v_mfma_f32_16x16x32_bf16 v[90:93], v[142:145], v[182:185], v[90:93]
	v_mfma_f32_16x16x32_bf16 v[86:89], v[134:137], v[190:193], v[86:89]
	v_mfma_f32_16x16x32_bf16 v[78:81], v[142:145], v[190:193], v[78:81]
	v_mfma_f32_16x16x32_bf16 v[118:121], v[146:149], v[162:165], 0
	v_mfma_f32_16x16x32_bf16 v[110:113], v[154:157], v[162:165], 0
	v_mfma_f32_16x16x32_bf16 v[102:105], v[146:149], v[170:173], 0
	v_mfma_f32_16x16x32_bf16 v[98:101], v[154:157], v[170:173], 0
	v_mfma_f32_16x16x32_bf16 v[82:85], v[146:149], v[178:181], 0
	v_mfma_f32_16x16x32_bf16 v[74:77], v[154:157], v[178:181], 0
	v_mfma_f32_16x16x32_bf16 v[70:73], v[146:149], v[186:189], 0
	v_mfma_f32_16x16x32_bf16 v[66:69], v[154:157], v[186:189], 0
	v_mfma_f32_16x16x32_bf16 v[118:121], v[150:153], v[166:169], v[118:121]
	v_mfma_f32_16x16x32_bf16 v[110:113], v[158:161], v[166:169], v[110:113]
	v_mfma_f32_16x16x32_bf16 v[102:105], v[150:153], v[174:177], v[102:105]
	v_mfma_f32_16x16x32_bf16 v[98:101], v[158:161], v[174:177], v[98:101]
	v_mfma_f32_16x16x32_bf16 v[82:85], v[150:153], v[182:185], v[82:85]
	v_mfma_f32_16x16x32_bf16 v[74:77], v[158:161], v[182:185], v[74:77]
	v_mfma_f32_16x16x32_bf16 v[70:73], v[150:153], v[190:193], v[70:73]
	v_mfma_f32_16x16x32_bf16 v[66:69], v[158:161], v[190:193], v[66:69]
	s_setprio 0
	s_barrier
	ds_read_b128 v[162:165], v236 offset:16384
	ds_read_b128 v[166:169], v236 offset:17408
	ds_read_b128 v[170:173], v236 offset:18432
	ds_read_b128 v[174:177], v236 offset:19456
	ds_read_b128 v[178:181], v236 offset:20480
	ds_read_b128 v[182:185], v236 offset:21504
	ds_read_b128 v[186:189], v236 offset:22528
	ds_read_b128 v[190:193], v236 offset:23552
	s_mov_b32 s58, m0
	s_mov_b32 m0, s30
	s_nop 2
	global_load_lds_dwordx4 v229, s[64:65]
	s_mov_b32 m0, s58
	s_mov_b32 s58, m0
	s_mov_b32 m0, s31
	s_nop 2
	global_load_lds_dwordx4 v231, s[64:65]
	s_mov_b32 m0, s58
	s_add_u32 s58, s64, 0x40000
	s_addc_u32 s59, s65, 0
	s_mov_b32 s88, m0
	s_mov_b32 m0, s34
	s_nop 2
	global_load_lds_dwordx4 v229, s[58:59]
	s_mov_b32 m0, s88
	s_mov_b32 s88, m0
	s_mov_b32 m0, s35
	s_nop 2
	global_load_lds_dwordx4 v231, s[58:59]
	s_mov_b32 m0, s88
	s_mov_b32 s58, m0
	s_mov_b32 m0, s28
	s_nop 2
	global_load_lds_dwordx4 v228, s[66:67]
	s_mov_b32 m0, s58
	s_mov_b32 s58, m0
	s_mov_b32 m0, s36
	s_nop 2
	global_load_lds_dwordx4 v230, s[66:67]
	s_mov_b32 m0, s58
	s_waitcnt vmcnt(8)
	s_waitcnt lgkmcnt(0)
	s_barrier
	s_setprio 1
	v_mfma_f32_16x16x32_bf16 v[62:65], v[130:133], v[162:165], 0
	v_mfma_f32_16x16x32_bf16 v[58:61], v[138:141], v[162:165], 0
	v_mfma_f32_16x16x32_bf16 v[54:57], v[130:133], v[170:173], 0
	v_mfma_f32_16x16x32_bf16 v[46:49], v[138:141], v[170:173], 0
	v_mfma_f32_16x16x32_bf16 v[38:41], v[130:133], v[178:181], 0
	v_mfma_f32_16x16x32_bf16 v[30:33], v[138:141], v[178:181], 0
	v_mfma_f32_16x16x32_bf16 v[22:25], v[130:133], v[186:189], 0
	v_mfma_f32_16x16x32_bf16 v[14:17], v[138:141], v[186:189], 0
	v_mfma_f32_16x16x32_bf16 v[62:65], v[134:137], v[166:169], v[62:65]
	v_mfma_f32_16x16x32_bf16 v[58:61], v[142:145], v[166:169], v[58:61]
	v_mfma_f32_16x16x32_bf16 v[54:57], v[134:137], v[174:177], v[54:57]
	v_mfma_f32_16x16x32_bf16 v[46:49], v[142:145], v[174:177], v[46:49]
	v_mfma_f32_16x16x32_bf16 v[38:41], v[134:137], v[182:185], v[38:41]
	v_mfma_f32_16x16x32_bf16 v[30:33], v[142:145], v[182:185], v[30:33]
	v_mfma_f32_16x16x32_bf16 v[22:25], v[134:137], v[190:193], v[22:25]
	v_mfma_f32_16x16x32_bf16 v[14:17], v[142:145], v[190:193], v[14:17]
	v_mfma_f32_16x16x32_bf16 v[50:53], v[146:149], v[162:165], 0
	v_mfma_f32_16x16x32_bf16 v[42:45], v[154:157], v[162:165], 0
	v_mfma_f32_16x16x32_bf16 v[34:37], v[146:149], v[170:173], 0
	v_mfma_f32_16x16x32_bf16 v[26:29], v[154:157], v[170:173], 0
	v_mfma_f32_16x16x32_bf16 v[18:21], v[146:149], v[178:181], 0
	v_mfma_f32_16x16x32_bf16 v[10:13], v[154:157], v[178:181], 0
	v_mfma_f32_16x16x32_bf16 v[6:9], v[146:149], v[186:189], 0
	v_mfma_f32_16x16x32_bf16 v[2:5], v[154:157], v[186:189], 0
	v_mfma_f32_16x16x32_bf16 v[50:53], v[150:153], v[166:169], v[50:53]
	v_mfma_f32_16x16x32_bf16 v[42:45], v[158:161], v[166:169], v[42:45]
	v_mfma_f32_16x16x32_bf16 v[34:37], v[150:153], v[174:177], v[34:37]
	v_mfma_f32_16x16x32_bf16 v[26:29], v[158:161], v[174:177], v[26:29]
	v_mfma_f32_16x16x32_bf16 v[18:21], v[150:153], v[182:185], v[18:21]
	v_mfma_f32_16x16x32_bf16 v[10:13], v[158:161], v[182:185], v[10:13]
	v_mfma_f32_16x16x32_bf16 v[6:9], v[150:153], v[190:193], v[6:9]
	v_mfma_f32_16x16x32_bf16 v[2:5], v[158:161], v[190:193], v[2:5]
	s_setprio 0
	s_barrier
	s_branch .Lmid1440
.LBB0_1440:
	ds_read_b128 v[130:133], v234
	ds_read_b128 v[134:137], v234 offset:1024
	ds_read_b128 v[138:141], v234 offset:2048
	ds_read_b128 v[142:145], v234 offset:3072
	ds_read_b128 v[146:149], v235
	ds_read_b128 v[150:153], v235 offset:1024
	ds_read_b128 v[154:157], v235 offset:2048
	ds_read_b128 v[158:161], v235 offset:3072
	s_add_u32 s60, s58, 0x100
	s_addc_u32 s61, s59, 0
	s_cmp_eq_u32 s87, 12
	s_cselect_b32 s66, s33, s60
	s_cselect_b32 s67, s21, s61
	s_cselect_b32 s64, s84, s85
	s_cselect_b32 s65, s19, s86
	s_add_u32 s62, s66, 0x80
	s_addc_u32 s63, s67, 0
	ds_read_b128 v[162:165], v236
	ds_read_b128 v[166:169], v236 offset:1024
	ds_read_b128 v[170:173], v236 offset:2048
	ds_read_b128 v[174:177], v236 offset:3072
	ds_read_b128 v[178:181], v236 offset:4096
	ds_read_b128 v[182:185], v236 offset:5120
	ds_read_b128 v[186:189], v236 offset:6144
	ds_read_b128 v[190:193], v236 offset:7168
	s_add_u32 s58, s58, 0x40080
	s_addc_u32 s59, s59, 0
	s_mov_b32 s88, m0
	s_mov_b32 m0, s80
	s_nop 2
	global_load_lds_dwordx4 v228, s[58:59]
	s_mov_b32 m0, s88
	s_mov_b32 s88, m0
	s_mov_b32 m0, s81
	s_nop 2
	global_load_lds_dwordx4 v230, s[58:59]
	s_mov_b32 m0, s88
	s_waitcnt vmcnt(8)
	s_waitcnt lgkmcnt(0)
	s_barrier
	s_setprio 1
	v_mfma_f32_16x16x32_bf16 v[126:129], v[130:133], v[162:165], v[126:129]
	v_mfma_f32_16x16x32_bf16 v[122:125], v[138:141], v[162:165], v[122:125]
	v_mfma_f32_16x16x32_bf16 v[114:117], v[130:133], v[170:173], v[114:117]
	v_mfma_f32_16x16x32_bf16 v[106:109], v[138:141], v[170:173], v[106:109]
	v_mfma_f32_16x16x32_bf16 v[94:97], v[130:133], v[178:181], v[94:97]
	v_mfma_f32_16x16x32_bf16 v[90:93], v[138:141], v[178:181], v[90:93]
	v_mfma_f32_16x16x32_bf16 v[86:89], v[130:133], v[186:189], v[86:89]
	v_mfma_f32_16x16x32_bf16 v[78:81], v[138:141], v[186:189], v[78:81]
	v_mfma_f32_16x16x32_bf16 v[126:129], v[134:137], v[166:169], v[126:129]
	v_mfma_f32_16x16x32_bf16 v[122:125], v[142:145], v[166:169], v[122:125]
	v_mfma_f32_16x16x32_bf16 v[114:117], v[134:137], v[174:177], v[114:117]
	v_mfma_f32_16x16x32_bf16 v[106:109], v[142:145], v[174:177], v[106:109]
	v_mfma_f32_16x16x32_bf16 v[94:97], v[134:137], v[182:185], v[94:97]
	v_mfma_f32_16x16x32_bf16 v[90:93], v[142:145], v[182:185], v[90:93]
	v_mfma_f32_16x16x32_bf16 v[86:89], v[134:137], v[190:193], v[86:89]
	v_mfma_f32_16x16x32_bf16 v[78:81], v[142:145], v[190:193], v[78:81]
	v_mfma_f32_16x16x32_bf16 v[118:121], v[146:149], v[162:165], v[118:121]
	v_mfma_f32_16x16x32_bf16 v[110:113], v[154:157], v[162:165], v[110:113]
	v_mfma_f32_16x16x32_bf16 v[102:105], v[146:149], v[170:173], v[102:105]
	v_mfma_f32_16x16x32_bf16 v[98:101], v[154:157], v[170:173], v[98:101]
	v_mfma_f32_16x16x32_bf16 v[82:85], v[146:149], v[178:181], v[82:85]
	v_mfma_f32_16x16x32_bf16 v[74:77], v[154:157], v[178:181], v[74:77]
	v_mfma_f32_16x16x32_bf16 v[70:73], v[146:149], v[186:189], v[70:73]
	v_mfma_f32_16x16x32_bf16 v[66:69], v[154:157], v[186:189], v[66:69]
	v_mfma_f32_16x16x32_bf16 v[118:121], v[150:153], v[166:169], v[118:121]
	v_mfma_f32_16x16x32_bf16 v[110:113], v[158:161], v[166:169], v[110:113]
	v_mfma_f32_16x16x32_bf16 v[102:105], v[150:153], v[174:177], v[102:105]
	v_mfma_f32_16x16x32_bf16 v[98:101], v[158:161], v[174:177], v[98:101]
	v_mfma_f32_16x16x32_bf16 v[82:85], v[150:153], v[182:185], v[82:85]
	v_mfma_f32_16x16x32_bf16 v[74:77], v[158:161], v[182:185], v[74:77]
	v_mfma_f32_16x16x32_bf16 v[70:73], v[150:153], v[190:193], v[70:73]
	v_mfma_f32_16x16x32_bf16 v[66:69], v[158:161], v[190:193], v[66:69]
	s_setprio 0
	s_barrier
	ds_read_b128 v[162:165], v236 offset:16384
	ds_read_b128 v[166:169], v236 offset:17408
	ds_read_b128 v[170:173], v236 offset:18432
	ds_read_b128 v[174:177], v236 offset:19456
	ds_read_b128 v[178:181], v236 offset:20480
	ds_read_b128 v[182:185], v236 offset:21504
	ds_read_b128 v[186:189], v236 offset:22528
	ds_read_b128 v[190:193], v236 offset:23552
	s_mov_b32 s58, m0
	s_mov_b32 m0, s30
	s_nop 2
	global_load_lds_dwordx4 v229, s[64:65]
	s_mov_b32 m0, s58
	s_mov_b32 s58, m0
	s_mov_b32 m0, s31
	s_nop 2
	global_load_lds_dwordx4 v231, s[64:65]
	s_mov_b32 m0, s58
	s_add_u32 s58, s64, 0x40000
	s_addc_u32 s59, s65, 0
	s_mov_b32 s88, m0
	s_mov_b32 m0, s34
	s_nop 2
	global_load_lds_dwordx4 v229, s[58:59]
	s_mov_b32 m0, s88
	s_mov_b32 s88, m0
	s_mov_b32 m0, s35
	s_nop 2
	global_load_lds_dwordx4 v231, s[58:59]
	s_mov_b32 m0, s88
	s_mov_b32 s58, m0
	s_mov_b32 m0, s28
	s_nop 2
	global_load_lds_dwordx4 v228, s[66:67]
	s_mov_b32 m0, s58
	s_mov_b32 s58, m0
	s_mov_b32 m0, s36
	s_nop 2
	global_load_lds_dwordx4 v230, s[66:67]
	s_mov_b32 m0, s58
	s_waitcnt vmcnt(8)
	s_waitcnt lgkmcnt(0)
	s_barrier
	s_setprio 1
	v_mfma_f32_16x16x32_bf16 v[62:65], v[130:133], v[162:165], v[62:65]
	v_mfma_f32_16x16x32_bf16 v[58:61], v[138:141], v[162:165], v[58:61]
	v_mfma_f32_16x16x32_bf16 v[54:57], v[130:133], v[170:173], v[54:57]
	v_mfma_f32_16x16x32_bf16 v[46:49], v[138:141], v[170:173], v[46:49]
	v_mfma_f32_16x16x32_bf16 v[38:41], v[130:133], v[178:181], v[38:41]
	v_mfma_f32_16x16x32_bf16 v[30:33], v[138:141], v[178:181], v[30:33]
	v_mfma_f32_16x16x32_bf16 v[22:25], v[130:133], v[186:189], v[22:25]
	v_mfma_f32_16x16x32_bf16 v[14:17], v[138:141], v[186:189], v[14:17]
	v_mfma_f32_16x16x32_bf16 v[62:65], v[134:137], v[166:169], v[62:65]
	v_mfma_f32_16x16x32_bf16 v[58:61], v[142:145], v[166:169], v[58:61]
	v_mfma_f32_16x16x32_bf16 v[54:57], v[134:137], v[174:177], v[54:57]
	v_mfma_f32_16x16x32_bf16 v[46:49], v[142:145], v[174:177], v[46:49]
	v_mfma_f32_16x16x32_bf16 v[38:41], v[134:137], v[182:185], v[38:41]
	v_mfma_f32_16x16x32_bf16 v[30:33], v[142:145], v[182:185], v[30:33]
	v_mfma_f32_16x16x32_bf16 v[22:25], v[134:137], v[190:193], v[22:25]
	v_mfma_f32_16x16x32_bf16 v[14:17], v[142:145], v[190:193], v[14:17]
	v_mfma_f32_16x16x32_bf16 v[50:53], v[146:149], v[162:165], v[50:53]
	v_mfma_f32_16x16x32_bf16 v[42:45], v[154:157], v[162:165], v[42:45]
	v_mfma_f32_16x16x32_bf16 v[34:37], v[146:149], v[170:173], v[34:37]
	v_mfma_f32_16x16x32_bf16 v[26:29], v[154:157], v[170:173], v[26:29]
	v_mfma_f32_16x16x32_bf16 v[18:21], v[146:149], v[178:181], v[18:21]
	v_mfma_f32_16x16x32_bf16 v[10:13], v[154:157], v[178:181], v[10:13]
	v_mfma_f32_16x16x32_bf16 v[6:9], v[146:149], v[186:189], v[6:9]
	v_mfma_f32_16x16x32_bf16 v[2:5], v[154:157], v[186:189], v[2:5]
	v_mfma_f32_16x16x32_bf16 v[50:53], v[150:153], v[166:169], v[50:53]
	v_mfma_f32_16x16x32_bf16 v[42:45], v[158:161], v[166:169], v[42:45]
	v_mfma_f32_16x16x32_bf16 v[34:37], v[150:153], v[174:177], v[34:37]
	v_mfma_f32_16x16x32_bf16 v[26:29], v[158:161], v[174:177], v[26:29]
	v_mfma_f32_16x16x32_bf16 v[18:21], v[150:153], v[182:185], v[18:21]
	v_mfma_f32_16x16x32_bf16 v[10:13], v[158:161], v[182:185], v[10:13]
	v_mfma_f32_16x16x32_bf16 v[6:9], v[150:153], v[190:193], v[6:9]
	v_mfma_f32_16x16x32_bf16 v[2:5], v[158:161], v[190:193], v[2:5]
	s_setprio 0
	s_barrier
.Lmid1440:
	ds_read_b128 v[130:133], v237
	ds_read_b128 v[134:137], v237 offset:1024
	ds_read_b128 v[138:141], v237 offset:2048
	ds_read_b128 v[142:145], v237 offset:3072
	ds_read_b128 v[146:149], v238
	ds_read_b128 v[150:153], v238 offset:1024
	ds_read_b128 v[154:157], v238 offset:2048
	ds_read_b128 v[158:161], v238 offset:3072
	ds_read_b128 v[162:165], v236 offset:32768
	ds_read_b128 v[166:169], v236 offset:33792
	ds_read_b128 v[170:173], v236 offset:34816
	ds_read_b128 v[174:177], v236 offset:35840
	ds_read_b128 v[178:181], v236 offset:36864
	ds_read_b128 v[182:185], v236 offset:37888
	ds_read_b128 v[186:189], v236 offset:38912
	ds_read_b128 v[190:193], v236 offset:39936
	s_add_u32 s58, s66, 0x40000
	s_addc_u32 s59, s67, 0
	s_mov_b32 s66, m0
	s_mov_b32 m0, s37
	s_nop 2
	global_load_lds_dwordx4 v228, s[58:59]
	s_mov_b32 m0, s66
	s_mov_b32 s66, m0
	s_mov_b32 m0, s52
	s_nop 2
	global_load_lds_dwordx4 v230, s[58:59]
	s_mov_b32 m0, s66
	s_waitcnt vmcnt(8)
	s_waitcnt lgkmcnt(0)
	s_barrier
	s_setprio 1
	v_mfma_f32_16x16x32_bf16 v[126:129], v[130:133], v[162:165], v[126:129]
	v_mfma_f32_16x16x32_bf16 v[122:125], v[138:141], v[162:165], v[122:125]
	v_mfma_f32_16x16x32_bf16 v[114:117], v[130:133], v[170:173], v[114:117]
	v_mfma_f32_16x16x32_bf16 v[106:109], v[138:141], v[170:173], v[106:109]
	v_mfma_f32_16x16x32_bf16 v[94:97], v[130:133], v[178:181], v[94:97]
	v_mfma_f32_16x16x32_bf16 v[90:93], v[138:141], v[178:181], v[90:93]
	v_mfma_f32_16x16x32_bf16 v[86:89], v[130:133], v[186:189], v[86:89]
	v_mfma_f32_16x16x32_bf16 v[78:81], v[138:141], v[186:189], v[78:81]
	v_mfma_f32_16x16x32_bf16 v[126:129], v[134:137], v[166:169], v[126:129]
	v_mfma_f32_16x16x32_bf16 v[122:125], v[142:145], v[166:169], v[122:125]
	v_mfma_f32_16x16x32_bf16 v[114:117], v[134:137], v[174:177], v[114:117]
	v_mfma_f32_16x16x32_bf16 v[106:109], v[142:145], v[174:177], v[106:109]
	v_mfma_f32_16x16x32_bf16 v[94:97], v[134:137], v[182:185], v[94:97]
	v_mfma_f32_16x16x32_bf16 v[90:93], v[142:145], v[182:185], v[90:93]
	v_mfma_f32_16x16x32_bf16 v[86:89], v[134:137], v[190:193], v[86:89]
	v_mfma_f32_16x16x32_bf16 v[78:81], v[142:145], v[190:193], v[78:81]
	v_mfma_f32_16x16x32_bf16 v[118:121], v[146:149], v[162:165], v[118:121]
	v_mfma_f32_16x16x32_bf16 v[110:113], v[154:157], v[162:165], v[110:113]
	v_mfma_f32_16x16x32_bf16 v[102:105], v[146:149], v[170:173], v[102:105]
	v_mfma_f32_16x16x32_bf16 v[98:101], v[154:157], v[170:173], v[98:101]
	v_mfma_f32_16x16x32_bf16 v[82:85], v[146:149], v[178:181], v[82:85]
	v_mfma_f32_16x16x32_bf16 v[74:77], v[154:157], v[178:181], v[74:77]
	v_mfma_f32_16x16x32_bf16 v[70:73], v[146:149], v[186:189], v[70:73]
	v_mfma_f32_16x16x32_bf16 v[66:69], v[154:157], v[186:189], v[66:69]
	v_mfma_f32_16x16x32_bf16 v[118:121], v[150:153], v[166:169], v[118:121]
	v_mfma_f32_16x16x32_bf16 v[110:113], v[158:161], v[166:169], v[110:113]
	v_mfma_f32_16x16x32_bf16 v[102:105], v[150:153], v[174:177], v[102:105]
	v_mfma_f32_16x16x32_bf16 v[98:101], v[158:161], v[174:177], v[98:101]
	v_mfma_f32_16x16x32_bf16 v[82:85], v[150:153], v[182:185], v[82:85]
	v_mfma_f32_16x16x32_bf16 v[74:77], v[158:161], v[182:185], v[74:77]
	v_mfma_f32_16x16x32_bf16 v[70:73], v[150:153], v[190:193], v[70:73]
	v_mfma_f32_16x16x32_bf16 v[66:69], v[158:161], v[190:193], v[66:69]
	s_setprio 0
	s_barrier
	ds_read_b128 v[162:165], v236 offset:49152
	ds_read_b128 v[166:169], v236 offset:50176
	ds_read_b128 v[170:173], v236 offset:51200
	ds_read_b128 v[174:177], v236 offset:52224
	ds_read_b128 v[178:181], v236 offset:53248
	ds_read_b128 v[182:185], v236 offset:54272
	ds_read_b128 v[186:189], v236 offset:55296
	ds_read_b128 v[190:193], v236 offset:56320
	s_add_u32 s58, s64, 0x80
	s_addc_u32 s59, s65, 0
	s_mov_b32 s66, m0
	s_mov_b32 m0, s68
	s_nop 2
	global_load_lds_dwordx4 v229, s[58:59]
	s_mov_b32 m0, s66
	s_mov_b32 s66, m0
	s_mov_b32 m0, s69
	s_nop 2
	global_load_lds_dwordx4 v231, s[58:59]
	s_mov_b32 m0, s66
	s_add_u32 s58, s64, 0x40080
	s_addc_u32 s59, s65, 0
	s_mov_b32 s64, m0
	s_mov_b32 m0, s78
	s_nop 2
	global_load_lds_dwordx4 v229, s[58:59]
	s_mov_b32 m0, s64
	s_mov_b32 s64, m0
	s_mov_b32 m0, s79
	s_nop 2
	global_load_lds_dwordx4 v231, s[58:59]
	s_mov_b32 m0, s64
	s_mov_b32 s58, m0
	s_mov_b32 m0, s76
	s_nop 2
	global_load_lds_dwordx4 v228, s[62:63]
	s_mov_b32 m0, s58
	s_mov_b32 s58, m0
	s_mov_b32 m0, s77
	s_nop 2
	global_load_lds_dwordx4 v230, s[62:63]
	s_mov_b32 m0, s58
	s_waitcnt vmcnt(8)
	s_waitcnt lgkmcnt(0)
	s_barrier
	s_setprio 1
	v_mfma_f32_16x16x32_bf16 v[62:65], v[130:133], v[162:165], v[62:65]
	v_mfma_f32_16x16x32_bf16 v[58:61], v[138:141], v[162:165], v[58:61]
	v_mfma_f32_16x16x32_bf16 v[54:57], v[130:133], v[170:173], v[54:57]
	v_mfma_f32_16x16x32_bf16 v[46:49], v[138:141], v[170:173], v[46:49]
	v_mfma_f32_16x16x32_bf16 v[38:41], v[130:133], v[178:181], v[38:41]
	v_mfma_f32_16x16x32_bf16 v[30:33], v[138:141], v[178:181], v[30:33]
	v_mfma_f32_16x16x32_bf16 v[22:25], v[130:133], v[186:189], v[22:25]
	v_mfma_f32_16x16x32_bf16 v[14:17], v[138:141], v[186:189], v[14:17]
	v_mfma_f32_16x16x32_bf16 v[62:65], v[134:137], v[166:169], v[62:65]
	v_mfma_f32_16x16x32_bf16 v[58:61], v[142:145], v[166:169], v[58:61]
	v_mfma_f32_16x16x32_bf16 v[54:57], v[134:137], v[174:177], v[54:57]
	v_mfma_f32_16x16x32_bf16 v[46:49], v[142:145], v[174:177], v[46:49]
	v_mfma_f32_16x16x32_bf16 v[38:41], v[134:137], v[182:185], v[38:41]
	v_mfma_f32_16x16x32_bf16 v[30:33], v[142:145], v[182:185], v[30:33]
	v_mfma_f32_16x16x32_bf16 v[22:25], v[134:137], v[190:193], v[22:25]
	v_mfma_f32_16x16x32_bf16 v[14:17], v[142:145], v[190:193], v[14:17]
	v_mfma_f32_16x16x32_bf16 v[50:53], v[146:149], v[162:165], v[50:53]
	v_mfma_f32_16x16x32_bf16 v[42:45], v[154:157], v[162:165], v[42:45]
	v_mfma_f32_16x16x32_bf16 v[34:37], v[146:149], v[170:173], v[34:37]
	v_mfma_f32_16x16x32_bf16 v[26:29], v[154:157], v[170:173], v[26:29]
	v_mfma_f32_16x16x32_bf16 v[18:21], v[146:149], v[178:181], v[18:21]
	v_mfma_f32_16x16x32_bf16 v[10:13], v[154:157], v[178:181], v[10:13]
	v_mfma_f32_16x16x32_bf16 v[6:9], v[146:149], v[186:189], v[6:9]
	v_mfma_f32_16x16x32_bf16 v[2:5], v[154:157], v[186:189], v[2:5]
	v_mfma_f32_16x16x32_bf16 v[50:53], v[150:153], v[166:169], v[50:53]
	v_mfma_f32_16x16x32_bf16 v[42:45], v[158:161], v[166:169], v[42:45]
	v_mfma_f32_16x16x32_bf16 v[34:37], v[150:153], v[174:177], v[34:37]
	v_mfma_f32_16x16x32_bf16 v[26:29], v[158:161], v[174:177], v[26:29]
	v_mfma_f32_16x16x32_bf16 v[18:21], v[150:153], v[182:185], v[18:21]
	v_mfma_f32_16x16x32_bf16 v[10:13], v[158:161], v[182:185], v[10:13]
	v_mfma_f32_16x16x32_bf16 v[6:9], v[150:153], v[190:193], v[6:9]
	v_mfma_f32_16x16x32_bf16 v[2:5], v[158:161], v[190:193], v[2:5]
	s_setprio 0
	s_barrier
	s_add_i32 s87, s87, 2
	s_add_u32 s85, s85, 0x100
	s_addc_u32 s86, s86, 0
	s_cmp_gt_u32 s87, 13
	s_mov_b64 s[58:59], s[60:61]
	s_cbranch_scc0 .LBB0_1440
	s_and_b64 vcc, exec, s[16:17]
	s_cbranch_vccz .LBB0_1443
	s_barrier

.LBB0_1717:
	s_mov_b32 s0, m0
	s_mov_b32 m0, s3
	s_nop 2
	global_load_lds_dwordx4 v178, s[12:13]
	s_mov_b32 m0, s0
	s_and_b64 vcc, exec, s[8:9]
	s_mov_b32 s0, m0
	s_mov_b32 m0, s26
	s_nop 2
	global_load_lds_dwordx4 v179, s[12:13]
	s_mov_b32 m0, s0
	s_mov_b32 s0, m0
	s_mov_b32 m0, s27
	s_nop 2
	global_load_lds_dwordx4 v180, s[12:13]
	s_mov_b32 m0, s0
	s_mov_b32 s0, m0
	s_mov_b32 m0, s34
	s_nop 2
	global_load_lds_dwordx4 v181, s[12:13]
	s_mov_b32 m0, s0
	s_mov_b32 s0, m0
	s_mov_b32 m0, s35
	s_nop 2
	global_load_lds_dwordx4 v182, s[12:13]
	s_mov_b32 m0, s0
	s_mov_b32 s0, m0
	s_mov_b32 m0, s56
	s_nop 2
	global_load_lds_dwordx4 v183, s[12:13]
	s_mov_b32 m0, s0
	s_mov_b32 s0, m0
	s_mov_b32 m0, s57
	s_nop 2
	global_load_lds_dwordx4 v184, s[12:13]
	s_mov_b32 m0, s0
	s_mov_b32 s0, m0
	s_mov_b32 m0, s58
	s_nop 2
	global_load_lds_dwordx4 v185, s[12:13]
	s_mov_b32 m0, s0
	s_mov_b32 s0, m0
	s_mov_b32 m0, s59
	s_nop 2
	global_load_lds_dwordx4 v186, s[12:13]
	s_mov_b32 m0, s0
	s_mov_b32 s0, m0
	s_mov_b32 m0, s60
	s_nop 2
	global_load_lds_dwordx4 v187, s[12:13]
	s_mov_b32 m0, s0
	s_mov_b32 s0, m0
	s_mov_b32 m0, s61
	s_nop 2
	global_load_lds_dwordx4 v188, s[12:13]
	s_mov_b32 m0, s0
	s_mov_b32 s0, m0
	s_mov_b32 m0, s62
	s_nop 2
	global_load_lds_dwordx4 v189, s[12:13]
	s_mov_b32 m0, s0
	s_mov_b32 s0, m0
	s_mov_b32 m0, s63
	s_nop 2
	global_load_lds_dwordx4 v190, s[12:13]
	s_mov_b32 m0, s0
	s_mov_b32 s0, m0
	s_mov_b32 m0, s64
	s_nop 2
	global_load_lds_dwordx4 v191, s[12:13]
	s_mov_b32 m0, s0
	s_mov_b32 s0, m0
	s_mov_b32 m0, s65
	s_nop 2
	global_load_lds_dwordx4 v192, s[12:13]
	s_mov_b32 m0, s0
	s_mov_b32 s0, m0
	s_mov_b32 m0, s66
	s_nop 2
	global_load_lds_dwordx4 v193, s[12:13]
	s_mov_b32 m0, s0
	s_waitcnt vmcnt(0)
	s_waitcnt lgkmcnt(0)
	s_barrier
	s_cbranch_vccnz .LBB0_1721
	v_add_u32_e32 v136, v175, v194
	ds_read_b128 v[132:135], v136
	ds_read_b128 v[136:139], v136 offset:32768
	v_add_u32_e32 v140, v176, v194
	ds_read_b128 v[140:143], v140
	v_add_u32_e32 v144, v177, v194
	s_waitcnt vmcnt(31) lgkmcnt(2)
	v_mfma_f32_16x16x32_bf16 v[132:135], v[126:129], v[132:135], 0
	ds_read_b128 v[144:147], v144
	v_and_b32_e32 v149, 0xffff0000, v127
	v_med3_f32 v150, v149, s78, v240
	s_waitcnt lgkmcnt(2)
	v_mfma_f32_16x16x32_bf16 v[136:139], v[126:129], v[136:139], 0
	v_lshlrev_b32_e32 v151, 16, v128
	v_and_b32_e32 v153, 0xffff0000, v128
	v_med3_f32 v152, v151, s78, v240
	s_waitcnt lgkmcnt(1)
	v_mfma_f32_16x16x32_bf16 v[132:135], v[126:129], v[140:143], v[132:135]
	v_lshlrev_b32_e32 v141, 16, v126
	v_and_b32_e32 v143, 0xffff0000, v126
	v_med3_f32 v154, v153, s78, v240
	s_waitcnt lgkmcnt(0)
	v_mfma_f32_16x16x32_bf16 v[136:139], v[126:129], v[144:147], v[136:139]
	v_med3_f32 v145, v141, s78, v240
	v_med3_f32 v146, v143, s78, v240
	v_mov_b32_e32 v144, 0
	v_cvt_pk_fp8_f32 v144, v145, v146
	v_lshlrev_b32_e32 v147, 16, v127
	v_med3_f32 v145, v147, s78, v240
	v_lshlrev_b32_e32 v155, 16, v129
	v_cvt_pk_fp8_f32 v144, v145, v150 op_sel:[0,0,1]
	v_mov_b32_e32 v145, 0
	v_cvt_pk_fp8_f32 v145, v152, v154
	v_and_b32_e32 v157, 0xffff0000, v129
	v_med3_f32 v152, v155, s78, v240
	v_med3_f32 v154, v157, s78, v240
	v_cvt_pk_fp8_f32 v145, v152, v154 op_sel:[0,0,1]
	v_lshlrev_b64 v[130:131], 10, v[130:131]
	v_lshl_add_u64 v[130:131], v[164:165], 0, v[130:131]
	s_waitcnt vmcnt(30)
	v_and_b32_e32 v142, 0xffff0000, v122
	v_lshlrev_b32_e32 v140, 16, v122
	v_and_b32_e32 v148, 0xffff0000, v123
	global_store_dwordx2 v[130:131], v[144:145], off
	v_pk_mul_f32 v[144:145], v[142:143], v[142:143]
	v_lshlrev_b32_e32 v146, 16, v123
	v_pk_fma_f32 v[144:145], v[140:141], v[140:141], v[144:145]
	v_pk_mul_f32 v[158:159], v[148:149], v[148:149]
	v_med3_f32 v140, v140, s78, v240
	v_med3_f32 v141, v142, s78, v240
	v_mov_b32_e32 v160, 0
	v_and_b32_e32 v152, 0xffff0000, v124
	v_pk_fma_f32 v[158:159], v[146:147], v[146:147], v[158:159]
	v_cvt_pk_fp8_f32 v160, v140, v141
	v_lshlrev_b32_e32 v150, 16, v124
	v_pk_add_f32 v[144:145], v[144:145], v[158:159]
	v_pk_mul_f32 v[158:159], v[152:153], v[152:153]
	v_and_b32_e32 v156, 0xffff0000, v125
	v_pk_fma_f32 v[158:159], v[150:151], v[150:151], v[158:159]
	v_lshlrev_b32_e32 v154, 16, v125
	v_pk_add_f32 v[158:159], v[158:159], v[144:145]
	v_pk_mul_f32 v[144:145], v[156:157], v[156:157]
	v_med3_f32 v140, v146, s78, v240
	v_med3_f32 v141, v148, s78, v240
	v_add_u32_e32 v146, v175, v195
	v_pk_fma_f32 v[244:245], v[154:155], v[154:155], v[144:145]
	v_cvt_pk_fp8_f32 v160, v140, v141 op_sel:[0,0,1]
	v_med3_f32 v144, v150, s78, v240
	v_med3_f32 v145, v152, s78, v240
	ds_read_b128 v[140:143], v146
	v_mov_b32_e32 v161, 0
	v_cvt_pk_fp8_f32 v161, v144, v145
	ds_read_b128 v[144:147], v146 offset:32768
	s_waitcnt lgkmcnt(1)
	v_mfma_f32_16x16x32_bf16 v[132:135], v[122:125], v[140:143], v[132:135]
	v_add_u32_e32 v140, v176, v195
	ds_read_b128 v[140:143], v140
	v_med3_f32 v148, v154, s78, v240
	s_waitcnt lgkmcnt(1)
	v_mfma_f32_16x16x32_bf16 v[136:139], v[122:125], v[144:147], v[136:139]
	v_add_u32_e32 v144, v177, v195
	ds_read_b128 v[144:147], v144
	v_med3_f32 v149, v156, s78, v240
	s_waitcnt lgkmcnt(1)
	v_mfma_f32_16x16x32_bf16 v[132:135], v[122:125], v[140:143], v[132:135]
	v_add_f32_e64 v140, v244, v158
	v_add_f32_e64 v141, v245, v159
	s_waitcnt vmcnt(30)
	v_and_b32_e32 v143, 0xffff0000, v119
	v_and_b32_e32 v142, 0xffff0000, v118
	v_cvt_pk_fp8_f32 v161, v148, v149 op_sel:[0,0,1]
	v_pk_add_f32 v[148:149], v[140:141], v[140:141] op_sel_hi:[0,1]
	s_waitcnt lgkmcnt(0)
	v_mfma_f32_16x16x32_bf16 v[136:139], v[122:125], v[144:147], v[136:139]
	v_lshlrev_b32_e32 v141, 16, v119
	v_lshlrev_b32_e32 v140, 16, v118
	v_pk_mul_f32 v[144:145], v[142:143], v[142:143]
	v_med3_f32 v142, v142, s78, v240
	v_pk_fma_f32 v[144:145], v[140:141], v[140:141], v[144:145]
	v_med3_f32 v140, v140, s78, v240
	v_mov_b32_e32 v154, 0
	v_cvt_pk_fp8_f32 v154, v140, v142
	v_and_b32_e32 v151, 0xffff0000, v121
	v_and_b32_e32 v150, 0xffff0000, v120
	v_lshlrev_b32_e32 v147, 16, v121
	v_lshlrev_b32_e32 v146, 16, v120
	v_pk_mul_f32 v[152:153], v[150:151], v[150:151]
	v_add_f32_e32 v148, v144, v145
	v_pk_fma_f32 v[152:153], v[146:147], v[146:147], v[152:153]
	v_med3_f32 v140, v141, s78, v240
	v_med3_f32 v141, v143, s78, v240
	v_med3_f32 v144, v146, s78, v240
	v_med3_f32 v145, v150, s78, v240
	v_add_u32_e32 v146, v175, v196
	v_mov_b32_e32 v155, 0
	v_cvt_pk_fp8_f32 v154, v140, v141 op_sel:[0,0,1]
	ds_read_b128 v[140:143], v146
	v_cvt_pk_fp8_f32 v155, v144, v145
	v_med3_f32 v150, v147, s78, v240
	ds_read_b128 v[144:147], v146 offset:32768
	s_waitcnt lgkmcnt(1)
	v_mfma_f32_16x16x32_bf16 v[132:135], v[118:121], v[140:143], v[132:135]
	v_add_u32_e32 v140, v176, v196
	ds_read_b128 v[140:143], v140
	v_med3_f32 v151, v151, s78, v240
	s_waitcnt lgkmcnt(1)
	v_mfma_f32_16x16x32_bf16 v[136:139], v[118:121], v[144:147], v[136:139]
	v_add_u32_e32 v144, v177, v196
	ds_read_b128 v[144:147], v144
	v_cvt_pk_fp8_f32 v155, v150, v151 op_sel:[0,0,1]
	s_waitcnt lgkmcnt(1)
	v_mfma_f32_16x16x32_bf16 v[132:135], v[118:121], v[140:143], v[132:135]
	v_add_f32_e32 v140, v152, v148
	v_pk_add_f32 v[150:151], v[152:153], v[140:141] op_sel_hi:[1,0]
	global_store_dwordx2 v[130:131], v[154:155], off offset:64
	s_waitcnt lgkmcnt(0)
	v_mfma_f32_16x16x32_bf16 v[136:139], v[118:121], v[144:147], v[136:139]
	s_waitcnt vmcnt(30)
	v_lshlrev_b32_e32 v144, 16, v114
	v_and_b32_e32 v145, 0xffff0000, v114
	v_mul_f32_e32 v140, v144, v144
	v_add_u32_e32 v147, v175, v197
	v_pk_fma_f32 v[152:153], v[144:145], v[144:145], v[140:141] op_sel_hi:[1,1,0]
	v_lshlrev_b32_e32 v154, 16, v115
	ds_read_b128 v[140:143], v147
	v_and_b32_e32 v155, 0xffff0000, v115
	v_mul_f32_e32 v146, v154, v154
	v_pk_fma_f32 v[156:157], v[154:155], v[154:155], v[146:147] op_sel_hi:[1,1,0]
	v_med3_f32 v148, v144, s78, v240
	v_med3_f32 v150, v145, s78, v240
	ds_read_b128 v[144:147], v147 offset:32768
	s_waitcnt lgkmcnt(1)
	v_mfma_f32_16x16x32_bf16 v[132:135], v[114:117], v[140:143], v[132:135]
	v_add_u32_e32 v140, v176, v197
	ds_read_b128 v[140:143], v140
	v_mov_b32_e32 v158, 0
	s_waitcnt lgkmcnt(1)
	v_mfma_f32_16x16x32_bf16 v[136:139], v[114:117], v[144:147], v[136:139]
	v_add_u32_e32 v144, v177, v197
	v_cvt_pk_fp8_f32 v158, v148, v150
	ds_read_b128 v[144:147], v144
	s_waitcnt lgkmcnt(1)
	v_mfma_f32_16x16x32_bf16 v[132:135], v[114:117], v[140:143], v[132:135]
	v_med3_f32 v140, v154, s78, v240
	v_med3_f32 v141, v155, s78, v240
	v_cvt_pk_fp8_f32 v158, v140, v141 op_sel:[0,0,1]
	v_lshlrev_b32_e32 v141, 16, v116
	v_and_b32_e32 v143, 0xffff0000, v116
	s_waitcnt lgkmcnt(0)
	v_mfma_f32_16x16x32_bf16 v[136:139], v[114:117], v[144:147], v[136:139]
	v_med3_f32 v142, v141, s78, v240
	v_med3_f32 v144, v143, s78, v240
	v_mov_b32_e32 v159, 0
	v_cvt_pk_fp8_f32 v159, v142, v144
	v_lshlrev_b32_e32 v145, 16, v117
	v_and_b32_e32 v147, 0xffff0000, v117
	v_med3_f32 v142, v145, s78, v240
	v_med3_f32 v144, v147, s78, v240
	global_store_dwordx2 v[130:131], v[160:161], off offset:32
	s_waitcnt vmcnt(30)
	v_lshlrev_b32_e32 v160, 16, v111
	v_and_b32_e32 v161, 0xffff0000, v111
	v_cvt_pk_fp8_f32 v159, v142, v144 op_sel:[0,0,1]
	v_and_b32_e32 v142, 0xffff0000, v110
	v_mul_f32_e32 v152, v160, v160
	v_mul_f32_e32 v156, v161, v161
	v_lshlrev_b32_e32 v140, 16, v110
	v_pk_mul_f32 v[154:155], v[142:143], v[142:143]
	v_and_b32_e32 v146, 0xffff0000, v112
	v_pk_fma_f32 v[154:155], v[140:141], v[140:141], v[154:155]
	v_pk_add_f32 v[152:153], v[152:153], v[156:157]
	v_lshlrev_b32_e32 v144, 16, v112
	v_pk_add_f32 v[152:153], v[154:155], v[152:153]
	v_pk_mul_f32 v[154:155], v[146:147], v[146:147]
	v_med3_f32 v140, v140, s78, v240
	v_pk_fma_f32 v[154:155], v[144:145], v[144:145], v[154:155]
	v_med3_f32 v141, v142, s78, v240
	v_pk_add_f32 v[152:153], v[154:155], v[152:153]
	v_mov_b32_e32 v154, 0
	v_cvt_pk_fp8_f32 v154, v140, v141
	v_med3_f32 v140, v160, s78, v240
	v_med3_f32 v141, v161, s78, v240
	v_med3_f32 v145, v146, s78, v240
	v_add_u32_e32 v146, v175, v198
	v_cvt_pk_fp8_f32 v154, v140, v141 op_sel:[0,0,1]
	v_med3_f32 v144, v144, s78, v240
	ds_read_b128 v[140:143], v146
	v_mov_b32_e32 v155, 0
	v_cvt_pk_fp8_f32 v155, v144, v145
	ds_read_b128 v[144:147], v146 offset:32768
	s_waitcnt lgkmcnt(1)
	v_mfma_f32_16x16x32_bf16 v[132:135], v[110:113], v[140:143], v[132:135]
	v_add_u32_e32 v140, v176, v198
	v_lshlrev_b32_e32 v173, 16, v113
	v_and_b32_e32 v243, 0xffff0000, v113
	ds_read_b128 v[140:143], v140
	s_waitcnt lgkmcnt(1)
	v_mfma_f32_16x16x32_bf16 v[136:139], v[110:113], v[144:147], v[136:139]
	v_add_u32_e32 v144, v177, v198
	v_mul_f32_e32 v150, v173, v173
	v_mul_f32_e32 v148, v243, v243
	ds_read_b128 v[144:147], v144
	v_pk_add_f32 v[148:149], v[150:151], v[148:149]
	v_med3_f32 v150, v173, s78, v240
	v_med3_f32 v151, v243, s78, v240
	v_cvt_pk_fp8_f32 v155, v150, v151 op_sel:[0,0,1]
	s_waitcnt lgkmcnt(1)
	v_mfma_f32_16x16x32_bf16 v[132:135], v[110:113], v[140:143], v[132:135]
	v_add_f32_e64 v140, v152, v148
	v_add_f32_e64 v141, v153, v149
	s_waitcnt vmcnt(29)
	v_and_b32_e32 v143, 0xffff0000, v107
	v_and_b32_e32 v142, 0xffff0000, v106
	v_pk_add_f32 v[148:149], v[140:141], v[140:141] op_sel_hi:[0,1]
	s_waitcnt lgkmcnt(0)
	v_mfma_f32_16x16x32_bf16 v[136:139], v[110:113], v[144:147], v[136:139]
	v_lshlrev_b32_e32 v141, 16, v107
	v_lshlrev_b32_e32 v140, 16, v106
	v_pk_mul_f32 v[144:145], v[142:143], v[142:143]
	global_store_dwordx2 v[130:131], v[154:155], off offset:128
	v_pk_fma_f32 v[144:145], v[140:141], v[140:141], v[144:145]
	v_med3_f32 v140, v140, s78, v240
	v_med3_f32 v142, v142, s78, v240
	v_mov_b32_e32 v154, 0
	v_cvt_pk_fp8_f32 v154, v140, v142
	v_and_b32_e32 v151, 0xffff0000, v109
	v_and_b32_e32 v150, 0xffff0000, v108
	v_lshlrev_b32_e32 v147, 16, v109
	v_lshlrev_b32_e32 v146, 16, v108
	v_pk_mul_f32 v[152:153], v[150:151], v[150:151]
	v_add_f32_e32 v148, v144, v145
	v_pk_fma_f32 v[152:153], v[146:147], v[146:147], v[152:153]
	v_med3_f32 v140, v141, s78, v240
	v_med3_f32 v141, v143, s78, v240
	v_med3_f32 v144, v146, s78, v240
	v_med3_f32 v145, v150, s78, v240
	v_add_u32_e32 v146, v175, v199
	v_mov_b32_e32 v155, 0
	v_cvt_pk_fp8_f32 v154, v140, v141 op_sel:[0,0,1]
	ds_read_b128 v[140:143], v146
	v_cvt_pk_fp8_f32 v155, v144, v145
	v_med3_f32 v150, v147, s78, v240
	ds_read_b128 v[144:147], v146 offset:32768
	s_waitcnt lgkmcnt(1)
	v_mfma_f32_16x16x32_bf16 v[132:135], v[106:109], v[140:143], v[132:135]
	v_add_u32_e32 v140, v176, v199
	ds_read_b128 v[140:143], v140
	v_med3_f32 v151, v151, s78, v240
	s_waitcnt lgkmcnt(1)
	v_mfma_f32_16x16x32_bf16 v[136:139], v[106:109], v[144:147], v[136:139]
	v_add_u32_e32 v144, v177, v199
	ds_read_b128 v[144:147], v144
	v_cvt_pk_fp8_f32 v155, v150, v151 op_sel:[0,0,1]
	s_waitcnt lgkmcnt(1)
	v_mfma_f32_16x16x32_bf16 v[132:135], v[106:109], v[140:143], v[132:135]
	v_add_f32_e32 v140, v152, v148
	v_pk_add_f32 v[150:151], v[152:153], v[140:141] op_sel_hi:[1,0]
	global_store_dwordx2 v[130:131], v[154:155], off offset:160
	s_waitcnt lgkmcnt(0)
	v_mfma_f32_16x16x32_bf16 v[136:139], v[106:109], v[144:147], v[136:139]
	s_waitcnt vmcnt(30)
	v_lshlrev_b32_e32 v144, 16, v102
	v_and_b32_e32 v145, 0xffff0000, v102
	v_mul_f32_e32 v140, v144, v144
	v_add_u32_e32 v147, v175, v200
	v_pk_fma_f32 v[152:153], v[144:145], v[144:145], v[140:141] op_sel_hi:[1,1,0]
	v_lshlrev_b32_e32 v154, 16, v103
	ds_read_b128 v[140:143], v147
	v_and_b32_e32 v155, 0xffff0000, v103
	v_mul_f32_e32 v146, v154, v154
	v_pk_fma_f32 v[156:157], v[154:155], v[154:155], v[146:147] op_sel_hi:[1,1,0]
	v_med3_f32 v148, v144, s78, v240
	v_med3_f32 v150, v145, s78, v240
	ds_read_b128 v[144:147], v147 offset:32768
	s_waitcnt lgkmcnt(1)
	v_mfma_f32_16x16x32_bf16 v[132:135], v[102:105], v[140:143], v[132:135]
	v_add_u32_e32 v140, v176, v200
	ds_read_b128 v[140:143], v140
	global_store_dwordx2 v[130:131], v[158:159], off offset:96
	v_mov_b32_e32 v158, 0
	s_waitcnt lgkmcnt(1)
	v_mfma_f32_16x16x32_bf16 v[136:139], v[102:105], v[144:147], v[136:139]
	v_add_u32_e32 v144, v177, v200
	v_cvt_pk_fp8_f32 v158, v148, v150
	ds_read_b128 v[144:147], v144
	s_waitcnt lgkmcnt(1)
	v_mfma_f32_16x16x32_bf16 v[132:135], v[102:105], v[140:143], v[132:135]
	v_med3_f32 v140, v154, s78, v240
	v_med3_f32 v141, v155, s78, v240
	v_cvt_pk_fp8_f32 v158, v140, v141 op_sel:[0,0,1]
	v_lshlrev_b32_e32 v141, 16, v104
	v_and_b32_e32 v143, 0xffff0000, v104
	s_waitcnt lgkmcnt(0)
	v_mfma_f32_16x16x32_bf16 v[136:139], v[102:105], v[144:147], v[136:139]
	v_med3_f32 v142, v141, s78, v240
	v_med3_f32 v144, v143, s78, v240
	v_mov_b32_e32 v159, 0
	v_cvt_pk_fp8_f32 v159, v142, v144
	v_lshlrev_b32_e32 v145, 16, v105
	v_and_b32_e32 v147, 0xffff0000, v105
	v_med3_f32 v142, v145, s78, v240
	v_med3_f32 v144, v147, s78, v240
	s_waitcnt vmcnt(30)
	v_lshlrev_b32_e32 v160, 16, v99
	v_and_b32_e32 v161, 0xffff0000, v99
	v_cvt_pk_fp8_f32 v159, v142, v144 op_sel:[0,0,1]
	v_and_b32_e32 v142, 0xffff0000, v98
	v_mul_f32_e32 v152, v160, v160
	v_mul_f32_e32 v156, v161, v161
	v_lshlrev_b32_e32 v140, 16, v98
	v_pk_mul_f32 v[154:155], v[142:143], v[142:143]
	v_and_b32_e32 v146, 0xffff0000, v100
	v_pk_fma_f32 v[154:155], v[140:141], v[140:141], v[154:155]
	v_pk_add_f32 v[152:153], v[152:153], v[156:157]
	v_lshlrev_b32_e32 v144, 16, v100
	v_pk_add_f32 v[152:153], v[154:155], v[152:153]
	v_pk_mul_f32 v[154:155], v[146:147], v[146:147]
	v_med3_f32 v140, v140, s78, v240
	v_pk_fma_f32 v[154:155], v[144:145], v[144:145], v[154:155]
	v_med3_f32 v141, v142, s78, v240
	v_pk_add_f32 v[152:153], v[154:155], v[152:153]
	v_mov_b32_e32 v154, 0
	v_cvt_pk_fp8_f32 v154, v140, v141
	v_med3_f32 v140, v160, s78, v240
	v_med3_f32 v141, v161, s78, v240
	v_med3_f32 v145, v146, s78, v240
	v_add_u32_e32 v146, v175, v201
	v_cvt_pk_fp8_f32 v154, v140, v141 op_sel:[0,0,1]
	v_med3_f32 v144, v144, s78, v240
	ds_read_b128 v[140:143], v146
	v_mov_b32_e32 v155, 0
	v_cvt_pk_fp8_f32 v155, v144, v145
	ds_read_b128 v[144:147], v146 offset:32768
	s_waitcnt lgkmcnt(1)
	v_mfma_f32_16x16x32_bf16 v[132:135], v[98:101], v[140:143], v[132:135]
	v_add_u32_e32 v140, v176, v201
	v_lshlrev_b32_e32 v173, 16, v101
	v_and_b32_e32 v243, 0xffff0000, v101
	ds_read_b128 v[140:143], v140
	s_waitcnt lgkmcnt(1)
	v_mfma_f32_16x16x32_bf16 v[136:139], v[98:101], v[144:147], v[136:139]
	v_add_u32_e32 v144, v177, v201
	v_mul_f32_e32 v150, v173, v173
	v_mul_f32_e32 v148, v243, v243
	ds_read_b128 v[144:147], v144
	v_pk_add_f32 v[148:149], v[150:151], v[148:149]
	v_med3_f32 v150, v173, s78, v240
	v_med3_f32 v151, v243, s78, v240
	v_cvt_pk_fp8_f32 v155, v150, v151 op_sel:[0,0,1]
	s_waitcnt lgkmcnt(1)
	v_mfma_f32_16x16x32_bf16 v[132:135], v[98:101], v[140:143], v[132:135]
	v_add_f32_e64 v140, v152, v148
	v_add_f32_e64 v141, v153, v149
	s_waitcnt vmcnt(29)
	v_and_b32_e32 v143, 0xffff0000, v95
	v_and_b32_e32 v142, 0xffff0000, v94
	v_pk_add_f32 v[148:149], v[140:141], v[140:141] op_sel_hi:[0,1]
	s_waitcnt lgkmcnt(0)
	v_mfma_f32_16x16x32_bf16 v[136:139], v[98:101], v[144:147], v[136:139]
	v_lshlrev_b32_e32 v141, 16, v95
	v_lshlrev_b32_e32 v140, 16, v94
	v_pk_mul_f32 v[144:145], v[142:143], v[142:143]
	global_store_dwordx2 v[130:131], v[154:155], off offset:224
	v_pk_fma_f32 v[144:145], v[140:141], v[140:141], v[144:145]
	v_med3_f32 v140, v140, s78, v240
	v_med3_f32 v142, v142, s78, v240
	v_mov_b32_e32 v154, 0
	v_cvt_pk_fp8_f32 v154, v140, v142
	v_and_b32_e32 v151, 0xffff0000, v97
	v_and_b32_e32 v150, 0xffff0000, v96
	v_lshlrev_b32_e32 v147, 16, v97
	v_lshlrev_b32_e32 v146, 16, v96
	v_pk_mul_f32 v[152:153], v[150:151], v[150:151]
	v_add_f32_e32 v148, v144, v145
	v_pk_fma_f32 v[152:153], v[146:147], v[146:147], v[152:153]
	v_med3_f32 v140, v141, s78, v240
	v_med3_f32 v141, v143, s78, v240
	v_med3_f32 v144, v146, s78, v240
	v_med3_f32 v145, v150, s78, v240
	v_add_u32_e32 v146, v175, v202
	v_mov_b32_e32 v155, 0
	v_cvt_pk_fp8_f32 v154, v140, v141 op_sel:[0,0,1]
	ds_read_b128 v[140:143], v146
	v_cvt_pk_fp8_f32 v155, v144, v145
	v_med3_f32 v150, v147, s78, v240
	ds_read_b128 v[144:147], v146 offset:32768
	s_waitcnt lgkmcnt(1)
	v_mfma_f32_16x16x32_bf16 v[132:135], v[94:97], v[140:143], v[132:135]
	v_add_u32_e32 v140, v176, v202
	ds_read_b128 v[140:143], v140
	v_med3_f32 v151, v151, s78, v240
	s_waitcnt lgkmcnt(1)
	v_mfma_f32_16x16x32_bf16 v[136:139], v[94:97], v[144:147], v[136:139]
	v_add_u32_e32 v144, v177, v202
	ds_read_b128 v[144:147], v144
	v_cvt_pk_fp8_f32 v155, v150, v151 op_sel:[0,0,1]
	s_waitcnt lgkmcnt(1)
	v_mfma_f32_16x16x32_bf16 v[132:135], v[94:97], v[140:143], v[132:135]
	v_add_f32_e32 v140, v152, v148
	v_pk_add_f32 v[150:151], v[152:153], v[140:141] op_sel_hi:[1,0]
	global_store_dwordx2 v[130:131], v[154:155], off offset:256
	s_waitcnt lgkmcnt(0)
	v_mfma_f32_16x16x32_bf16 v[136:139], v[94:97], v[144:147], v[136:139]
	s_waitcnt vmcnt(30)
	v_lshlrev_b32_e32 v144, 16, v90
	v_and_b32_e32 v145, 0xffff0000, v90
	v_mul_f32_e32 v140, v144, v144
	v_add_u32_e32 v147, v175, v203
	v_pk_fma_f32 v[152:153], v[144:145], v[144:145], v[140:141] op_sel_hi:[1,1,0]
	v_lshlrev_b32_e32 v154, 16, v91
	ds_read_b128 v[140:143], v147
	v_and_b32_e32 v155, 0xffff0000, v91
	v_mul_f32_e32 v146, v154, v154
	v_pk_fma_f32 v[156:157], v[154:155], v[154:155], v[146:147] op_sel_hi:[1,1,0]
	v_med3_f32 v148, v144, s78, v240
	v_med3_f32 v150, v145, s78, v240
	ds_read_b128 v[144:147], v147 offset:32768
	s_waitcnt lgkmcnt(1)
	v_mfma_f32_16x16x32_bf16 v[132:135], v[90:93], v[140:143], v[132:135]
	v_add_u32_e32 v140, v176, v203
	ds_read_b128 v[140:143], v140
	global_store_dwordx2 v[130:131], v[158:159], off offset:192
	v_mov_b32_e32 v158, 0
	s_waitcnt lgkmcnt(1)
	v_mfma_f32_16x16x32_bf16 v[136:139], v[90:93], v[144:147], v[136:139]
	v_add_u32_e32 v144, v177, v203
	v_cvt_pk_fp8_f32 v158, v148, v150
	ds_read_b128 v[144:147], v144
	s_waitcnt lgkmcnt(1)
	v_mfma_f32_16x16x32_bf16 v[132:135], v[90:93], v[140:143], v[132:135]
	v_med3_f32 v140, v154, s78, v240
	v_med3_f32 v141, v155, s78, v240
	v_cvt_pk_fp8_f32 v158, v140, v141 op_sel:[0,0,1]
	v_lshlrev_b32_e32 v141, 16, v92
	v_and_b32_e32 v143, 0xffff0000, v92
	s_waitcnt lgkmcnt(0)
	v_mfma_f32_16x16x32_bf16 v[136:139], v[90:93], v[144:147], v[136:139]
	v_med3_f32 v142, v141, s78, v240
	v_med3_f32 v144, v143, s78, v240
	v_mov_b32_e32 v159, 0
	v_cvt_pk_fp8_f32 v159, v142, v144
	v_lshlrev_b32_e32 v145, 16, v93
	v_and_b32_e32 v147, 0xffff0000, v93
	v_med3_f32 v142, v145, s78, v240
	v_med3_f32 v144, v147, s78, v240
	s_waitcnt vmcnt(30)
	v_lshlrev_b32_e32 v160, 16, v87
	v_and_b32_e32 v161, 0xffff0000, v87
	v_cvt_pk_fp8_f32 v159, v142, v144 op_sel:[0,0,1]
	v_and_b32_e32 v142, 0xffff0000, v86
	v_mul_f32_e32 v152, v160, v160
	v_mul_f32_e32 v156, v161, v161
	v_lshlrev_b32_e32 v140, 16, v86
	v_pk_mul_f32 v[154:155], v[142:143], v[142:143]
	v_and_b32_e32 v146, 0xffff0000, v88
	v_pk_fma_f32 v[154:155], v[140:141], v[140:141], v[154:155]
	v_pk_add_f32 v[152:153], v[152:153], v[156:157]
	v_lshlrev_b32_e32 v144, 16, v88
	v_pk_add_f32 v[152:153], v[154:155], v[152:153]
	v_pk_mul_f32 v[154:155], v[146:147], v[146:147]
	v_med3_f32 v140, v140, s78, v240
	v_pk_fma_f32 v[154:155], v[144:145], v[144:145], v[154:155]
	v_med3_f32 v141, v142, s78, v240
	v_pk_add_f32 v[152:153], v[154:155], v[152:153]
	v_mov_b32_e32 v154, 0
	v_cvt_pk_fp8_f32 v154, v140, v141
	v_med3_f32 v140, v160, s78, v240
	v_med3_f32 v141, v161, s78, v240
	v_med3_f32 v145, v146, s78, v240
	v_add_u32_e32 v146, v175, v204
	v_cvt_pk_fp8_f32 v154, v140, v141 op_sel:[0,0,1]
	v_med3_f32 v144, v144, s78, v240
	ds_read_b128 v[140:143], v146
	v_mov_b32_e32 v155, 0
	v_cvt_pk_fp8_f32 v155, v144, v145
	ds_read_b128 v[144:147], v146 offset:32768
	s_waitcnt lgkmcnt(1)
	v_mfma_f32_16x16x32_bf16 v[132:135], v[86:89], v[140:143], v[132:135]
	v_add_u32_e32 v140, v176, v204
	v_lshlrev_b32_e32 v173, 16, v89
	v_and_b32_e32 v243, 0xffff0000, v89
	ds_read_b128 v[140:143], v140
	s_waitcnt lgkmcnt(1)
	v_mfma_f32_16x16x32_bf16 v[136:139], v[86:89], v[144:147], v[136:139]
	v_add_u32_e32 v144, v177, v204
	v_mul_f32_e32 v150, v173, v173
	v_mul_f32_e32 v148, v243, v243
	ds_read_b128 v[144:147], v144
	v_pk_add_f32 v[148:149], v[150:151], v[148:149]
	v_med3_f32 v150, v173, s78, v240
	v_med3_f32 v151, v243, s78, v240
	v_cvt_pk_fp8_f32 v155, v150, v151 op_sel:[0,0,1]
	s_waitcnt lgkmcnt(1)
	v_mfma_f32_16x16x32_bf16 v[132:135], v[86:89], v[140:143], v[132:135]
	v_add_f32_e64 v140, v152, v148
	v_add_f32_e64 v141, v153, v149
	s_waitcnt vmcnt(29)
	v_and_b32_e32 v143, 0xffff0000, v83
	v_and_b32_e32 v142, 0xffff0000, v82
	v_pk_add_f32 v[148:149], v[140:141], v[140:141] op_sel_hi:[0,1]
	s_waitcnt lgkmcnt(0)
	v_mfma_f32_16x16x32_bf16 v[136:139], v[86:89], v[144:147], v[136:139]
	v_lshlrev_b32_e32 v141, 16, v83
	v_lshlrev_b32_e32 v140, 16, v82
	v_pk_mul_f32 v[144:145], v[142:143], v[142:143]
	global_store_dwordx2 v[130:131], v[154:155], off offset:320
	v_pk_fma_f32 v[144:145], v[140:141], v[140:141], v[144:145]
	v_med3_f32 v140, v140, s78, v240
	v_med3_f32 v142, v142, s78, v240
	v_mov_b32_e32 v154, 0
	v_cvt_pk_fp8_f32 v154, v140, v142
	v_and_b32_e32 v151, 0xffff0000, v85
	v_and_b32_e32 v150, 0xffff0000, v84
	v_lshlrev_b32_e32 v147, 16, v85
	v_lshlrev_b32_e32 v146, 16, v84
	v_pk_mul_f32 v[152:153], v[150:151], v[150:151]
	v_add_f32_e32 v148, v144, v145
	v_pk_fma_f32 v[152:153], v[146:147], v[146:147], v[152:153]
	v_med3_f32 v140, v141, s78, v240
	v_med3_f32 v141, v143, s78, v240
	v_med3_f32 v144, v146, s78, v240
	v_med3_f32 v145, v150, s78, v240
	v_add_u32_e32 v146, v175, v205
	v_mov_b32_e32 v155, 0
	v_cvt_pk_fp8_f32 v154, v140, v141 op_sel:[0,0,1]
	ds_read_b128 v[140:143], v146
	v_cvt_pk_fp8_f32 v155, v144, v145
	v_med3_f32 v150, v147, s78, v240
	ds_read_b128 v[144:147], v146 offset:32768
	s_waitcnt lgkmcnt(1)
	v_mfma_f32_16x16x32_bf16 v[132:135], v[82:85], v[140:143], v[132:135]
	v_add_u32_e32 v140, v176, v205
	ds_read_b128 v[140:143], v140
	v_med3_f32 v151, v151, s78, v240
	s_waitcnt lgkmcnt(1)
	v_mfma_f32_16x16x32_bf16 v[136:139], v[82:85], v[144:147], v[136:139]
	v_add_u32_e32 v144, v177, v205
	ds_read_b128 v[144:147], v144
	v_cvt_pk_fp8_f32 v155, v150, v151 op_sel:[0,0,1]
	s_waitcnt lgkmcnt(1)
	v_mfma_f32_16x16x32_bf16 v[132:135], v[82:85], v[140:143], v[132:135]
	v_add_f32_e32 v140, v152, v148
	v_pk_add_f32 v[150:151], v[152:153], v[140:141] op_sel_hi:[1,0]
	global_store_dwordx2 v[130:131], v[154:155], off offset:352
	s_waitcnt lgkmcnt(0)
	v_mfma_f32_16x16x32_bf16 v[136:139], v[82:85], v[144:147], v[136:139]
	s_waitcnt vmcnt(30)
	v_lshlrev_b32_e32 v144, 16, v78
	v_and_b32_e32 v145, 0xffff0000, v78
	v_mul_f32_e32 v140, v144, v144
	v_add_u32_e32 v147, v175, v206
	v_pk_fma_f32 v[152:153], v[144:145], v[144:145], v[140:141] op_sel_hi:[1,1,0]
	v_lshlrev_b32_e32 v154, 16, v79
	ds_read_b128 v[140:143], v147
	v_and_b32_e32 v155, 0xffff0000, v79
	v_mul_f32_e32 v146, v154, v154
	v_pk_fma_f32 v[156:157], v[154:155], v[154:155], v[146:147] op_sel_hi:[1,1,0]
	v_med3_f32 v148, v144, s78, v240
	v_med3_f32 v150, v145, s78, v240
	ds_read_b128 v[144:147], v147 offset:32768
	s_waitcnt lgkmcnt(1)
	v_mfma_f32_16x16x32_bf16 v[132:135], v[78:81], v[140:143], v[132:135]
	v_add_u32_e32 v140, v176, v206
	ds_read_b128 v[140:143], v140
	global_store_dwordx2 v[130:131], v[158:159], off offset:288
	v_mov_b32_e32 v158, 0
	s_waitcnt lgkmcnt(1)
	v_mfma_f32_16x16x32_bf16 v[136:139], v[78:81], v[144:147], v[136:139]
	v_add_u32_e32 v144, v177, v206
	v_cvt_pk_fp8_f32 v158, v148, v150
	ds_read_b128 v[144:147], v144
	s_waitcnt lgkmcnt(1)
	v_mfma_f32_16x16x32_bf16 v[132:135], v[78:81], v[140:143], v[132:135]
	v_med3_f32 v140, v154, s78, v240
	v_med3_f32 v141, v155, s78, v240
	v_cvt_pk_fp8_f32 v158, v140, v141 op_sel:[0,0,1]
	v_lshlrev_b32_e32 v141, 16, v80
	v_and_b32_e32 v143, 0xffff0000, v80
	s_waitcnt lgkmcnt(0)
	v_mfma_f32_16x16x32_bf16 v[136:139], v[78:81], v[144:147], v[136:139]
	v_med3_f32 v142, v141, s78, v240
	v_med3_f32 v144, v143, s78, v240
	v_mov_b32_e32 v159, 0
	v_cvt_pk_fp8_f32 v159, v142, v144
	v_lshlrev_b32_e32 v145, 16, v81
	v_and_b32_e32 v147, 0xffff0000, v81
	v_med3_f32 v142, v145, s78, v240
	v_med3_f32 v144, v147, s78, v240
	s_waitcnt vmcnt(30)
	v_lshlrev_b32_e32 v160, 16, v75
	v_and_b32_e32 v161, 0xffff0000, v75
	v_cvt_pk_fp8_f32 v159, v142, v144 op_sel:[0,0,1]
	v_and_b32_e32 v142, 0xffff0000, v74
	v_mul_f32_e32 v152, v160, v160
	v_mul_f32_e32 v156, v161, v161
	v_lshlrev_b32_e32 v140, 16, v74
	v_pk_mul_f32 v[154:155], v[142:143], v[142:143]
	v_and_b32_e32 v146, 0xffff0000, v76
	v_pk_fma_f32 v[154:155], v[140:141], v[140:141], v[154:155]
	v_pk_add_f32 v[152:153], v[152:153], v[156:157]
	v_lshlrev_b32_e32 v144, 16, v76
	v_pk_add_f32 v[152:153], v[154:155], v[152:153]
	v_pk_mul_f32 v[154:155], v[146:147], v[146:147]
	v_med3_f32 v140, v140, s78, v240
	v_pk_fma_f32 v[154:155], v[144:145], v[144:145], v[154:155]
	v_med3_f32 v141, v142, s78, v240
	v_pk_add_f32 v[152:153], v[154:155], v[152:153]
	v_mov_b32_e32 v154, 0
	v_cvt_pk_fp8_f32 v154, v140, v141
	v_med3_f32 v140, v160, s78, v240
	v_med3_f32 v141, v161, s78, v240
	v_med3_f32 v145, v146, s78, v240
	v_add_u32_e32 v146, v175, v207
	v_cvt_pk_fp8_f32 v154, v140, v141 op_sel:[0,0,1]
	v_med3_f32 v144, v144, s78, v240
	ds_read_b128 v[140:143], v146
	v_mov_b32_e32 v155, 0
	v_cvt_pk_fp8_f32 v155, v144, v145
	ds_read_b128 v[144:147], v146 offset:32768
	s_waitcnt lgkmcnt(1)
	v_mfma_f32_16x16x32_bf16 v[132:135], v[74:77], v[140:143], v[132:135]
	v_add_u32_e32 v140, v176, v207
	v_lshlrev_b32_e32 v173, 16, v77
	v_and_b32_e32 v243, 0xffff0000, v77
	ds_read_b128 v[140:143], v140
	s_waitcnt lgkmcnt(1)
	v_mfma_f32_16x16x32_bf16 v[136:139], v[74:77], v[144:147], v[136:139]
	v_add_u32_e32 v144, v177, v207
	v_mul_f32_e32 v150, v173, v173
	v_mul_f32_e32 v148, v243, v243
	ds_read_b128 v[144:147], v144
	v_pk_add_f32 v[148:149], v[150:151], v[148:149]
	v_med3_f32 v150, v173, s78, v240
	v_med3_f32 v151, v243, s78, v240
	v_cvt_pk_fp8_f32 v155, v150, v151 op_sel:[0,0,1]
	s_waitcnt lgkmcnt(1)
	v_mfma_f32_16x16x32_bf16 v[132:135], v[74:77], v[140:143], v[132:135]
	v_add_f32_e64 v140, v152, v148
	v_add_f32_e64 v141, v153, v149
	s_waitcnt vmcnt(29)
	v_and_b32_e32 v143, 0xffff0000, v71
	v_and_b32_e32 v142, 0xffff0000, v70
	v_pk_add_f32 v[148:149], v[140:141], v[140:141] op_sel_hi:[0,1]
	s_waitcnt lgkmcnt(0)
	v_mfma_f32_16x16x32_bf16 v[136:139], v[74:77], v[144:147], v[136:139]
	v_lshlrev_b32_e32 v141, 16, v71
	v_lshlrev_b32_e32 v140, 16, v70
	v_pk_mul_f32 v[144:145], v[142:143], v[142:143]
	global_store_dwordx2 v[130:131], v[154:155], off offset:416
	v_pk_fma_f32 v[144:145], v[140:141], v[140:141], v[144:145]
	v_med3_f32 v140, v140, s78, v240
	v_med3_f32 v142, v142, s78, v240
	v_mov_b32_e32 v154, 0
	v_cvt_pk_fp8_f32 v154, v140, v142
	v_and_b32_e32 v151, 0xffff0000, v73
	v_and_b32_e32 v150, 0xffff0000, v72
	v_lshlrev_b32_e32 v147, 16, v73
	v_lshlrev_b32_e32 v146, 16, v72
	v_pk_mul_f32 v[152:153], v[150:151], v[150:151]
	v_add_f32_e32 v148, v144, v145
	v_pk_fma_f32 v[152:153], v[146:147], v[146:147], v[152:153]
	v_med3_f32 v140, v141, s78, v240
	v_med3_f32 v141, v143, s78, v240
	v_med3_f32 v144, v146, s78, v240
	v_med3_f32 v145, v150, s78, v240
	v_add_u32_e32 v146, v175, v208
	v_mov_b32_e32 v155, 0
	v_cvt_pk_fp8_f32 v154, v140, v141 op_sel:[0,0,1]
	ds_read_b128 v[140:143], v146
	v_cvt_pk_fp8_f32 v155, v144, v145
	v_med3_f32 v150, v147, s78, v240
	ds_read_b128 v[144:147], v146 offset:32768
	s_waitcnt lgkmcnt(1)
	v_mfma_f32_16x16x32_bf16 v[132:135], v[70:73], v[140:143], v[132:135]
	v_add_u32_e32 v140, v176, v208
	ds_read_b128 v[140:143], v140
	v_med3_f32 v151, v151, s78, v240
	s_waitcnt lgkmcnt(1)
	v_mfma_f32_16x16x32_bf16 v[136:139], v[70:73], v[144:147], v[136:139]
	v_add_u32_e32 v144, v177, v208
	ds_read_b128 v[144:147], v144
	v_cvt_pk_fp8_f32 v155, v150, v151 op_sel:[0,0,1]
	s_waitcnt lgkmcnt(1)
	v_mfma_f32_16x16x32_bf16 v[132:135], v[70:73], v[140:143], v[132:135]
	v_add_f32_e32 v140, v152, v148
	v_pk_add_f32 v[150:151], v[152:153], v[140:141] op_sel_hi:[1,0]
	global_store_dwordx2 v[130:131], v[154:155], off offset:448
	s_waitcnt lgkmcnt(0)
	v_mfma_f32_16x16x32_bf16 v[136:139], v[70:73], v[144:147], v[136:139]
	s_waitcnt vmcnt(30)
	v_lshlrev_b32_e32 v144, 16, v66
	v_and_b32_e32 v145, 0xffff0000, v66
	v_mul_f32_e32 v140, v144, v144
	v_add_u32_e32 v147, v175, v209
	v_pk_fma_f32 v[152:153], v[144:145], v[144:145], v[140:141] op_sel_hi:[1,1,0]
	v_lshlrev_b32_e32 v154, 16, v67
	ds_read_b128 v[140:143], v147
	v_and_b32_e32 v155, 0xffff0000, v67
	v_mul_f32_e32 v146, v154, v154
	v_pk_fma_f32 v[156:157], v[154:155], v[154:155], v[146:147] op_sel_hi:[1,1,0]
	v_med3_f32 v148, v144, s78, v240
	v_med3_f32 v150, v145, s78, v240
	ds_read_b128 v[144:147], v147 offset:32768
	s_waitcnt lgkmcnt(1)
	v_mfma_f32_16x16x32_bf16 v[132:135], v[66:69], v[140:143], v[132:135]
	v_add_u32_e32 v140, v176, v209
	ds_read_b128 v[140:143], v140
	global_store_dwordx2 v[130:131], v[158:159], off offset:384
	v_mov_b32_e32 v158, 0
	s_waitcnt lgkmcnt(1)
	v_mfma_f32_16x16x32_bf16 v[136:139], v[66:69], v[144:147], v[136:139]
	v_add_u32_e32 v144, v177, v209
	v_cvt_pk_fp8_f32 v158, v148, v150
	ds_read_b128 v[144:147], v144
	s_waitcnt lgkmcnt(1)
	v_mfma_f32_16x16x32_bf16 v[132:135], v[66:69], v[140:143], v[132:135]
	v_med3_f32 v140, v154, s78, v240
	v_med3_f32 v141, v155, s78, v240
	v_cvt_pk_fp8_f32 v158, v140, v141 op_sel:[0,0,1]
	v_lshlrev_b32_e32 v141, 16, v68
	v_and_b32_e32 v143, 0xffff0000, v68
	s_waitcnt lgkmcnt(0)
	v_mfma_f32_16x16x32_bf16 v[136:139], v[66:69], v[144:147], v[136:139]
	v_med3_f32 v142, v141, s78, v240
	v_med3_f32 v144, v143, s78, v240
	v_mov_b32_e32 v159, 0
	v_cvt_pk_fp8_f32 v159, v142, v144
	v_lshlrev_b32_e32 v145, 16, v69
	v_and_b32_e32 v147, 0xffff0000, v69
	v_med3_f32 v142, v145, s78, v240
	v_med3_f32 v144, v147, s78, v240
	s_waitcnt vmcnt(16)
	v_lshlrev_b32_e32 v160, 16, v63
	v_and_b32_e32 v161, 0xffff0000, v63
	v_cvt_pk_fp8_f32 v159, v142, v144 op_sel:[0,0,1]
	v_and_b32_e32 v142, 0xffff0000, v62
	v_mul_f32_e32 v152, v160, v160
	v_mul_f32_e32 v156, v161, v161
	v_lshlrev_b32_e32 v140, 16, v62
	v_pk_mul_f32 v[154:155], v[142:143], v[142:143]
	v_and_b32_e32 v146, 0xffff0000, v64
	v_pk_fma_f32 v[154:155], v[140:141], v[140:141], v[154:155]
	v_pk_add_f32 v[152:153], v[152:153], v[156:157]
	v_lshlrev_b32_e32 v144, 16, v64
	v_pk_add_f32 v[152:153], v[154:155], v[152:153]
	v_pk_mul_f32 v[154:155], v[146:147], v[146:147]
	v_med3_f32 v140, v140, s78, v240
	v_pk_fma_f32 v[154:155], v[144:145], v[144:145], v[154:155]
	v_med3_f32 v141, v142, s78, v240
	v_pk_add_f32 v[152:153], v[154:155], v[152:153]
	v_mov_b32_e32 v154, 0
	v_cvt_pk_fp8_f32 v154, v140, v141
	v_med3_f32 v140, v160, s78, v240
	v_med3_f32 v141, v161, s78, v240
	v_med3_f32 v145, v146, s78, v240
	v_add_u32_e32 v146, v175, v210
	v_cvt_pk_fp8_f32 v154, v140, v141 op_sel:[0,0,1]
	v_med3_f32 v144, v144, s78, v240
	ds_read_b128 v[140:143], v146
	v_mov_b32_e32 v155, 0
	v_cvt_pk_fp8_f32 v155, v144, v145
	ds_read_b128 v[144:147], v146 offset:32768
	s_waitcnt lgkmcnt(1)
	v_mfma_f32_16x16x32_bf16 v[132:135], v[62:65], v[140:143], v[132:135]
	v_add_u32_e32 v140, v176, v210
	v_lshlrev_b32_e32 v173, 16, v65
	v_and_b32_e32 v243, 0xffff0000, v65
	ds_read_b128 v[140:143], v140
	s_waitcnt lgkmcnt(1)
	v_mfma_f32_16x16x32_bf16 v[136:139], v[62:65], v[144:147], v[136:139]
	v_add_u32_e32 v144, v177, v210
	v_mul_f32_e32 v150, v173, v173
	v_mul_f32_e32 v148, v243, v243
	ds_read_b128 v[144:147], v144
	v_pk_add_f32 v[148:149], v[150:151], v[148:149]
	v_med3_f32 v150, v173, s78, v240
	v_med3_f32 v151, v243, s78, v240
	v_cvt_pk_fp8_f32 v155, v150, v151 op_sel:[0,0,1]
	s_waitcnt lgkmcnt(1)
	v_mfma_f32_16x16x32_bf16 v[132:135], v[62:65], v[140:143], v[132:135]
	v_add_f32_e64 v140, v152, v148
	v_add_f32_e64 v141, v153, v149
	s_waitcnt vmcnt(15)
	v_and_b32_e32 v143, 0xffff0000, v59
	v_and_b32_e32 v142, 0xffff0000, v58
	v_pk_add_f32 v[148:149], v[140:141], v[140:141] op_sel_hi:[0,1]
	s_waitcnt lgkmcnt(0)
	v_mfma_f32_16x16x32_bf16 v[136:139], v[62:65], v[144:147], v[136:139]
	v_lshlrev_b32_e32 v141, 16, v59
	v_lshlrev_b32_e32 v140, 16, v58
	v_pk_mul_f32 v[144:145], v[142:143], v[142:143]
	global_store_dwordx2 v[130:131], v[154:155], off offset:512
	v_pk_fma_f32 v[144:145], v[140:141], v[140:141], v[144:145]
	v_med3_f32 v140, v140, s78, v240
	v_med3_f32 v142, v142, s78, v240
	v_mov_b32_e32 v154, 0
	v_cvt_pk_fp8_f32 v154, v140, v142
	v_and_b32_e32 v151, 0xffff0000, v61
	v_and_b32_e32 v150, 0xffff0000, v60
	v_lshlrev_b32_e32 v147, 16, v61
	v_lshlrev_b32_e32 v146, 16, v60
	v_pk_mul_f32 v[152:153], v[150:151], v[150:151]
	v_add_f32_e32 v148, v144, v145
	v_pk_fma_f32 v[152:153], v[146:147], v[146:147], v[152:153]
	v_med3_f32 v140, v141, s78, v240
	v_med3_f32 v141, v143, s78, v240
	v_med3_f32 v144, v146, s78, v240
	v_med3_f32 v145, v150, s78, v240
	v_add_u32_e32 v146, v175, v211
	v_mov_b32_e32 v155, 0
	v_cvt_pk_fp8_f32 v154, v140, v141 op_sel:[0,0,1]
	ds_read_b128 v[140:143], v146
	v_cvt_pk_fp8_f32 v155, v144, v145
	v_med3_f32 v150, v147, s78, v240
	ds_read_b128 v[144:147], v146 offset:32768
	s_waitcnt lgkmcnt(1)
	v_mfma_f32_16x16x32_bf16 v[132:135], v[58:61], v[140:143], v[132:135]
	v_add_u32_e32 v140, v176, v211
	ds_read_b128 v[140:143], v140
	v_med3_f32 v151, v151, s78, v240
	s_waitcnt lgkmcnt(1)
	v_mfma_f32_16x16x32_bf16 v[136:139], v[58:61], v[144:147], v[136:139]
	v_add_u32_e32 v144, v177, v211
	ds_read_b128 v[144:147], v144
	v_cvt_pk_fp8_f32 v155, v150, v151 op_sel:[0,0,1]
	s_waitcnt lgkmcnt(1)
	v_mfma_f32_16x16x32_bf16 v[132:135], v[58:61], v[140:143], v[132:135]
	v_add_f32_e32 v140, v152, v148
	v_pk_add_f32 v[150:151], v[152:153], v[140:141] op_sel_hi:[1,0]
	global_store_dwordx2 v[130:131], v[154:155], off offset:544
	s_waitcnt lgkmcnt(0)
	v_mfma_f32_16x16x32_bf16 v[136:139], v[58:61], v[144:147], v[136:139]
	v_lshlrev_b32_e32 v144, 16, v54
	v_and_b32_e32 v145, 0xffff0000, v54
	v_mul_f32_e32 v140, v144, v144
	v_add_u32_e32 v147, v175, v212
	v_pk_fma_f32 v[152:153], v[144:145], v[144:145], v[140:141] op_sel_hi:[1,1,0]
	v_lshlrev_b32_e32 v154, 16, v55
	ds_read_b128 v[140:143], v147
	v_and_b32_e32 v155, 0xffff0000, v55
	v_mul_f32_e32 v146, v154, v154
	v_pk_fma_f32 v[156:157], v[154:155], v[154:155], v[146:147] op_sel_hi:[1,1,0]
	v_med3_f32 v148, v144, s78, v240
	v_med3_f32 v150, v145, s78, v240
	ds_read_b128 v[144:147], v147 offset:32768
	s_waitcnt lgkmcnt(1)
	v_mfma_f32_16x16x32_bf16 v[132:135], v[54:57], v[140:143], v[132:135]
	v_add_u32_e32 v140, v176, v212
	ds_read_b128 v[140:143], v140
	global_store_dwordx2 v[130:131], v[158:159], off offset:480
	v_mov_b32_e32 v158, 0
	s_waitcnt lgkmcnt(1)
	v_mfma_f32_16x16x32_bf16 v[136:139], v[54:57], v[144:147], v[136:139]
	v_add_u32_e32 v144, v177, v212
	v_cvt_pk_fp8_f32 v158, v148, v150
	ds_read_b128 v[144:147], v144
	s_waitcnt lgkmcnt(1)
	v_mfma_f32_16x16x32_bf16 v[132:135], v[54:57], v[140:143], v[132:135]
	v_med3_f32 v140, v154, s78, v240
	v_med3_f32 v141, v155, s78, v240
	v_cvt_pk_fp8_f32 v158, v140, v141 op_sel:[0,0,1]
	v_lshlrev_b32_e32 v141, 16, v56
	v_and_b32_e32 v143, 0xffff0000, v56
	s_waitcnt lgkmcnt(0)
	v_mfma_f32_16x16x32_bf16 v[136:139], v[54:57], v[144:147], v[136:139]
	v_med3_f32 v142, v141, s78, v240
	v_med3_f32 v144, v143, s78, v240
	v_mov_b32_e32 v159, 0
	v_cvt_pk_fp8_f32 v159, v142, v144
	v_lshlrev_b32_e32 v145, 16, v57
	v_and_b32_e32 v147, 0xffff0000, v57
	v_med3_f32 v142, v145, s78, v240
	v_med3_f32 v144, v147, s78, v240
	v_lshlrev_b32_e32 v160, 16, v51
	v_and_b32_e32 v161, 0xffff0000, v51
	v_cvt_pk_fp8_f32 v159, v142, v144 op_sel:[0,0,1]
	v_and_b32_e32 v142, 0xffff0000, v50
	v_mul_f32_e32 v152, v160, v160
	v_mul_f32_e32 v156, v161, v161
	v_lshlrev_b32_e32 v140, 16, v50
	v_pk_mul_f32 v[154:155], v[142:143], v[142:143]
	v_and_b32_e32 v146, 0xffff0000, v52
	v_pk_fma_f32 v[154:155], v[140:141], v[140:141], v[154:155]
	v_pk_add_f32 v[152:153], v[152:153], v[156:157]
	v_lshlrev_b32_e32 v144, 16, v52
	v_pk_add_f32 v[152:153], v[154:155], v[152:153]
	v_pk_mul_f32 v[154:155], v[146:147], v[146:147]
	v_med3_f32 v140, v140, s78, v240
	v_pk_fma_f32 v[154:155], v[144:145], v[144:145], v[154:155]
	v_med3_f32 v141, v142, s78, v240
	v_pk_add_f32 v[152:153], v[154:155], v[152:153]
	v_mov_b32_e32 v154, 0
	v_cvt_pk_fp8_f32 v154, v140, v141
	v_med3_f32 v140, v160, s78, v240
	v_med3_f32 v141, v161, s78, v240
	v_med3_f32 v145, v146, s78, v240
	v_add_u32_e32 v146, v175, v213
	v_cvt_pk_fp8_f32 v154, v140, v141 op_sel:[0,0,1]
	v_med3_f32 v144, v144, s78, v240
	ds_read_b128 v[140:143], v146
	v_mov_b32_e32 v155, 0
	v_cvt_pk_fp8_f32 v155, v144, v145
	ds_read_b128 v[144:147], v146 offset:32768
	s_waitcnt lgkmcnt(1)
	v_mfma_f32_16x16x32_bf16 v[132:135], v[50:53], v[140:143], v[132:135]
	v_add_u32_e32 v140, v176, v213
	v_lshlrev_b32_e32 v173, 16, v53
	v_and_b32_e32 v243, 0xffff0000, v53
	ds_read_b128 v[140:143], v140
	s_waitcnt lgkmcnt(1)
	v_mfma_f32_16x16x32_bf16 v[136:139], v[50:53], v[144:147], v[136:139]
	v_add_u32_e32 v144, v177, v213
	v_mul_f32_e32 v150, v173, v173
	v_mul_f32_e32 v148, v243, v243
	ds_read_b128 v[144:147], v144
	v_pk_add_f32 v[148:149], v[150:151], v[148:149]
	v_med3_f32 v150, v173, s78, v240
	v_med3_f32 v151, v243, s78, v240
	v_cvt_pk_fp8_f32 v155, v150, v151 op_sel:[0,0,1]
	s_waitcnt lgkmcnt(1)
	v_mfma_f32_16x16x32_bf16 v[132:135], v[50:53], v[140:143], v[132:135]
	v_add_f32_e64 v140, v152, v148
	v_add_f32_e64 v141, v153, v149
	v_and_b32_e32 v143, 0xffff0000, v47
	v_and_b32_e32 v142, 0xffff0000, v46
	v_pk_add_f32 v[148:149], v[140:141], v[140:141] op_sel_hi:[0,1]
	s_waitcnt lgkmcnt(0)
	v_mfma_f32_16x16x32_bf16 v[136:139], v[50:53], v[144:147], v[136:139]
	v_lshlrev_b32_e32 v141, 16, v47
	v_lshlrev_b32_e32 v140, 16, v46
	v_pk_mul_f32 v[144:145], v[142:143], v[142:143]
	global_store_dwordx2 v[130:131], v[154:155], off offset:608
	v_pk_fma_f32 v[144:145], v[140:141], v[140:141], v[144:145]
	v_med3_f32 v140, v140, s78, v240
	v_med3_f32 v142, v142, s78, v240
	v_mov_b32_e32 v154, 0
	v_cvt_pk_fp8_f32 v154, v140, v142
	v_and_b32_e32 v151, 0xffff0000, v49
	v_and_b32_e32 v150, 0xffff0000, v48
	v_lshlrev_b32_e32 v147, 16, v49
	v_lshlrev_b32_e32 v146, 16, v48
	v_pk_mul_f32 v[152:153], v[150:151], v[150:151]
	v_add_f32_e32 v148, v144, v145
	v_pk_fma_f32 v[152:153], v[146:147], v[146:147], v[152:153]
	v_med3_f32 v140, v141, s78, v240
	v_med3_f32 v141, v143, s78, v240
	v_med3_f32 v144, v146, s78, v240
	v_med3_f32 v145, v150, s78, v240
	v_add_u32_e32 v146, v175, v214
	v_mov_b32_e32 v155, 0
	v_cvt_pk_fp8_f32 v154, v140, v141 op_sel:[0,0,1]
	ds_read_b128 v[140:143], v146
	v_cvt_pk_fp8_f32 v155, v144, v145
	v_med3_f32 v150, v147, s78, v240
	ds_read_b128 v[144:147], v146 offset:32768
	s_waitcnt lgkmcnt(1)
	v_mfma_f32_16x16x32_bf16 v[132:135], v[46:49], v[140:143], v[132:135]
	v_add_u32_e32 v140, v176, v214
	ds_read_b128 v[140:143], v140
	v_med3_f32 v151, v151, s78, v240
	s_waitcnt lgkmcnt(1)
	v_mfma_f32_16x16x32_bf16 v[136:139], v[46:49], v[144:147], v[136:139]
	v_add_u32_e32 v144, v177, v214
	ds_read_b128 v[144:147], v144
	v_cvt_pk_fp8_f32 v155, v150, v151 op_sel:[0,0,1]
	s_waitcnt lgkmcnt(1)
	v_mfma_f32_16x16x32_bf16 v[132:135], v[46:49], v[140:143], v[132:135]
	v_add_f32_e32 v140, v152, v148
	v_pk_add_f32 v[150:151], v[152:153], v[140:141] op_sel_hi:[1,0]
	global_store_dwordx2 v[130:131], v[154:155], off offset:640
	s_waitcnt lgkmcnt(0)
	v_mfma_f32_16x16x32_bf16 v[136:139], v[46:49], v[144:147], v[136:139]
	v_lshlrev_b32_e32 v144, 16, v42
	v_and_b32_e32 v145, 0xffff0000, v42
	v_mul_f32_e32 v140, v144, v144
	v_add_u32_e32 v147, v175, v215
	v_pk_fma_f32 v[152:153], v[144:145], v[144:145], v[140:141] op_sel_hi:[1,1,0]
	v_lshlrev_b32_e32 v154, 16, v43
	ds_read_b128 v[140:143], v147
	v_and_b32_e32 v155, 0xffff0000, v43
	v_mul_f32_e32 v146, v154, v154
	v_pk_fma_f32 v[156:157], v[154:155], v[154:155], v[146:147] op_sel_hi:[1,1,0]
	v_med3_f32 v148, v144, s78, v240
	v_med3_f32 v150, v145, s78, v240
	ds_read_b128 v[144:147], v147 offset:32768
	s_waitcnt lgkmcnt(1)
	v_mfma_f32_16x16x32_bf16 v[132:135], v[42:45], v[140:143], v[132:135]
	v_add_u32_e32 v140, v176, v215
	ds_read_b128 v[140:143], v140
	global_store_dwordx2 v[130:131], v[158:159], off offset:576
	v_mov_b32_e32 v158, 0
	s_waitcnt lgkmcnt(1)
	v_mfma_f32_16x16x32_bf16 v[136:139], v[42:45], v[144:147], v[136:139]
	v_add_u32_e32 v144, v177, v215
	v_cvt_pk_fp8_f32 v158, v148, v150
	ds_read_b128 v[144:147], v144
	s_waitcnt lgkmcnt(1)
	v_mfma_f32_16x16x32_bf16 v[132:135], v[42:45], v[140:143], v[132:135]
	v_med3_f32 v140, v154, s78, v240
	v_med3_f32 v141, v155, s78, v240
	v_cvt_pk_fp8_f32 v158, v140, v141 op_sel:[0,0,1]
	v_lshlrev_b32_e32 v141, 16, v44
	v_and_b32_e32 v143, 0xffff0000, v44
	s_waitcnt lgkmcnt(0)
	v_mfma_f32_16x16x32_bf16 v[136:139], v[42:45], v[144:147], v[136:139]
	v_med3_f32 v142, v141, s78, v240
	v_med3_f32 v144, v143, s78, v240
	v_mov_b32_e32 v159, 0
	v_cvt_pk_fp8_f32 v159, v142, v144
	v_lshlrev_b32_e32 v145, 16, v45
	v_and_b32_e32 v147, 0xffff0000, v45
	v_med3_f32 v142, v145, s78, v240
	v_med3_f32 v144, v147, s78, v240
	v_lshlrev_b32_e32 v160, 16, v39
	v_and_b32_e32 v161, 0xffff0000, v39
	v_cvt_pk_fp8_f32 v159, v142, v144 op_sel:[0,0,1]
	v_and_b32_e32 v142, 0xffff0000, v38
	v_mul_f32_e32 v152, v160, v160
	v_mul_f32_e32 v156, v161, v161
	v_lshlrev_b32_e32 v140, 16, v38
	v_pk_mul_f32 v[154:155], v[142:143], v[142:143]
	v_and_b32_e32 v146, 0xffff0000, v40
	v_pk_fma_f32 v[154:155], v[140:141], v[140:141], v[154:155]
	v_pk_add_f32 v[152:153], v[152:153], v[156:157]
	v_lshlrev_b32_e32 v144, 16, v40
	v_pk_add_f32 v[152:153], v[154:155], v[152:153]
	v_pk_mul_f32 v[154:155], v[146:147], v[146:147]
	v_med3_f32 v140, v140, s78, v240
	v_pk_fma_f32 v[154:155], v[144:145], v[144:145], v[154:155]
	v_med3_f32 v141, v142, s78, v240
	v_pk_add_f32 v[152:153], v[154:155], v[152:153]
	v_mov_b32_e32 v154, 0
	v_cvt_pk_fp8_f32 v154, v140, v141
	v_med3_f32 v140, v160, s78, v240
	v_med3_f32 v141, v161, s78, v240
	v_med3_f32 v145, v146, s78, v240
	v_add_u32_e32 v146, v175, v216
	v_cvt_pk_fp8_f32 v154, v140, v141 op_sel:[0,0,1]
	v_med3_f32 v144, v144, s78, v240
	ds_read_b128 v[140:143], v146
	v_mov_b32_e32 v155, 0
	v_cvt_pk_fp8_f32 v155, v144, v145
	ds_read_b128 v[144:147], v146 offset:32768
	s_waitcnt lgkmcnt(1)
	v_mfma_f32_16x16x32_bf16 v[132:135], v[38:41], v[140:143], v[132:135]
	v_add_u32_e32 v140, v176, v216
	v_lshlrev_b32_e32 v173, 16, v41
	v_and_b32_e32 v243, 0xffff0000, v41
	ds_read_b128 v[140:143], v140
	s_waitcnt lgkmcnt(1)
	v_mfma_f32_16x16x32_bf16 v[136:139], v[38:41], v[144:147], v[136:139]
	v_add_u32_e32 v144, v177, v216
	v_mul_f32_e32 v150, v173, v173
	v_mul_f32_e32 v148, v243, v243
	ds_read_b128 v[144:147], v144
	v_pk_add_f32 v[148:149], v[150:151], v[148:149]
	v_med3_f32 v150, v173, s78, v240
	v_med3_f32 v151, v243, s78, v240
	v_cvt_pk_fp8_f32 v155, v150, v151 op_sel:[0,0,1]
	s_waitcnt lgkmcnt(1)
	v_mfma_f32_16x16x32_bf16 v[132:135], v[38:41], v[140:143], v[132:135]
	v_add_f32_e64 v140, v152, v148
	v_add_f32_e64 v141, v153, v149
	v_and_b32_e32 v143, 0xffff0000, v35
	v_and_b32_e32 v142, 0xffff0000, v34
	v_pk_add_f32 v[148:149], v[140:141], v[140:141] op_sel_hi:[0,1]
	s_waitcnt lgkmcnt(0)
	v_mfma_f32_16x16x32_bf16 v[136:139], v[38:41], v[144:147], v[136:139]
	v_lshlrev_b32_e32 v141, 16, v35
	v_lshlrev_b32_e32 v140, 16, v34
	v_pk_mul_f32 v[144:145], v[142:143], v[142:143]
	global_store_dwordx2 v[130:131], v[154:155], off offset:704
	v_pk_fma_f32 v[144:145], v[140:141], v[140:141], v[144:145]
	v_med3_f32 v140, v140, s78, v240
	v_med3_f32 v142, v142, s78, v240
	v_mov_b32_e32 v154, 0
	v_cvt_pk_fp8_f32 v154, v140, v142
	v_and_b32_e32 v151, 0xffff0000, v37
	v_and_b32_e32 v150, 0xffff0000, v36
	v_lshlrev_b32_e32 v147, 16, v37
	v_lshlrev_b32_e32 v146, 16, v36
	v_pk_mul_f32 v[152:153], v[150:151], v[150:151]
	v_add_f32_e32 v148, v144, v145
	v_pk_fma_f32 v[152:153], v[146:147], v[146:147], v[152:153]
	v_med3_f32 v140, v141, s78, v240
	v_med3_f32 v141, v143, s78, v240
	v_med3_f32 v144, v146, s78, v240
	v_med3_f32 v145, v150, s78, v240
	v_add_u32_e32 v146, v175, v217
	v_mov_b32_e32 v155, 0
	v_cvt_pk_fp8_f32 v154, v140, v141 op_sel:[0,0,1]
	ds_read_b128 v[140:143], v146
	v_cvt_pk_fp8_f32 v155, v144, v145
	v_med3_f32 v150, v147, s78, v240
	ds_read_b128 v[144:147], v146 offset:32768
	s_waitcnt lgkmcnt(1)
	v_mfma_f32_16x16x32_bf16 v[132:135], v[34:37], v[140:143], v[132:135]
	v_add_u32_e32 v140, v176, v217
	ds_read_b128 v[140:143], v140
	v_med3_f32 v151, v151, s78, v240
	s_waitcnt lgkmcnt(1)
	v_mfma_f32_16x16x32_bf16 v[136:139], v[34:37], v[144:147], v[136:139]
	v_add_u32_e32 v144, v177, v217
	ds_read_b128 v[144:147], v144
	v_cvt_pk_fp8_f32 v155, v150, v151 op_sel:[0,0,1]
	s_waitcnt lgkmcnt(1)
	v_mfma_f32_16x16x32_bf16 v[132:135], v[34:37], v[140:143], v[132:135]
	v_add_f32_e32 v140, v152, v148
	v_pk_add_f32 v[150:151], v[152:153], v[140:141] op_sel_hi:[1,0]
	global_store_dwordx2 v[130:131], v[154:155], off offset:736
	s_waitcnt lgkmcnt(0)
	v_mfma_f32_16x16x32_bf16 v[136:139], v[34:37], v[144:147], v[136:139]
	v_lshlrev_b32_e32 v144, 16, v30
	v_and_b32_e32 v145, 0xffff0000, v30
	v_mul_f32_e32 v140, v144, v144
	v_add_u32_e32 v147, v175, v219
	v_pk_fma_f32 v[152:153], v[144:145], v[144:145], v[140:141] op_sel_hi:[1,1,0]
	v_lshlrev_b32_e32 v154, 16, v31
	ds_read_b128 v[140:143], v147
	v_and_b32_e32 v155, 0xffff0000, v31
	v_mul_f32_e32 v146, v154, v154
	v_pk_fma_f32 v[156:157], v[154:155], v[154:155], v[146:147] op_sel_hi:[1,1,0]
	v_med3_f32 v148, v144, s78, v240
	v_med3_f32 v150, v145, s78, v240
	ds_read_b128 v[144:147], v147 offset:32768
	s_waitcnt lgkmcnt(1)
	v_mfma_f32_16x16x32_bf16 v[132:135], v[30:33], v[140:143], v[132:135]
	v_add_u32_e32 v140, v176, v219
	ds_read_b128 v[140:143], v140
	global_store_dwordx2 v[130:131], v[158:159], off offset:672
	v_mov_b32_e32 v158, 0
	s_waitcnt lgkmcnt(1)
	v_mfma_f32_16x16x32_bf16 v[136:139], v[30:33], v[144:147], v[136:139]
	v_add_u32_e32 v144, v177, v219
	v_cvt_pk_fp8_f32 v158, v148, v150
	ds_read_b128 v[144:147], v144
	s_waitcnt lgkmcnt(1)
	v_mfma_f32_16x16x32_bf16 v[132:135], v[30:33], v[140:143], v[132:135]
	v_med3_f32 v140, v154, s78, v240
	v_med3_f32 v141, v155, s78, v240
	v_cvt_pk_fp8_f32 v158, v140, v141 op_sel:[0,0,1]
	v_lshlrev_b32_e32 v141, 16, v32
	v_and_b32_e32 v143, 0xffff0000, v32
	s_waitcnt lgkmcnt(0)
	v_mfma_f32_16x16x32_bf16 v[136:139], v[30:33], v[144:147], v[136:139]
	v_med3_f32 v142, v141, s78, v240
	v_med3_f32 v144, v143, s78, v240
	v_mov_b32_e32 v159, 0
	v_cvt_pk_fp8_f32 v159, v142, v144
	v_lshlrev_b32_e32 v145, 16, v33
	v_and_b32_e32 v147, 0xffff0000, v33
	v_med3_f32 v142, v145, s78, v240
	v_med3_f32 v144, v147, s78, v240
	v_lshlrev_b32_e32 v160, 16, v27
	v_and_b32_e32 v161, 0xffff0000, v27
	v_cvt_pk_fp8_f32 v159, v142, v144 op_sel:[0,0,1]
	v_and_b32_e32 v142, 0xffff0000, v26
	v_mul_f32_e32 v152, v160, v160
	v_mul_f32_e32 v156, v161, v161
	v_lshlrev_b32_e32 v140, 16, v26
	v_pk_mul_f32 v[154:155], v[142:143], v[142:143]
	v_and_b32_e32 v146, 0xffff0000, v28
	v_pk_fma_f32 v[154:155], v[140:141], v[140:141], v[154:155]
	v_pk_add_f32 v[152:153], v[152:153], v[156:157]
	v_lshlrev_b32_e32 v144, 16, v28
	v_pk_add_f32 v[152:153], v[154:155], v[152:153]
	v_pk_mul_f32 v[154:155], v[146:147], v[146:147]
	v_med3_f32 v140, v140, s78, v240
	v_pk_fma_f32 v[154:155], v[144:145], v[144:145], v[154:155]
	v_med3_f32 v141, v142, s78, v240
	v_pk_add_f32 v[152:153], v[154:155], v[152:153]
	v_mov_b32_e32 v154, 0
	v_cvt_pk_fp8_f32 v154, v140, v141
	v_med3_f32 v140, v160, s78, v240
	v_med3_f32 v141, v161, s78, v240
	v_med3_f32 v145, v146, s78, v240
	v_add_u32_e32 v146, v175, v220
	v_cvt_pk_fp8_f32 v154, v140, v141 op_sel:[0,0,1]
	v_med3_f32 v144, v144, s78, v240
	ds_read_b128 v[140:143], v146
	v_mov_b32_e32 v155, 0
	v_cvt_pk_fp8_f32 v155, v144, v145
	ds_read_b128 v[144:147], v146 offset:32768
	s_waitcnt lgkmcnt(1)
	v_mfma_f32_16x16x32_bf16 v[132:135], v[26:29], v[140:143], v[132:135]
	v_add_u32_e32 v140, v176, v220
	v_lshlrev_b32_e32 v173, 16, v29
	v_and_b32_e32 v243, 0xffff0000, v29
	ds_read_b128 v[140:143], v140
	s_waitcnt lgkmcnt(1)
	v_mfma_f32_16x16x32_bf16 v[136:139], v[26:29], v[144:147], v[136:139]
	v_add_u32_e32 v144, v177, v220
	v_mul_f32_e32 v150, v173, v173
	v_mul_f32_e32 v148, v243, v243
	ds_read_b128 v[144:147], v144
	v_pk_add_f32 v[148:149], v[150:151], v[148:149]
	v_med3_f32 v150, v173, s78, v240
	v_med3_f32 v151, v243, s78, v240
	v_cvt_pk_fp8_f32 v155, v150, v151 op_sel:[0,0,1]
	s_waitcnt lgkmcnt(1)
	v_mfma_f32_16x16x32_bf16 v[132:135], v[26:29], v[140:143], v[132:135]
	v_add_f32_e64 v140, v152, v148
	v_add_f32_e64 v141, v153, v149
	v_and_b32_e32 v143, 0xffff0000, v23
	v_and_b32_e32 v142, 0xffff0000, v22
	v_pk_add_f32 v[148:149], v[140:141], v[140:141] op_sel_hi:[0,1]
	s_waitcnt lgkmcnt(0)
	v_mfma_f32_16x16x32_bf16 v[136:139], v[26:29], v[144:147], v[136:139]
	v_lshlrev_b32_e32 v141, 16, v23
	v_lshlrev_b32_e32 v140, 16, v22
	v_pk_mul_f32 v[144:145], v[142:143], v[142:143]
	global_store_dwordx2 v[130:131], v[154:155], off offset:800
	v_pk_fma_f32 v[144:145], v[140:141], v[140:141], v[144:145]
	v_med3_f32 v140, v140, s78, v240
	v_med3_f32 v142, v142, s78, v240
	v_mov_b32_e32 v154, 0
	v_cvt_pk_fp8_f32 v154, v140, v142
	v_and_b32_e32 v151, 0xffff0000, v25
	v_and_b32_e32 v150, 0xffff0000, v24
	v_lshlrev_b32_e32 v147, 16, v25
	v_lshlrev_b32_e32 v146, 16, v24
	v_pk_mul_f32 v[152:153], v[150:151], v[150:151]
	v_add_f32_e32 v148, v144, v145
	v_pk_fma_f32 v[152:153], v[146:147], v[146:147], v[152:153]
	v_med3_f32 v140, v141, s78, v240
	v_med3_f32 v141, v143, s78, v240
	v_med3_f32 v144, v146, s78, v240
	v_med3_f32 v145, v150, s78, v240
	v_add_u32_e32 v146, v175, v221
	v_mov_b32_e32 v155, 0
	v_cvt_pk_fp8_f32 v154, v140, v141 op_sel:[0,0,1]
	ds_read_b128 v[140:143], v146
	v_cvt_pk_fp8_f32 v155, v144, v145
	v_med3_f32 v150, v147, s78, v240
	ds_read_b128 v[144:147], v146 offset:32768
	s_waitcnt lgkmcnt(1)
	v_mfma_f32_16x16x32_bf16 v[132:135], v[22:25], v[140:143], v[132:135]
	v_add_u32_e32 v140, v176, v221
	ds_read_b128 v[140:143], v140
	v_med3_f32 v151, v151, s78, v240
	s_waitcnt lgkmcnt(1)
	v_mfma_f32_16x16x32_bf16 v[136:139], v[22:25], v[144:147], v[136:139]
	v_add_u32_e32 v144, v177, v221
	ds_read_b128 v[144:147], v144
	v_cvt_pk_fp8_f32 v155, v150, v151 op_sel:[0,0,1]
	s_waitcnt lgkmcnt(1)
	v_mfma_f32_16x16x32_bf16 v[132:135], v[22:25], v[140:143], v[132:135]
	v_add_f32_e32 v140, v152, v148
	v_pk_add_f32 v[150:151], v[152:153], v[140:141] op_sel_hi:[1,0]
	global_store_dwordx2 v[130:131], v[154:155], off offset:832
	s_waitcnt lgkmcnt(0)
	v_mfma_f32_16x16x32_bf16 v[136:139], v[22:25], v[144:147], v[136:139]
	v_lshlrev_b32_e32 v144, 16, v18
	v_and_b32_e32 v145, 0xffff0000, v18
	v_mul_f32_e32 v140, v144, v144
	v_add_u32_e32 v147, v175, v222
	v_pk_fma_f32 v[152:153], v[144:145], v[144:145], v[140:141] op_sel_hi:[1,1,0]
	v_lshlrev_b32_e32 v154, 16, v19
	ds_read_b128 v[140:143], v147
	v_and_b32_e32 v155, 0xffff0000, v19
	v_mul_f32_e32 v146, v154, v154
	v_pk_fma_f32 v[156:157], v[154:155], v[154:155], v[146:147] op_sel_hi:[1,1,0]
	v_med3_f32 v148, v144, s78, v240
	v_med3_f32 v150, v145, s78, v240
	ds_read_b128 v[144:147], v147 offset:32768
	s_waitcnt lgkmcnt(1)
	v_mfma_f32_16x16x32_bf16 v[132:135], v[18:21], v[140:143], v[132:135]
	v_add_u32_e32 v140, v176, v222
	ds_read_b128 v[140:143], v140
	global_store_dwordx2 v[130:131], v[158:159], off offset:768
	v_mov_b32_e32 v158, 0
	s_waitcnt lgkmcnt(1)
	v_mfma_f32_16x16x32_bf16 v[136:139], v[18:21], v[144:147], v[136:139]
	v_add_u32_e32 v144, v177, v222
	v_cvt_pk_fp8_f32 v158, v148, v150
	ds_read_b128 v[144:147], v144
	s_waitcnt lgkmcnt(1)
	v_mfma_f32_16x16x32_bf16 v[132:135], v[18:21], v[140:143], v[132:135]
	v_med3_f32 v140, v154, s78, v240
	v_med3_f32 v141, v155, s78, v240
	v_cvt_pk_fp8_f32 v158, v140, v141 op_sel:[0,0,1]
	v_lshlrev_b32_e32 v141, 16, v20
	v_and_b32_e32 v143, 0xffff0000, v20
	s_waitcnt lgkmcnt(0)
	v_mfma_f32_16x16x32_bf16 v[136:139], v[18:21], v[144:147], v[136:139]
	v_med3_f32 v142, v141, s78, v240
	v_med3_f32 v144, v143, s78, v240
	v_mov_b32_e32 v159, 0
	v_cvt_pk_fp8_f32 v159, v142, v144
	v_lshlrev_b32_e32 v145, 16, v21
	v_and_b32_e32 v147, 0xffff0000, v21
	v_med3_f32 v142, v145, s78, v240
	v_med3_f32 v144, v147, s78, v240
	v_lshlrev_b32_e32 v160, 16, v15
	v_and_b32_e32 v161, 0xffff0000, v15
	v_cvt_pk_fp8_f32 v159, v142, v144 op_sel:[0,0,1]
	v_and_b32_e32 v142, 0xffff0000, v14
	v_mul_f32_e32 v152, v160, v160
	v_mul_f32_e32 v156, v161, v161
	v_lshlrev_b32_e32 v140, 16, v14
	v_pk_mul_f32 v[154:155], v[142:143], v[142:143]
	v_and_b32_e32 v146, 0xffff0000, v16
	v_pk_fma_f32 v[154:155], v[140:141], v[140:141], v[154:155]
	v_pk_add_f32 v[152:153], v[152:153], v[156:157]
	v_lshlrev_b32_e32 v144, 16, v16
	v_pk_add_f32 v[152:153], v[154:155], v[152:153]
	v_pk_mul_f32 v[154:155], v[146:147], v[146:147]
	v_med3_f32 v140, v140, s78, v240
	v_pk_fma_f32 v[154:155], v[144:145], v[144:145], v[154:155]
	v_med3_f32 v141, v142, s78, v240
	v_pk_add_f32 v[152:153], v[154:155], v[152:153]
	v_mov_b32_e32 v154, 0
	v_cvt_pk_fp8_f32 v154, v140, v141
	v_med3_f32 v140, v160, s78, v240
	v_med3_f32 v141, v161, s78, v240
	v_med3_f32 v145, v146, s78, v240
	v_add_u32_e32 v146, v175, v223
	v_cvt_pk_fp8_f32 v154, v140, v141 op_sel:[0,0,1]
	v_med3_f32 v144, v144, s78, v240
	ds_read_b128 v[140:143], v146
	v_mov_b32_e32 v155, 0
	v_cvt_pk_fp8_f32 v155, v144, v145
	ds_read_b128 v[144:147], v146 offset:32768
	s_waitcnt lgkmcnt(1)
	v_mfma_f32_16x16x32_bf16 v[132:135], v[14:17], v[140:143], v[132:135]
	v_add_u32_e32 v140, v176, v223
	v_lshlrev_b32_e32 v173, 16, v17
	v_and_b32_e32 v243, 0xffff0000, v17
	ds_read_b128 v[140:143], v140
	s_waitcnt lgkmcnt(1)
	v_mfma_f32_16x16x32_bf16 v[136:139], v[14:17], v[144:147], v[136:139]
	v_add_u32_e32 v144, v177, v223
	v_mul_f32_e32 v150, v173, v173
	v_mul_f32_e32 v148, v243, v243
	ds_read_b128 v[144:147], v144
	v_pk_add_f32 v[148:149], v[150:151], v[148:149]
	v_med3_f32 v150, v173, s78, v240
	v_med3_f32 v151, v243, s78, v240
	v_cvt_pk_fp8_f32 v155, v150, v151 op_sel:[0,0,1]
	s_waitcnt lgkmcnt(1)
	v_mfma_f32_16x16x32_bf16 v[132:135], v[14:17], v[140:143], v[132:135]
	v_add_f32_e64 v140, v152, v148
	v_add_f32_e64 v141, v153, v149
	v_and_b32_e32 v143, 0xffff0000, v11
	v_and_b32_e32 v142, 0xffff0000, v10
	v_pk_add_f32 v[148:149], v[140:141], v[140:141] op_sel_hi:[0,1]
	s_waitcnt lgkmcnt(0)
	v_mfma_f32_16x16x32_bf16 v[136:139], v[14:17], v[144:147], v[136:139]
	v_lshlrev_b32_e32 v141, 16, v11
	v_lshlrev_b32_e32 v140, 16, v10
	v_pk_mul_f32 v[144:145], v[142:143], v[142:143]
	global_store_dwordx2 v[130:131], v[154:155], off offset:896
	v_pk_fma_f32 v[144:145], v[140:141], v[140:141], v[144:145]
	v_med3_f32 v140, v140, s78, v240
	v_med3_f32 v142, v142, s78, v240
	v_mov_b32_e32 v154, 0
	v_cvt_pk_fp8_f32 v154, v140, v142
	v_and_b32_e32 v151, 0xffff0000, v13
	v_and_b32_e32 v150, 0xffff0000, v12
	v_lshlrev_b32_e32 v147, 16, v13
	v_lshlrev_b32_e32 v146, 16, v12
	v_pk_mul_f32 v[152:153], v[150:151], v[150:151]
	v_add_f32_e32 v148, v144, v145
	v_pk_fma_f32 v[152:153], v[146:147], v[146:147], v[152:153]
	v_med3_f32 v140, v141, s78, v240
	v_med3_f32 v141, v143, s78, v240
	v_med3_f32 v144, v146, s78, v240
	v_add_u32_e32 v146, v175, v224
	v_cvt_pk_fp8_f32 v154, v140, v141 op_sel:[0,0,1]
	ds_read_b128 v[140:143], v146
	v_med3_f32 v145, v150, s78, v240
	v_mov_b32_e32 v155, 0
	v_cvt_pk_fp8_f32 v155, v144, v145
	v_med3_f32 v150, v147, s78, v240
	ds_read_b128 v[144:147], v146 offset:32768
	s_waitcnt lgkmcnt(1)
	v_mfma_f32_16x16x32_bf16 v[132:135], v[10:13], v[140:143], v[132:135]
	v_add_u32_e32 v140, v176, v224
	ds_read_b128 v[140:143], v140
	v_med3_f32 v151, v151, s78, v240
	s_waitcnt lgkmcnt(1)
	v_mfma_f32_16x16x32_bf16 v[136:139], v[10:13], v[144:147], v[136:139]
	v_add_u32_e32 v144, v177, v224
	v_cvt_pk_fp8_f32 v155, v150, v151 op_sel:[0,0,1]
	ds_read_b128 v[144:147], v144
	s_waitcnt lgkmcnt(1)
	v_mfma_f32_16x16x32_bf16 v[132:135], v[10:13], v[140:143], v[132:135]
	v_add_f32_e32 v140, v152, v148
	v_pk_add_f32 v[150:151], v[152:153], v[140:141] op_sel_hi:[1,0]
	v_lshlrev_b32_e32 v140, 16, v6
	global_store_dwordx2 v[130:131], v[154:155], off offset:928
	v_and_b32_e32 v141, 0xffff0000, v6
	v_mul_f32_e32 v142, v140, v140
	v_lshlrev_b32_e32 v154, 16, v7
	s_waitcnt lgkmcnt(0)
	v_mfma_f32_16x16x32_bf16 v[136:139], v[10:13], v[144:147], v[136:139]
	v_fma_f32 v152, v140, v140, v142
	v_fma_f32 v153, v141, v141, v142
	v_and_b32_e32 v155, 0xffff0000, v7
	v_mul_f32_e32 v142, v154, v154
	v_add_u32_e32 v146, v175, v225
	v_pk_fma_f32 v[156:157], v[154:155], v[154:155], v[142:143] op_sel_hi:[1,1,0]
	v_med3_f32 v144, v140, s78, v240
	v_med3_f32 v145, v141, s78, v240
	ds_read_b128 v[140:143], v146
	global_store_dwordx2 v[130:131], v[158:159], off offset:864
	v_mov_b32_e32 v158, 0
	v_cvt_pk_fp8_f32 v158, v144, v145
	ds_read_b128 v[144:147], v146 offset:32768
	s_waitcnt lgkmcnt(1)
	v_mfma_f32_16x16x32_bf16 v[132:135], v[6:9], v[140:143], v[132:135]
	v_add_u32_e32 v140, v176, v225
	ds_read_b128 v[140:143], v140
	v_med3_f32 v148, v154, s78, v240
	s_waitcnt lgkmcnt(1)
	v_mfma_f32_16x16x32_bf16 v[136:139], v[6:9], v[144:147], v[136:139]
	v_add_u32_e32 v144, v177, v225
	ds_read_b128 v[144:147], v144
	v_med3_f32 v150, v155, s78, v240
	s_waitcnt lgkmcnt(1)
	v_mfma_f32_16x16x32_bf16 v[132:135], v[6:9], v[140:143], v[132:135]
	v_lshlrev_b32_e32 v141, 16, v8
	v_and_b32_e32 v143, 0xffff0000, v8
	v_med3_f32 v154, v141, s78, v240
	v_med3_f32 v155, v143, s78, v240
	v_mov_b32_e32 v159, 0
	v_cvt_pk_fp8_f32 v159, v154, v155
	v_lshlrev_b32_e32 v155, 16, v9
	v_and_b32_e32 v161, 0xffff0000, v9
	v_lshlrev_b32_e32 v140, 16, v2
	v_and_b32_e32 v142, 0xffff0000, v2
	v_med3_f32 v244, v155, s78, v240
	v_med3_f32 v245, v161, s78, v240
	v_lshlrev_b32_e32 v154, 16, v4
	v_and_b32_e32 v160, 0xffff0000, v4
	v_cvt_pk_fp8_f32 v159, v244, v245 op_sel:[0,0,1]
	v_med3_f32 v245, v140, s78, v240
	v_med3_f32 v246, v142, s78, v240
	v_mov_b32_e32 v244, 0
	v_cvt_pk_fp8_f32 v244, v245, v246
	v_med3_f32 v246, v154, s78, v240
	v_med3_f32 v247, v160, s78, v240
	v_mov_b32_e32 v245, 0
	v_cvt_pk_fp8_f32 v245, v246, v247
	v_cvt_pk_fp8_f32 v158, v148, v150 op_sel:[0,0,1]
	v_lshlrev_b32_e32 v148, 16, v3
	v_and_b32_e32 v150, 0xffff0000, v3
	v_lshlrev_b32_e32 v173, 16, v5
	v_and_b32_e32 v243, 0xffff0000, v5
	v_mul_f32_e32 v152, v148, v148
	v_mul_f32_e32 v156, v150, v150
	v_med3_f32 v148, v148, s78, v240
	v_med3_f32 v150, v150, s78, v240
	v_cvt_pk_fp8_f32 v244, v148, v150 op_sel:[0,0,1]
	v_med3_f32 v148, v173, s78, v240
	v_med3_f32 v150, v243, s78, v240
	v_cvt_pk_fp8_f32 v245, v148, v150 op_sel:[0,0,1]
	global_store_dwordx2 v[130:131], v[158:159], off offset:960
	global_store_dwordx2 v[130:131], v[244:245], off offset:992
	global_load_dword v158, v[168:169], off
	s_nop 0
	global_load_dword v159, v[168:169], off offset:64
	v_pk_mul_f32 v[130:131], v[142:143], v[142:143]
	v_mul_f32_e32 v150, v173, v173
	v_pk_fma_f32 v[130:131], v[140:141], v[140:141], v[130:131]
	v_pk_add_f32 v[140:141], v[152:153], v[156:157]
	v_mul_f32_e32 v148, v243, v243
	v_pk_add_f32 v[130:131], v[130:131], v[140:141]
	v_pk_mul_f32 v[140:141], v[160:161], v[160:161]
	s_waitcnt lgkmcnt(0)
	v_mfma_f32_16x16x32_bf16 v[136:139], v[6:9], v[144:147], v[136:139]
	v_fma_f32 v140, v154, v154, v140
	v_fma_f32 v141, v155, v155, v141
	v_add_u32_e32 v144, v175, v226
	v_pk_add_f32 v[130:131], v[140:141], v[130:131]
	v_pk_add_f32 v[140:141], v[150:151], v[148:149]
	v_and_b32_e32 v148, 64, v241
	v_pk_add_f32 v[130:131], v[130:131], v[140:141]
	v_add_u32_e32 v149, 64, v148
	v_add_f32_e32 v130, v130, v131
	v_xor_b32_e32 v131, 16, v241
	v_cmp_lt_i32_e32 vcc, v131, v149
	ds_read_b128 v[140:143], v144
	s_mov_b32 s0, 0xf800000
	v_cndmask_b32_e32 v131, v241, v131, vcc
	v_lshlrev_b32_e32 v131, 2, v131
	ds_bpermute_b32 v131, v131, v130
	s_waitcnt lgkmcnt(1)
	v_mfma_f32_16x16x32_bf16 v[132:135], v[2:5], v[140:143], v[132:135]
	ds_read_b128 v[144:147], v144 offset:32768
	v_mov_b32_e32 v243, 0
	v_mov_b32_e32 v244, 0
	s_waitcnt lgkmcnt(1)
	v_add_f32_e32 v130, v130, v131
	v_xor_b32_e32 v131, 32, v241
	v_cmp_lt_i32_e32 vcc, v131, v149
	v_mov_b32_e32 v245, 0
	s_nop 0
	v_cndmask_b32_e32 v131, v241, v131, vcc
	v_lshlrev_b32_e32 v131, 2, v131
	ds_bpermute_b32 v149, v131, v130
	v_mov_b32_e32 v131, 0
	s_waitcnt lgkmcnt(0)
	v_add_f32_e32 v130, v130, v149
	v_fmamk_f32 v130, v130, 0x3a800000, v166
	v_mul_f32_e32 v140, 0x4f800000, v130
	v_cmp_gt_f32_e32 vcc, s0, v130
	s_nop 1
	v_cndmask_b32_e32 v130, v130, v140, vcc
	v_sqrt_f32_e32 v149, v130
	v_add_u32_e32 v140, v176, v226
	ds_read_b128 v[140:143], v140
	v_mfma_f32_16x16x32_bf16 v[136:139], v[2:5], v[144:147], v[136:139]
	v_add_u32_e32 v144, -1, v149
	v_fma_f32 v145, -v144, v149, v130
	v_cmp_ge_f32_e64 s[0:1], 0, v145
	v_add_u32_e32 v145, 1, v149
	v_fma_f32 v146, -v145, v149, v130
	v_cndmask_b32_e64 v144, v149, v144, s[0:1]
	v_cmp_lt_f32_e64 s[0:1], 0, v146
	s_waitcnt lgkmcnt(0)
	v_mfma_f32_16x16x32_bf16 v[132:135], v[2:5], v[140:143], v[132:135]
	v_cndmask_b32_e64 v144, v144, v145, s[0:1]
	v_mul_f32_e32 v145, 0x37800000, v144
	v_cndmask_b32_e32 v144, v144, v145, vcc
	v_cmp_class_f32_e32 vcc, v130, v237
	s_nop 1
	v_cndmask_b32_e32 v130, v144, v130, vcc
	v_div_scale_f32 v149, s[0:1], v130, v130, 1.0
	v_rcp_f32_e32 v150, v149
	v_add_u32_e32 v144, v177, v226
	ds_read_b128 v[144:147], v144
	v_fma_f32 v140, -v149, v150, 1.0
	v_fmac_f32_e32 v150, v140, v150
	v_div_scale_f32 v140, vcc, 1.0, v130, 1.0
	v_mul_f32_e32 v141, v140, v150
	v_fma_f32 v142, -v149, v141, v140
	v_fmac_f32_e32 v141, v142, v150
	v_fma_f32 v140, -v149, v141, v140
	v_div_fmas_f32 v140, v140, v150, v141
	v_div_fixup_f32 v173, v140, v130, 1.0
	v_or_b32_e32 v130, v148, v227
	v_lshlrev_b32_e32 v130, 2, v130
	v_or_b32_e32 v140, v148, v229
	ds_bpermute_b32 v130, v130, v173
	v_lshlrev_b32_e32 v140, 2, v140
	ds_bpermute_b32 v140, v140, v173
	s_waitcnt lgkmcnt(2)
	v_mfma_f32_16x16x32_bf16 v[136:139], v[2:5], v[144:147], v[136:139]
	s_waitcnt vmcnt(1) lgkmcnt(1)
	v_fma_f32 v132, v132, v130, v158
	s_waitcnt vmcnt(0)
	s_nop 4
	v_fma_f32 v130, v136, v130, v159
	ds_write2_b32 v228, v132, v130 offset1:16
	s_waitcnt lgkmcnt(1)
	v_fma_f32 v130, v133, v140, v158
	v_or_b32_e32 v133, v148, v231
	v_or_b32_e32 v136, v148, v233
	v_lshlrev_b32_e32 v133, 2, v133
	v_lshlrev_b32_e32 v136, 2, v136
	ds_bpermute_b32 v133, v133, v173
	ds_bpermute_b32 v136, v136, v173
	v_fma_f32 v132, v137, v140, v159
	ds_write2_b32 v230, v130, v132 offset1:16
	v_mov_b32_e32 v137, 0
	s_waitcnt lgkmcnt(2)
	v_fma_f32 v130, v134, v133, v158
	v_fma_f32 v132, v138, v133, v159
	s_waitcnt lgkmcnt(1)
	v_fmac_f32_e32 v158, v135, v136
	v_fmac_f32_e32 v159, v139, v136
	ds_write2_b32 v232, v130, v132 offset1:16
	ds_write2_b32 v234, v158, v159 offset1:16
	s_waitcnt lgkmcnt(0)
	v_mov_b32_e32 v130, 0
	v_mov_b32_e32 v134, 0
	v_mov_b32_e32 v133, 0
	v_mov_b32_e32 v132, 0
	v_mov_b32_e32 v135, 0
	v_mov_b32_e32 v136, 0
	v_mov_b32_e32 v138, 0
	s_and_saveexec_b64 s[54:55], s[4:5]
	s_cbranch_execz .LBB0_1720
	ds_read_b128 v[158:161], v238
	ds_read_b128 v[154:157], v238 offset:16
	ds_read_b128 v[150:153], v238 offset:32
	ds_read_b128 v[146:149], v238 offset:48
	ds_read_b128 v[142:145], v238 offset:64
	ds_read_b128 v[138:141], v238 offset:80
	ds_read_b128 v[134:137], v238 offset:96
	ds_read_b128 v[130:133], v238 offset:112
	s_waitcnt lgkmcnt(7)
	v_max_f32_e32 v243, v158, v158
	s_mov_b32 s0, 0xff61b1e6
	v_max_f32_e32 v243, 0xff61b1e6, v243
	v_cmp_lt_f32_e32 vcc, s0, v158
	v_cmp_gt_f32_e64 s[0:1], v159, v243
	s_nop 1
	v_cndmask_b32_e64 v243, v243, v159, s[0:1]
	v_cndmask_b32_e64 v244, 0, 1, s[0:1]
	v_cmp_gt_f32_e64 s[0:1], v160, v243
	s_nop 1
	v_cndmask_b32_e64 v243, v243, v160, s[0:1]
	v_cndmask_b32_e64 v244, v244, 2, s[0:1]
	v_cmp_gt_f32_e64 s[0:1], v161, v243
	s_nop 1
	v_cndmask_b32_e64 v243, v243, v161, s[0:1]
	v_cndmask_b32_e64 v244, v244, 3, s[0:1]
	s_waitcnt lgkmcnt(6)
	v_cmp_gt_f32_e64 s[0:1], v154, v243
	s_nop 1
	v_cndmask_b32_e64 v243, v243, v154, s[0:1]
	v_cndmask_b32_e64 v244, v244, 4, s[0:1]
	v_cmp_gt_f32_e64 s[0:1], v155, v243
	s_nop 1
	v_cndmask_b32_e64 v243, v243, v155, s[0:1]
	v_cndmask_b32_e64 v244, v244, 5, s[0:1]
	v_cmp_gt_f32_e64 s[0:1], v156, v243
	s_nop 1
	v_cndmask_b32_e64 v243, v243, v156, s[0:1]
	v_cndmask_b32_e64 v244, v244, 6, s[0:1]
	v_cmp_gt_f32_e64 s[0:1], v157, v243
	s_nop 1
	v_cndmask_b32_e64 v243, v243, v157, s[0:1]
	v_cndmask_b32_e64 v244, v244, 7, s[0:1]
	s_waitcnt lgkmcnt(5)
	v_cmp_gt_f32_e64 s[0:1], v150, v243
	s_nop 1
	v_cndmask_b32_e64 v243, v243, v150, s[0:1]
	v_cndmask_b32_e64 v244, v244, 8, s[0:1]
	v_cmp_gt_f32_e64 s[0:1], v151, v243
	s_nop 1
	v_cndmask_b32_e64 v243, v243, v151, s[0:1]
	v_cndmask_b32_e64 v244, v244, 9, s[0:1]
	v_cmp_gt_f32_e64 s[0:1], v152, v243
	s_nop 1
	v_cndmask_b32_e64 v243, v243, v152, s[0:1]
	v_cndmask_b32_e64 v244, v244, 10, s[0:1]
	v_cmp_gt_f32_e64 s[0:1], v153, v243
	s_nop 1
	v_cndmask_b32_e64 v243, v243, v153, s[0:1]
	v_cndmask_b32_e64 v244, v244, 11, s[0:1]
	s_waitcnt lgkmcnt(4)
	v_cmp_gt_f32_e64 s[0:1], v146, v243
	s_nop 1
	v_cndmask_b32_e64 v243, v243, v146, s[0:1]
	v_cndmask_b32_e64 v244, v244, 12, s[0:1]
	v_cmp_gt_f32_e64 s[0:1], v147, v243
	s_nop 1
	v_cndmask_b32_e64 v243, v243, v147, s[0:1]
	v_cndmask_b32_e64 v244, v244, 13, s[0:1]
	v_cmp_gt_f32_e64 s[0:1], v148, v243
	s_nop 1
	v_cndmask_b32_e64 v243, v243, v148, s[0:1]
	v_cndmask_b32_e64 v244, v244, 14, s[0:1]
	v_cmp_gt_f32_e64 s[0:1], v149, v243
	s_nop 1
	v_cndmask_b32_e64 v243, v243, v149, s[0:1]
	v_cndmask_b32_e64 v244, v244, 15, s[0:1]
	s_waitcnt lgkmcnt(3)
	v_cmp_gt_f32_e64 s[0:1], v142, v243
	s_nop 1
	v_cndmask_b32_e64 v243, v243, v142, s[0:1]
	v_cndmask_b32_e64 v244, v244, 16, s[0:1]
	v_cmp_gt_f32_e64 s[0:1], v143, v243
	s_nop 1
	v_cndmask_b32_e64 v243, v243, v143, s[0:1]
	v_cndmask_b32_e64 v244, v244, 17, s[0:1]
	v_cmp_gt_f32_e64 s[0:1], v144, v243
	s_nop 1
	v_cndmask_b32_e64 v243, v243, v144, s[0:1]
	v_cndmask_b32_e64 v244, v244, 18, s[0:1]
	v_cmp_gt_f32_e64 s[0:1], v145, v243
	s_nop 1
	v_cndmask_b32_e64 v243, v243, v145, s[0:1]
	v_cndmask_b32_e64 v244, v244, 19, s[0:1]
	s_waitcnt lgkmcnt(2)
	v_cmp_gt_f32_e64 s[0:1], v138, v243
	s_nop 1
	v_cndmask_b32_e64 v243, v243, v138, s[0:1]
	v_cndmask_b32_e64 v244, v244, 20, s[0:1]
	v_cmp_gt_f32_e64 s[0:1], v139, v243
	s_nop 1
	v_cndmask_b32_e64 v243, v243, v139, s[0:1]
	v_cndmask_b32_e64 v244, v244, 21, s[0:1]
	v_cmp_gt_f32_e64 s[0:1], v140, v243
	s_nop 1
	v_cndmask_b32_e64 v243, v243, v140, s[0:1]
	v_cndmask_b32_e64 v244, v244, 22, s[0:1]
	v_cmp_gt_f32_e64 s[0:1], v141, v243
	s_nop 1
	v_cndmask_b32_e64 v243, v243, v141, s[0:1]
	v_cndmask_b32_e64 v244, v244, 23, s[0:1]
	s_waitcnt lgkmcnt(1)
	v_cmp_gt_f32_e64 s[0:1], v134, v243
	s_nop 1
	v_cndmask_b32_e64 v243, v243, v134, s[0:1]
	v_cndmask_b32_e64 v244, v244, 24, s[0:1]
	v_cmp_gt_f32_e64 s[0:1], v135, v243
	s_nop 1
	v_cndmask_b32_e64 v243, v243, v135, s[0:1]
	v_cndmask_b32_e64 v244, v244, 25, s[0:1]
	v_cmp_gt_f32_e64 s[0:1], v136, v243
	s_nop 1
	v_cndmask_b32_e64 v243, v243, v136, s[0:1]
	v_cndmask_b32_e64 v244, v244, 26, s[0:1]
	v_cmp_gt_f32_e64 s[0:1], v137, v243
	s_nop 1
	v_cndmask_b32_e64 v243, v243, v137, s[0:1]
	v_cndmask_b32_e64 v244, v244, 27, s[0:1]
	s_waitcnt lgkmcnt(0)
	v_cmp_gt_f32_e64 s[0:1], v130, v243
	s_nop 1
	v_cndmask_b32_e64 v243, v243, v130, s[0:1]
	v_cndmask_b32_e64 v244, v244, 28, s[0:1]
	v_cmp_gt_f32_e64 s[0:1], v131, v243
	s_nop 1
	v_cndmask_b32_e64 v243, v243, v131, s[0:1]
	v_cndmask_b32_e64 v244, v244, 29, s[0:1]
	v_cmp_gt_f32_e64 s[0:1], v132, v243
	s_nop 1
	v_cndmask_b32_e64 v245, v243, v132, s[0:1]
	v_cndmask_b32_e64 v244, v244, 30, s[0:1]
	v_cmp_gt_f32_e64 s[0:1], v133, v245
	s_nop 1
	v_cndmask_b32_e64 v243, v244, 31, s[0:1]
	v_cndmask_b32_e64 v246, v245, v133, s[0:1]
	v_cmp_ne_u32_e64 s[0:1], 0, v243
	v_lshlrev_b32_e64 v245, v243, 1
	s_and_b64 s[0:1], s[0:1], vcc
	v_cndmask_b32_e64 v244, v242, v158, s[0:1]
	v_and_b32_e32 v247, 2, v245
	v_cmp_eq_u32_e64 s[0:1], 0, v247
	v_cmp_gt_f32_e64 s[8:9], v159, v244
	s_and_b64 s[0:1], s[0:1], s[8:9]
	v_cndmask_b32_e64 v244, v244, v159, s[0:1]
	v_and_b32_e32 v248, 4, v245
	v_cndmask_b32_e64 v247, 0, 1, s[0:1]
	v_cmp_eq_u32_e64 s[0:1], 0, v248
	v_cmp_gt_f32_e64 s[8:9], v160, v244
	s_and_b64 s[0:1], s[0:1], s[8:9]
	v_cndmask_b32_e64 v244, v244, v160, s[0:1]
	v_and_b32_e32 v248, 8, v245
	v_cndmask_b32_e64 v247, v247, 2, s[0:1]
	v_cmp_eq_u32_e64 s[0:1], 0, v248
	v_cmp_gt_f32_e64 s[8:9], v161, v244
	s_and_b64 s[0:1], s[0:1], s[8:9]
	v_cndmask_b32_e64 v244, v244, v161, s[0:1]
	v_and_b32_e32 v248, 16, v245
	v_cndmask_b32_e64 v247, v247, 3, s[0:1]
	v_cmp_eq_u32_e64 s[0:1], 0, v248
	v_cmp_gt_f32_e64 s[8:9], v154, v244
	s_and_b64 s[0:1], s[0:1], s[8:9]
	v_cndmask_b32_e64 v244, v244, v154, s[0:1]
	v_and_b32_e32 v248, 32, v245
	v_cndmask_b32_e64 v247, v247, 4, s[0:1]
	v_cmp_eq_u32_e64 s[0:1], 0, v248
	v_cmp_gt_f32_e64 s[8:9], v155, v244
	s_and_b64 s[0:1], s[0:1], s[8:9]
	v_cndmask_b32_e64 v244, v244, v155, s[0:1]
	v_and_b32_e32 v248, 64, v245
	v_cndmask_b32_e64 v247, v247, 5, s[0:1]
	v_cmp_eq_u32_e64 s[0:1], 0, v248
	v_cmp_gt_f32_e64 s[8:9], v156, v244
	s_and_b64 s[0:1], s[0:1], s[8:9]
	v_cndmask_b32_e64 v244, v244, v156, s[0:1]
	v_and_b32_e32 v248, 0x80, v245
	v_cndmask_b32_e64 v247, v247, 6, s[0:1]
	v_cmp_eq_u32_e64 s[0:1], 0, v248
	v_cmp_gt_f32_e64 s[8:9], v157, v244
	s_and_b64 s[0:1], s[0:1], s[8:9]
	v_cndmask_b32_e64 v244, v244, v157, s[0:1]
	v_and_b32_e32 v248, 0x100, v245
	v_cndmask_b32_e64 v247, v247, 7, s[0:1]
	v_cmp_eq_u32_e64 s[0:1], 0, v248
	v_cmp_gt_f32_e64 s[8:9], v150, v244
	s_and_b64 s[0:1], s[0:1], s[8:9]
	v_cndmask_b32_e64 v244, v244, v150, s[0:1]
	v_and_b32_e32 v248, 0x200, v245
	v_cndmask_b32_e64 v247, v247, 8, s[0:1]
	v_cmp_eq_u32_e64 s[0:1], 0, v248
	v_cmp_gt_f32_e64 s[8:9], v151, v244
	s_and_b64 s[0:1], s[0:1], s[8:9]
	v_cndmask_b32_e64 v244, v244, v151, s[0:1]
	v_and_b32_e32 v248, 0x400, v245
	v_cndmask_b32_e64 v247, v247, 9, s[0:1]
	v_cmp_eq_u32_e64 s[0:1], 0, v248
	v_cmp_gt_f32_e64 s[8:9], v152, v244
	s_and_b64 s[0:1], s[0:1], s[8:9]
	v_cndmask_b32_e64 v244, v244, v152, s[0:1]
	v_and_b32_e32 v248, 0x800, v245
	v_cndmask_b32_e64 v247, v247, 10, s[0:1]
	v_cmp_eq_u32_e64 s[0:1], 0, v248
	v_cmp_gt_f32_e64 s[8:9], v153, v244
	s_and_b64 s[0:1], s[0:1], s[8:9]
	v_cndmask_b32_e64 v244, v244, v153, s[0:1]
	v_and_b32_e32 v248, 0x1000, v245
	v_cndmask_b32_e64 v247, v247, 11, s[0:1]
	v_cmp_eq_u32_e64 s[0:1], 0, v248
	v_cmp_gt_f32_e64 s[8:9], v146, v244
	s_and_b64 s[0:1], s[0:1], s[8:9]
	v_cndmask_b32_e64 v244, v244, v146, s[0:1]
	v_and_b32_e32 v248, 0x2000, v245
	v_cndmask_b32_e64 v247, v247, 12, s[0:1]
	v_cmp_eq_u32_e64 s[0:1], 0, v248
	v_cmp_gt_f32_e64 s[8:9], v147, v244
	s_and_b64 s[0:1], s[0:1], s[8:9]
	v_cndmask_b32_e64 v244, v244, v147, s[0:1]
	v_and_b32_e32 v248, 0x4000, v245
	v_cndmask_b32_e64 v247, v247, 13, s[0:1]
	v_cmp_eq_u32_e64 s[0:1], 0, v248
	v_cmp_gt_f32_e64 s[8:9], v148, v244
	s_and_b64 s[0:1], s[0:1], s[8:9]
	v_cndmask_b32_e64 v244, v244, v148, s[0:1]
	v_and_b32_e32 v248, 0x8000, v245
	v_cndmask_b32_e64 v247, v247, 14, s[0:1]
	v_cmp_eq_u32_e64 s[0:1], 0, v248
	v_cmp_gt_f32_e64 s[8:9], v149, v244
	s_and_b64 s[0:1], s[0:1], s[8:9]
	v_cndmask_b32_e64 v244, v244, v149, s[0:1]
	v_and_b32_e32 v248, 0x10000, v245
	v_cndmask_b32_e64 v247, v247, 15, s[0:1]
	v_cmp_eq_u32_e64 s[0:1], 0, v248
	v_cmp_gt_f32_e64 s[8:9], v142, v244
	s_and_b64 s[0:1], s[0:1], s[8:9]
	v_cndmask_b32_e64 v244, v244, v142, s[0:1]
	v_and_b32_e32 v248, 0x20000, v245
	v_cndmask_b32_e64 v247, v247, 16, s[0:1]
	v_cmp_eq_u32_e64 s[0:1], 0, v248
	v_cmp_gt_f32_e64 s[8:9], v143, v244
	s_and_b64 s[0:1], s[0:1], s[8:9]
	v_cndmask_b32_e64 v244, v244, v143, s[0:1]
	v_and_b32_e32 v248, 0x40000, v245
	v_cndmask_b32_e64 v247, v247, 17, s[0:1]
	v_cmp_eq_u32_e64 s[0:1], 0, v248
	v_cmp_gt_f32_e64 s[8:9], v144, v244
	s_and_b64 s[0:1], s[0:1], s[8:9]
	v_cndmask_b32_e64 v244, v244, v144, s[0:1]
	v_and_b32_e32 v248, 0x80000, v245
	v_cndmask_b32_e64 v247, v247, 18, s[0:1]
	v_cmp_eq_u32_e64 s[0:1], 0, v248
	v_cmp_gt_f32_e64 s[8:9], v145, v244
	s_and_b64 s[0:1], s[0:1], s[8:9]
	v_cndmask_b32_e64 v244, v244, v145, s[0:1]
	v_and_b32_e32 v248, 0x100000, v245
	v_cndmask_b32_e64 v247, v247, 19, s[0:1]
	v_cmp_eq_u32_e64 s[0:1], 0, v248
	v_cmp_gt_f32_e64 s[8:9], v138, v244
	s_and_b64 s[0:1], s[0:1], s[8:9]
	v_cndmask_b32_e64 v244, v244, v138, s[0:1]
	v_and_b32_e32 v248, 0x200000, v245
	v_cndmask_b32_e64 v247, v247, 20, s[0:1]
	v_cmp_eq_u32_e64 s[0:1], 0, v248
	v_cmp_gt_f32_e64 s[8:9], v139, v244
	s_and_b64 s[0:1], s[0:1], s[8:9]
	v_cndmask_b32_e64 v244, v244, v139, s[0:1]
	v_and_b32_e32 v248, 0x400000, v245
	v_cndmask_b32_e64 v247, v247, 21, s[0:1]
	v_cmp_eq_u32_e64 s[0:1], 0, v248
	v_cmp_gt_f32_e64 s[8:9], v140, v244
	s_and_b64 s[0:1], s[0:1], s[8:9]
	v_cndmask_b32_e64 v244, v244, v140, s[0:1]
	v_and_b32_e32 v248, 0x800000, v245
	v_cndmask_b32_e64 v247, v247, 22, s[0:1]
	v_cmp_eq_u32_e64 s[0:1], 0, v248
	v_cmp_gt_f32_e64 s[8:9], v141, v244
	s_and_b64 s[0:1], s[0:1], s[8:9]
	v_cndmask_b32_e64 v244, v244, v141, s[0:1]
	v_and_b32_e32 v248, 0x1000000, v245
	v_cndmask_b32_e64 v247, v247, 23, s[0:1]
	v_cmp_eq_u32_e64 s[0:1], 0, v248
	v_cmp_gt_f32_e64 s[8:9], v134, v244
	s_and_b64 s[0:1], s[0:1], s[8:9]
	v_cndmask_b32_e64 v244, v244, v134, s[0:1]
	v_and_b32_e32 v248, 0x2000000, v245
	v_cndmask_b32_e64 v247, v247, 24, s[0:1]
	v_cmp_eq_u32_e64 s[0:1], 0, v248
	v_cmp_gt_f32_e64 s[8:9], v135, v244
	s_and_b64 s[0:1], s[0:1], s[8:9]
	v_cndmask_b32_e64 v244, v244, v135, s[0:1]
	v_and_b32_e32 v248, 0x4000000, v245
	v_cndmask_b32_e64 v247, v247, 25, s[0:1]
	v_cmp_eq_u32_e64 s[0:1], 0, v248
	v_cmp_gt_f32_e64 s[8:9], v136, v244
	s_and_b64 s[0:1], s[0:1], s[8:9]
	v_cndmask_b32_e64 v244, v244, v136, s[0:1]
	v_and_b32_e32 v248, 0x8000000, v245
	v_cndmask_b32_e64 v247, v247, 26, s[0:1]
	v_cmp_eq_u32_e64 s[0:1], 0, v248
	v_cmp_gt_f32_e64 s[8:9], v137, v244
	s_and_b64 s[0:1], s[0:1], s[8:9]
	v_cndmask_b32_e64 v244, v244, v137, s[0:1]
	v_and_b32_e32 v248, 0x10000000, v245
	v_cndmask_b32_e64 v247, v247, 27, s[0:1]
	v_cmp_eq_u32_e64 s[0:1], 0, v248
	v_cmp_gt_f32_e64 s[8:9], v130, v244
	s_and_b64 s[0:1], s[0:1], s[8:9]
	v_cndmask_b32_e64 v244, v244, v130, s[0:1]
	v_and_b32_e32 v248, 0x20000000, v245
	v_cndmask_b32_e64 v247, v247, 28, s[0:1]
	v_cmp_eq_u32_e64 s[0:1], 0, v248
	v_cmp_gt_f32_e64 s[8:9], v131, v244
	s_and_b64 s[0:1], s[0:1], s[8:9]
	v_cndmask_b32_e64 v244, v244, v131, s[0:1]
	v_and_b32_e32 v248, 2.0, v245
	v_cndmask_b32_e64 v247, v247, 29, s[0:1]
	v_cmp_eq_u32_e64 s[0:1], 0, v248
	v_cmp_gt_f32_e64 s[8:9], v132, v244
	s_and_b64 s[0:1], s[0:1], s[8:9]
	v_cndmask_b32_e64 v248, v244, v132, s[0:1]
	v_cndmask_b32_e64 v247, v247, 30, s[0:1]
	v_cmp_ne_u32_e64 s[0:1], 31, v243
	v_cmp_gt_f32_e64 s[8:9], v133, v248
	s_and_b64 s[0:1], s[0:1], s[8:9]
	v_cndmask_b32_e64 v244, v247, 31, s[0:1]
	v_cndmask_b32_e64 v247, v248, v133, s[0:1]
	v_lshl_or_b32 v248, 1, v244, v245
	v_and_b32_e32 v245, 1, v248
	v_cmp_eq_u32_e64 s[0:1], 0, v245
	s_and_b64 s[0:1], s[0:1], vcc
	v_and_b32_e32 v249, 2, v248
	v_cndmask_b32_e64 v245, v242, v158, s[0:1]
	v_cmp_eq_u32_e64 s[0:1], 0, v249
	v_cmp_gt_f32_e64 s[8:9], v159, v245
	s_and_b64 s[0:1], s[0:1], s[8:9]
	v_cndmask_b32_e64 v245, v245, v159, s[0:1]
	v_and_b32_e32 v250, 4, v248
	v_cndmask_b32_e64 v249, 0, 1, s[0:1]
	v_cmp_eq_u32_e64 s[0:1], 0, v250
	v_cmp_gt_f32_e64 s[8:9], v160, v245
	s_and_b64 s[0:1], s[0:1], s[8:9]
	v_cndmask_b32_e64 v245, v245, v160, s[0:1]
	v_and_b32_e32 v250, 8, v248
	v_cndmask_b32_e64 v249, v249, 2, s[0:1]
	v_cmp_eq_u32_e64 s[0:1], 0, v250
	v_cmp_gt_f32_e64 s[8:9], v161, v245
	s_and_b64 s[0:1], s[0:1], s[8:9]
	v_cndmask_b32_e64 v245, v245, v161, s[0:1]
	v_and_b32_e32 v250, 16, v248
	v_cndmask_b32_e64 v249, v249, 3, s[0:1]
	v_cmp_eq_u32_e64 s[0:1], 0, v250
	v_cmp_gt_f32_e64 s[8:9], v154, v245
	s_and_b64 s[0:1], s[0:1], s[8:9]
	v_cndmask_b32_e64 v245, v245, v154, s[0:1]
	v_and_b32_e32 v250, 32, v248
	v_cndmask_b32_e64 v249, v249, 4, s[0:1]
	v_cmp_eq_u32_e64 s[0:1], 0, v250
	v_cmp_gt_f32_e64 s[8:9], v155, v245
	s_and_b64 s[0:1], s[0:1], s[8:9]
	v_cndmask_b32_e64 v245, v245, v155, s[0:1]
	v_and_b32_e32 v250, 64, v248
	v_cndmask_b32_e64 v249, v249, 5, s[0:1]
	v_cmp_eq_u32_e64 s[0:1], 0, v250
	v_cmp_gt_f32_e64 s[8:9], v156, v245
	s_and_b64 s[0:1], s[0:1], s[8:9]
	v_cndmask_b32_e64 v245, v245, v156, s[0:1]
	v_and_b32_e32 v250, 0x80, v248
	v_cndmask_b32_e64 v249, v249, 6, s[0:1]
	v_cmp_eq_u32_e64 s[0:1], 0, v250
	v_cmp_gt_f32_e64 s[8:9], v157, v245
	s_and_b64 s[0:1], s[0:1], s[8:9]
	v_cndmask_b32_e64 v245, v245, v157, s[0:1]
	v_and_b32_e32 v250, 0x100, v248
	v_cndmask_b32_e64 v249, v249, 7, s[0:1]
	v_cmp_eq_u32_e64 s[0:1], 0, v250
	v_cmp_gt_f32_e64 s[8:9], v150, v245
	s_and_b64 s[0:1], s[0:1], s[8:9]
	v_cndmask_b32_e64 v245, v245, v150, s[0:1]
	v_and_b32_e32 v250, 0x200, v248
	v_cndmask_b32_e64 v249, v249, 8, s[0:1]
	v_cmp_eq_u32_e64 s[0:1], 0, v250
	v_cmp_gt_f32_e64 s[8:9], v151, v245
	s_and_b64 s[0:1], s[0:1], s[8:9]
	v_cndmask_b32_e64 v245, v245, v151, s[0:1]
	v_and_b32_e32 v250, 0x400, v248
	v_cndmask_b32_e64 v249, v249, 9, s[0:1]
	v_cmp_eq_u32_e64 s[0:1], 0, v250
	v_cmp_gt_f32_e64 s[8:9], v152, v245
	s_and_b64 s[0:1], s[0:1], s[8:9]
	v_cndmask_b32_e64 v245, v245, v152, s[0:1]
	v_and_b32_e32 v250, 0x800, v248
	v_cndmask_b32_e64 v249, v249, 10, s[0:1]
	v_cmp_eq_u32_e64 s[0:1], 0, v250
	v_cmp_gt_f32_e64 s[8:9], v153, v245
	s_and_b64 s[0:1], s[0:1], s[8:9]
	v_cndmask_b32_e64 v245, v245, v153, s[0:1]
	v_and_b32_e32 v250, 0x1000, v248
	v_cndmask_b32_e64 v249, v249, 11, s[0:1]
	v_cmp_eq_u32_e64 s[0:1], 0, v250
	v_cmp_gt_f32_e64 s[8:9], v146, v245
	s_and_b64 s[0:1], s[0:1], s[8:9]
	v_cndmask_b32_e64 v245, v245, v146, s[0:1]
	v_and_b32_e32 v250, 0x2000, v248
	v_cndmask_b32_e64 v249, v249, 12, s[0:1]
	v_cmp_eq_u32_e64 s[0:1], 0, v250
	v_cmp_gt_f32_e64 s[8:9], v147, v245
	s_and_b64 s[0:1], s[0:1], s[8:9]
	v_cndmask_b32_e64 v245, v245, v147, s[0:1]
	v_and_b32_e32 v250, 0x4000, v248
	v_cndmask_b32_e64 v249, v249, 13, s[0:1]
	v_cmp_eq_u32_e64 s[0:1], 0, v250
	v_cmp_gt_f32_e64 s[8:9], v148, v245
	s_and_b64 s[0:1], s[0:1], s[8:9]
	v_cndmask_b32_e64 v245, v245, v148, s[0:1]
	v_and_b32_e32 v250, 0x8000, v248
	v_cndmask_b32_e64 v249, v249, 14, s[0:1]
	v_cmp_eq_u32_e64 s[0:1], 0, v250
	v_cmp_gt_f32_e64 s[8:9], v149, v245
	s_and_b64 s[0:1], s[0:1], s[8:9]
	v_cndmask_b32_e64 v245, v245, v149, s[0:1]
	v_and_b32_e32 v250, 0x10000, v248
	v_cndmask_b32_e64 v249, v249, 15, s[0:1]
	v_cmp_eq_u32_e64 s[0:1], 0, v250
	v_cmp_gt_f32_e64 s[8:9], v142, v245
	s_and_b64 s[0:1], s[0:1], s[8:9]
	v_cndmask_b32_e64 v245, v245, v142, s[0:1]
	v_and_b32_e32 v250, 0x20000, v248
	v_cndmask_b32_e64 v249, v249, 16, s[0:1]
	v_cmp_eq_u32_e64 s[0:1], 0, v250
	v_cmp_gt_f32_e64 s[8:9], v143, v245
	s_and_b64 s[0:1], s[0:1], s[8:9]
	v_cndmask_b32_e64 v245, v245, v143, s[0:1]
	v_and_b32_e32 v250, 0x40000, v248
	v_cndmask_b32_e64 v249, v249, 17, s[0:1]
	v_cmp_eq_u32_e64 s[0:1], 0, v250
	v_cmp_gt_f32_e64 s[8:9], v144, v245
	s_and_b64 s[0:1], s[0:1], s[8:9]
	v_cndmask_b32_e64 v245, v245, v144, s[0:1]
	v_and_b32_e32 v250, 0x80000, v248
	v_cndmask_b32_e64 v249, v249, 18, s[0:1]
	v_cmp_eq_u32_e64 s[0:1], 0, v250
	v_cmp_gt_f32_e64 s[8:9], v145, v245
	s_and_b64 s[0:1], s[0:1], s[8:9]
	v_cndmask_b32_e64 v245, v245, v145, s[0:1]
	v_and_b32_e32 v250, 0x100000, v248
	v_cndmask_b32_e64 v249, v249, 19, s[0:1]
	v_cmp_eq_u32_e64 s[0:1], 0, v250
	v_cmp_gt_f32_e64 s[8:9], v138, v245
	s_and_b64 s[0:1], s[0:1], s[8:9]
	v_cndmask_b32_e64 v245, v245, v138, s[0:1]
	v_and_b32_e32 v250, 0x200000, v248
	v_cndmask_b32_e64 v249, v249, 20, s[0:1]
	v_cmp_eq_u32_e64 s[0:1], 0, v250
	v_cmp_gt_f32_e64 s[8:9], v139, v245
	s_and_b64 s[0:1], s[0:1], s[8:9]
	v_cndmask_b32_e64 v245, v245, v139, s[0:1]
	v_and_b32_e32 v250, 0x400000, v248
	v_cndmask_b32_e64 v249, v249, 21, s[0:1]
	v_cmp_eq_u32_e64 s[0:1], 0, v250
	v_cmp_gt_f32_e64 s[8:9], v140, v245
	s_and_b64 s[0:1], s[0:1], s[8:9]
	v_cndmask_b32_e64 v245, v245, v140, s[0:1]
	v_and_b32_e32 v250, 0x800000, v248
	v_cndmask_b32_e64 v249, v249, 22, s[0:1]
	v_cmp_eq_u32_e64 s[0:1], 0, v250
	v_cmp_gt_f32_e64 s[8:9], v141, v245
	s_and_b64 s[0:1], s[0:1], s[8:9]
	v_cndmask_b32_e64 v245, v245, v141, s[0:1]
	v_and_b32_e32 v250, 0x1000000, v248
	v_cndmask_b32_e64 v249, v249, 23, s[0:1]
	v_cmp_eq_u32_e64 s[0:1], 0, v250
	v_cmp_gt_f32_e64 s[8:9], v134, v245
	s_and_b64 s[0:1], s[0:1], s[8:9]
	v_cndmask_b32_e64 v245, v245, v134, s[0:1]
	v_and_b32_e32 v250, 0x2000000, v248
	v_cndmask_b32_e64 v249, v249, 24, s[0:1]
	v_cmp_eq_u32_e64 s[0:1], 0, v250
	v_cmp_gt_f32_e64 s[8:9], v135, v245
	s_and_b64 s[0:1], s[0:1], s[8:9]
	v_cndmask_b32_e64 v245, v245, v135, s[0:1]
	v_and_b32_e32 v250, 0x4000000, v248
	v_cndmask_b32_e64 v249, v249, 25, s[0:1]
	v_cmp_eq_u32_e64 s[0:1], 0, v250
	v_cmp_gt_f32_e64 s[8:9], v136, v245
	s_and_b64 s[0:1], s[0:1], s[8:9]
	v_cndmask_b32_e64 v245, v245, v136, s[0:1]
	v_and_b32_e32 v250, 0x8000000, v248
	v_cndmask_b32_e64 v249, v249, 26, s[0:1]
	v_cmp_eq_u32_e64 s[0:1], 0, v250
	v_cmp_gt_f32_e64 s[8:9], v137, v245
	s_and_b64 s[0:1], s[0:1], s[8:9]
	v_cndmask_b32_e64 v245, v245, v137, s[0:1]
	v_and_b32_e32 v250, 0x10000000, v248
	v_cndmask_b32_e64 v249, v249, 27, s[0:1]
	v_cmp_eq_u32_e64 s[0:1], 0, v250
	v_cmp_gt_f32_e64 s[8:9], v130, v245
	s_and_b64 s[0:1], s[0:1], s[8:9]
	v_cndmask_b32_e64 v245, v245, v130, s[0:1]
	v_and_b32_e32 v250, 0x20000000, v248
	v_cndmask_b32_e64 v249, v249, 28, s[0:1]
	v_cmp_eq_u32_e64 s[0:1], 0, v250
	v_cmp_gt_f32_e64 s[8:9], v131, v245
	s_and_b64 s[0:1], s[0:1], s[8:9]
	v_cndmask_b32_e64 v245, v245, v131, s[0:1]
	v_and_b32_e32 v250, 2.0, v248
	v_cndmask_b32_e64 v249, v249, 29, s[0:1]
	v_cmp_eq_u32_e64 s[0:1], 0, v250
	v_cmp_gt_f32_e64 s[8:9], v132, v245
	s_and_b64 s[0:1], s[0:1], s[8:9]
	v_cndmask_b32_e64 v250, v245, v132, s[0:1]
	v_cndmask_b32_e64 v249, v249, 30, s[0:1]
	v_cmp_lt_i32_e64 s[0:1], -1, v248
	v_cmp_gt_f32_e64 s[8:9], v133, v250
	s_and_b64 s[0:1], s[0:1], s[8:9]
	v_cndmask_b32_e64 v245, v249, 31, s[0:1]
	v_cndmask_b32_e64 v249, v250, v133, s[0:1]
	v_lshlrev_b32_e64 v250, v245, 1
	v_bitop3_b32 v252, v250, 1, v248 bitop3:0xc8
	v_cmp_eq_u32_e64 s[0:1], 0, v252
	s_and_b64 vcc, s[0:1], vcc
	v_cndmask_b32_e32 v158, v242, v158, vcc
	v_bitop3_b32 v252, v250, 2, v248 bitop3:0xc8
	v_cmp_eq_u32_e32 vcc, 0, v252
	v_cmp_gt_f32_e64 s[0:1], v159, v158
	s_and_b64 vcc, vcc, s[0:1]
	v_cndmask_b32_e32 v158, v158, v159, vcc
	v_bitop3_b32 v159, v250, 4, v248 bitop3:0xc8
	v_cndmask_b32_e64 v252, 0, 1, vcc
	v_cmp_eq_u32_e32 vcc, 0, v159
	v_cmp_gt_f32_e64 s[0:1], v160, v158
	s_and_b64 vcc, vcc, s[0:1]
	v_cndmask_b32_e32 v158, v158, v160, vcc
	v_bitop3_b32 v160, v250, 8, v248 bitop3:0xc8
	v_cndmask_b32_e64 v159, v252, 2, vcc
	v_cmp_eq_u32_e32 vcc, 0, v160
	v_cmp_gt_f32_e64 s[0:1], v161, v158
	s_and_b64 vcc, vcc, s[0:1]
	v_cndmask_b32_e32 v158, v158, v161, vcc
	v_bitop3_b32 v160, v250, 16, v248 bitop3:0xc8
	v_cndmask_b32_e64 v159, v159, 3, vcc
	v_cmp_eq_u32_e32 vcc, 0, v160
	v_cmp_gt_f32_e64 s[0:1], v154, v158
	s_and_b64 vcc, vcc, s[0:1]
	v_cndmask_b32_e32 v154, v158, v154, vcc
	v_bitop3_b32 v158, v250, 32, v248 bitop3:0xc8
	v_cndmask_b32_e64 v159, v159, 4, vcc
	v_cmp_eq_u32_e32 vcc, 0, v158
	v_cmp_gt_f32_e64 s[0:1], v155, v154
	s_and_b64 vcc, vcc, s[0:1]
	v_cndmask_b32_e32 v154, v154, v155, vcc
	v_bitop3_b32 v155, v250, 64, v248 bitop3:0xc8
	v_cndmask_b32_e64 v158, v159, 5, vcc
	v_cmp_eq_u32_e32 vcc, 0, v155
	v_cmp_gt_f32_e64 s[0:1], v156, v154
	s_and_b64 vcc, vcc, s[0:1]
	s_movk_i32 s0, 0x80
	v_cndmask_b32_e32 v154, v154, v156, vcc
	v_bitop3_b32 v156, v250, s0, v248 bitop3:0xc8
	v_cndmask_b32_e64 v155, v158, 6, vcc
	v_cmp_eq_u32_e32 vcc, 0, v156
	v_cmp_gt_f32_e64 s[0:1], v157, v154
	s_and_b64 vcc, vcc, s[0:1]
	s_movk_i32 s0, 0x100
	v_cndmask_b32_e32 v154, v154, v157, vcc
	v_bitop3_b32 v156, v250, s0, v248 bitop3:0xc8
	v_cndmask_b32_e64 v155, v155, 7, vcc
	v_cmp_eq_u32_e32 vcc, 0, v156
	v_cmp_gt_f32_e64 s[0:1], v150, v154
	s_and_b64 vcc, vcc, s[0:1]
	s_movk_i32 s0, 0x200
	v_cndmask_b32_e32 v150, v154, v150, vcc
	v_bitop3_b32 v154, v250, s0, v248 bitop3:0xc8
	v_cndmask_b32_e64 v155, v155, 8, vcc
	v_cmp_eq_u32_e32 vcc, 0, v154
	v_cmp_gt_f32_e64 s[0:1], v151, v150
	s_and_b64 vcc, vcc, s[0:1]
	s_movk_i32 s0, 0x400
	v_cndmask_b32_e32 v150, v150, v151, vcc
	v_bitop3_b32 v151, v250, s0, v248 bitop3:0xc8
	v_cndmask_b32_e64 v154, v155, 9, vcc
	v_cmp_eq_u32_e32 vcc, 0, v151
	v_cmp_gt_f32_e64 s[0:1], v152, v150
	s_and_b64 vcc, vcc, s[0:1]
	s_movk_i32 s0, 0x800
	v_cndmask_b32_e32 v150, v150, v152, vcc
	v_bitop3_b32 v152, v250, s0, v248 bitop3:0xc8
	v_cndmask_b32_e64 v151, v154, 10, vcc
	v_cmp_eq_u32_e32 vcc, 0, v152
	v_cmp_gt_f32_e64 s[0:1], v153, v150
	s_and_b64 vcc, vcc, s[0:1]
	s_movk_i32 s0, 0x1000
	v_cndmask_b32_e32 v150, v150, v153, vcc
	v_bitop3_b32 v152, v250, s0, v248 bitop3:0xc8
	v_cndmask_b32_e64 v151, v151, 11, vcc
	v_cmp_eq_u32_e32 vcc, 0, v152
	v_cmp_gt_f32_e64 s[0:1], v146, v150
	s_and_b64 vcc, vcc, s[0:1]
	s_movk_i32 s0, 0x2000
	v_cndmask_b32_e32 v146, v150, v146, vcc
	v_bitop3_b32 v150, v250, s0, v248 bitop3:0xc8
	v_cndmask_b32_e64 v151, v151, 12, vcc
	v_cmp_eq_u32_e32 vcc, 0, v150
	v_cmp_gt_f32_e64 s[0:1], v147, v146
	s_and_b64 vcc, vcc, s[0:1]
	s_movk_i32 s0, 0x4000
	v_cndmask_b32_e32 v146, v146, v147, vcc
	v_bitop3_b32 v147, v250, s0, v248 bitop3:0xc8
	v_cndmask_b32_e64 v150, v151, 13, vcc
	v_cmp_eq_u32_e32 vcc, 0, v147
	v_cmp_gt_f32_e64 s[0:1], v148, v146
	s_and_b64 vcc, vcc, s[0:1]
	s_mov_b32 s0, 0x8000
	v_cndmask_b32_e32 v146, v146, v148, vcc
	v_bitop3_b32 v148, v250, s0, v248 bitop3:0xc8
	v_cndmask_b32_e64 v147, v150, 14, vcc
	v_cmp_eq_u32_e32 vcc, 0, v148
	v_cmp_gt_f32_e64 s[0:1], v149, v146
	s_and_b64 vcc, vcc, s[0:1]
	s_mov_b32 s0, 0x10000
	v_cndmask_b32_e32 v146, v146, v149, vcc
	v_bitop3_b32 v148, v250, s0, v248 bitop3:0xc8
	v_cndmask_b32_e64 v147, v147, 15, vcc
	v_cmp_eq_u32_e32 vcc, 0, v148
	v_cmp_gt_f32_e64 s[0:1], v142, v146
	s_and_b64 vcc, vcc, s[0:1]
	s_mov_b32 s0, 0x20000
	v_cndmask_b32_e32 v142, v146, v142, vcc
	v_bitop3_b32 v146, v250, s0, v248 bitop3:0xc8
	v_cndmask_b32_e64 v147, v147, 16, vcc
	v_cmp_eq_u32_e32 vcc, 0, v146
	v_cmp_gt_f32_e64 s[0:1], v143, v142
	s_and_b64 vcc, vcc, s[0:1]
	v_cndmask_b32_e32 v142, v142, v143, vcc
	v_bitop3_b32 v143, v250, s79, v248 bitop3:0xc8
	v_cndmask_b32_e64 v146, v147, 17, vcc
	v_cmp_eq_u32_e32 vcc, 0, v143
	v_cmp_gt_f32_e64 s[0:1], v144, v142
	s_and_b64 vcc, vcc, s[0:1]
	v_cndmask_b32_e32 v142, v142, v144, vcc
	v_bitop3_b32 v144, v250, s80, v248 bitop3:0xc8
	v_cndmask_b32_e64 v143, v146, 18, vcc
	v_cmp_eq_u32_e32 vcc, 0, v144
	v_cmp_gt_f32_e64 s[0:1], v145, v142
	s_and_b64 vcc, vcc, s[0:1]
	v_cndmask_b32_e32 v142, v142, v145, vcc
	v_bitop3_b32 v144, v250, s81, v248 bitop3:0xc8
	v_cndmask_b32_e64 v143, v143, 19, vcc
	v_cmp_eq_u32_e32 vcc, 0, v144
	v_cmp_gt_f32_e64 s[0:1], v138, v142
	s_and_b64 vcc, vcc, s[0:1]
	v_cndmask_b32_e32 v138, v142, v138, vcc
	v_bitop3_b32 v142, v250, s82, v248 bitop3:0xc8
	v_cndmask_b32_e64 v143, v143, 20, vcc
	v_cmp_eq_u32_e32 vcc, 0, v142
	v_cmp_gt_f32_e64 s[0:1], v139, v138
	s_and_b64 vcc, vcc, s[0:1]
	v_cndmask_b32_e32 v138, v138, v139, vcc
	v_bitop3_b32 v139, v250, s83, v248 bitop3:0xc8
	v_cndmask_b32_e64 v142, v143, 21, vcc
	v_cmp_eq_u32_e32 vcc, 0, v139
	v_cmp_gt_f32_e64 s[0:1], v140, v138
	s_and_b64 vcc, vcc, s[0:1]
	v_cndmask_b32_e32 v138, v138, v140, vcc
	v_bitop3_b32 v140, v250, s84, v248 bitop3:0xc8
	v_cndmask_b32_e64 v139, v142, 22, vcc
	v_cmp_eq_u32_e32 vcc, 0, v140
	v_cmp_gt_f32_e64 s[0:1], v141, v138
	s_and_b64 vcc, vcc, s[0:1]
	v_cndmask_b32_e32 v138, v138, v141, vcc
	v_bitop3_b32 v140, v250, s85, v248 bitop3:0xc8
	v_cndmask_b32_e64 v139, v139, 23, vcc
	v_cmp_eq_u32_e32 vcc, 0, v140
	v_cmp_gt_f32_e64 s[0:1], v134, v138
	s_and_b64 vcc, vcc, s[0:1]
	v_cndmask_b32_e32 v134, v138, v134, vcc
	v_bitop3_b32 v138, v250, s86, v248 bitop3:0xc8
	v_cndmask_b32_e64 v139, v139, 24, vcc
	v_cmp_eq_u32_e32 vcc, 0, v138
	v_cmp_gt_f32_e64 s[0:1], v135, v134
	s_and_b64 vcc, vcc, s[0:1]
	v_cndmask_b32_e32 v134, v134, v135, vcc
	v_bitop3_b32 v135, v250, s87, v248 bitop3:0xc8
	v_cndmask_b32_e64 v138, v139, 25, vcc
	v_cmp_eq_u32_e32 vcc, 0, v135
	v_cmp_gt_f32_e64 s[0:1], v136, v134
	s_and_b64 vcc, vcc, s[0:1]
	v_cndmask_b32_e32 v134, v134, v136, vcc
	v_bitop3_b32 v136, v250, s91, v248 bitop3:0xc8
	v_cndmask_b32_e64 v135, v138, 26, vcc
	v_cmp_eq_u32_e32 vcc, 0, v136
	v_cmp_gt_f32_e64 s[0:1], v137, v134
	s_and_b64 vcc, vcc, s[0:1]
	v_cndmask_b32_e32 v134, v134, v137, vcc
	v_bitop3_b32 v136, v250, s92, v248 bitop3:0xc8
	v_cndmask_b32_e64 v135, v135, 27, vcc
	v_cmp_eq_u32_e32 vcc, 0, v136
	v_cmp_gt_f32_e64 s[0:1], v130, v134
	s_and_b64 vcc, vcc, s[0:1]
	v_cndmask_b32_e32 v130, v134, v130, vcc
	v_bitop3_b32 v134, v250, s93, v248 bitop3:0xc8
	v_cndmask_b32_e64 v135, v135, 28, vcc
	v_cmp_eq_u32_e32 vcc, 0, v134
	v_cmp_gt_f32_e64 s[0:1], v131, v130
	s_and_b64 vcc, vcc, s[0:1]
	v_cndmask_b32_e32 v130, v130, v131, vcc
	v_bitop3_b32 v131, v250, 2.0, v248 bitop3:0xc8
	v_cndmask_b32_e64 v134, v135, 29, vcc
	v_cmp_eq_u32_e32 vcc, 0, v131
	v_cmp_gt_f32_e64 s[0:1], v132, v130
	s_and_b64 vcc, vcc, s[0:1]
	v_or_b32_e32 v251, v250, v248
	v_cndmask_b32_e32 v130, v130, v132, vcc
	v_cndmask_b32_e64 v131, v134, 30, vcc
	v_cmp_lt_i32_e32 vcc, -1, v251
	v_cmp_gt_f32_e64 s[0:1], v133, v130
	s_and_b64 vcc, vcc, s[0:1]
	v_cndmask_b32_e32 v132, v130, v133, vcc
	v_sub_f32_e32 v130, v247, v246
	v_cndmask_b32_e64 v134, v131, 31, vcc
	v_mul_f32_e32 v130, 0x3fb8aa3b, v130
	v_sub_f32_e32 v131, v249, v246
	v_exp_f32_e32 v130, v130
	v_mul_f32_e32 v131, 0x3fb8aa3b, v131
	v_sub_f32_e32 v132, v132, v246
	v_exp_f32_e32 v131, v131
	v_mul_f32_e32 v132, 0x3fb8aa3b, v132
	v_exp_f32_e32 v133, v132
	v_add_f32_e32 v132, 1.0, v130
	v_add_f32_e32 v132, v132, v131
	v_add_f32_e32 v132, v132, v133
	v_div_scale_f32 v135, s[0:1], v132, v132, 1.0
	v_rcp_f32_e32 v139, v135
	s_nop 0
	v_fma_f32 v136, -v135, v139, 1.0
	v_fmac_f32_e32 v139, v136, v139
	v_div_scale_f32 v136, vcc, 1.0, v132, 1.0
	v_mul_f32_e32 v140, v136, v139
	v_fma_f32 v137, -v135, v140, v136
	v_fmac_f32_e32 v140, v137, v139
	v_fma_f32 v141, -v135, v140, v136
	v_lshl_add_u32 v135, v243, 2, s67
	ds_add_rtn_u32 v138, v135, v239
	v_lshl_add_u32 v135, v244, 2, s67
	ds_add_rtn_u32 v137, v135, v239
	v_lshl_add_u32 v135, v245, 2, s67
	ds_add_rtn_u32 v136, v135, v239
	v_lshl_add_u32 v135, v134, 2, s67
	ds_add_rtn_u32 v135, v135, v239
	v_div_fmas_f32 v139, v141, v139, v140
	v_div_fixup_f32 v132, v139, v132, 1.0
	v_pk_mul_f32 v[130:131], v[130:131], v[132:133] op_sel_hi:[1,0]
	v_mul_f32_e32 v133, v133, v132

.LBB0_1896:
	s_cmp_eq_u32 s40, 0
	s_cbranch_scc1 .Lpeel6
	s_add_u32 s33, s74, s40
	s_addc_u32 s44, s75, s41
	s_add_u32 s56, s33, 0x1d800080
	s_addc_u32 s57, s44, 0
	s_add_u32 s33, s33, 0x1d800100
	s_addc_u32 s52, s44, 0
	v_add_u32_e32 v2, 0x10000, v173
	v_add_u32_e32 v14, 0x14000, v173
	s_and_b64 s[44:45], s[42:43], exec
	ds_read_b128 v[18:21], v2
	ds_read_b128 v[22:25], v2 offset:1024
	ds_read_b128 v[26:29], v2 offset:2048
	ds_read_b128 v[30:33], v2 offset:3072
	ds_read_b128 v[2:5], v14
	ds_read_b128 v[6:9], v14 offset:1024
	ds_read_b128 v[10:13], v14 offset:2048
	ds_read_b128 v[14:17], v14 offset:3072
	s_cselect_b32 s55, s11, s52
	s_cselect_b32 s54, s10, s33
	s_add_u32 s33, s2, s40
	s_addc_u32 s44, s23, s41
	s_and_b64 s[42:43], s[42:43], exec
	s_cselect_b32 s43, s39, s44
	s_cselect_b32 s42, s38, s33
	s_add_u32 s44, s54, 0x80
	s_addc_u32 s45, s55, 0
	s_add_u32 s52, s42, 0x80
	s_addc_u32 s53, s43, 0
	ds_read_b128 v[180:183], v174
	ds_read_b128 v[184:187], v174 offset:1024
	ds_read_b128 v[188:191], v174 offset:2048
	ds_read_b128 v[192:195], v174 offset:3072
	ds_read_b128 v[196:199], v174 offset:4096
	ds_read_b128 v[200:203], v174 offset:5120
	ds_read_b128 v[204:207], v174 offset:6144
	ds_read_b128 v[208:211], v174 offset:7168
	s_mov_b32 s33, m0
	s_mov_b32 m0, s93
	s_nop 2
	global_load_lds_dwordx4 v178, s[56:57]
	s_mov_b32 m0, s33
	s_mov_b32 s33, m0
	s_mov_b32 m0, s94
	s_nop 2
	global_load_lds_dwordx4 v177, s[56:57]
	s_mov_b32 m0, s33
	s_waitcnt vmcnt(8)
	s_waitcnt lgkmcnt(0)
	s_barrier
	s_setprio 1
	v_mfma_f32_16x16x128_f8f6f4 v[158:161], v[18:25], v[180:187], v[158:161]
	v_mfma_f32_16x16x128_f8f6f4 v[154:157], v[26:33], v[180:187], v[154:157]
	v_mfma_f32_16x16x128_f8f6f4 v[150:153], v[18:25], v[188:195], v[150:153]
	v_mfma_f32_16x16x128_f8f6f4 v[146:149], v[26:33], v[188:195], v[146:149]
	v_mfma_f32_16x16x128_f8f6f4 v[142:145], v[18:25], v[196:203], v[142:145]
	v_mfma_f32_16x16x128_f8f6f4 v[138:141], v[26:33], v[196:203], v[138:141]
	v_mfma_f32_16x16x128_f8f6f4 v[134:137], v[18:25], v[204:211], v[134:137]
	v_mfma_f32_16x16x128_f8f6f4 v[130:133], v[26:33], v[204:211], v[130:133]
	v_mfma_f32_16x16x128_f8f6f4 v[126:129], v[2:9], v[180:187], v[126:129]
	v_mfma_f32_16x16x128_f8f6f4 v[122:125], v[10:17], v[180:187], v[122:125]
	v_mfma_f32_16x16x128_f8f6f4 v[118:121], v[2:9], v[188:195], v[118:121]
	v_mfma_f32_16x16x128_f8f6f4 v[114:117], v[10:17], v[188:195], v[114:117]
	v_mfma_f32_16x16x128_f8f6f4 v[110:113], v[2:9], v[196:203], v[110:113]
	v_mfma_f32_16x16x128_f8f6f4 v[106:109], v[10:17], v[196:203], v[106:109]
	v_mfma_f32_16x16x128_f8f6f4 v[102:105], v[2:9], v[204:211], v[102:105]
	v_mfma_f32_16x16x128_f8f6f4 v[98:101], v[10:17], v[204:211], v[98:101]
	s_setprio 0
	s_barrier
	ds_read_b128 v[180:183], v174 offset:16384
	ds_read_b128 v[184:187], v174 offset:17408
	ds_read_b128 v[188:191], v174 offset:18432
	ds_read_b128 v[192:195], v174 offset:19456
	ds_read_b128 v[196:199], v174 offset:20480
	ds_read_b128 v[200:203], v174 offset:21504
	ds_read_b128 v[204:207], v174 offset:22528
	ds_read_b128 v[208:211], v174 offset:23552
	s_mov_b32 s33, m0
	s_mov_b32 m0, s67
	s_nop 2
	global_load_lds_dwordx4 v1, s[42:43]
	s_mov_b32 m0, s33
	s_add_u32 s56, s42, 0x20000
	s_mov_b32 s33, m0
	s_mov_b32 m0, s68
	s_nop 2
	global_load_lds_dwordx4 v163, s[42:43]
	s_mov_b32 m0, s33
	s_addc_u32 s57, s43, 0
	s_mov_b32 s33, m0
	s_mov_b32 m0, s69
	s_nop 2
	global_load_lds_dwordx4 v1, s[56:57]
	s_mov_b32 m0, s33
	s_mov_b32 s33, m0
	s_mov_b32 m0, s76
	s_nop 2
	global_load_lds_dwordx4 v163, s[56:57]
	s_mov_b32 m0, s33
	s_mov_b32 s33, m0
	s_mov_b32 m0, s15
	s_nop 2
	global_load_lds_dwordx4 v168, s[54:55]
	s_mov_b32 m0, s33
	s_mov_b32 s33, m0
	s_mov_b32 m0, s79
	s_nop 2
	global_load_lds_dwordx4 v172, s[54:55]
	s_mov_b32 m0, s33
	s_waitcnt vmcnt(8)
	s_waitcnt lgkmcnt(0)
	s_barrier
	s_setprio 1
	v_mfma_f32_16x16x128_f8f6f4 v[94:97], v[18:25], v[180:187], v[94:97]
	v_mfma_f32_16x16x128_f8f6f4 v[90:93], v[26:33], v[180:187], v[90:93]
	v_mfma_f32_16x16x128_f8f6f4 v[86:89], v[18:25], v[188:195], v[86:89]
	v_mfma_f32_16x16x128_f8f6f4 v[82:85], v[26:33], v[188:195], v[82:85]
	v_mfma_f32_16x16x128_f8f6f4 v[78:81], v[18:25], v[196:203], v[78:81]
	v_mfma_f32_16x16x128_f8f6f4 v[74:77], v[26:33], v[196:203], v[74:77]
	v_mfma_f32_16x16x128_f8f6f4 v[70:73], v[18:25], v[204:211], v[70:73]
	v_mfma_f32_16x16x128_f8f6f4 v[66:69], v[26:33], v[204:211], v[66:69]
	v_mfma_f32_16x16x128_f8f6f4 v[62:65], v[2:9], v[180:187], v[62:65]
	v_mfma_f32_16x16x128_f8f6f4 v[58:61], v[10:17], v[180:187], v[58:61]
	v_mfma_f32_16x16x128_f8f6f4 v[54:57], v[2:9], v[188:195], v[54:57]
	v_mfma_f32_16x16x128_f8f6f4 v[50:53], v[10:17], v[188:195], v[50:53]
	v_mfma_f32_16x16x128_f8f6f4 v[46:49], v[2:9], v[196:203], v[46:49]
	v_mfma_f32_16x16x128_f8f6f4 v[42:45], v[10:17], v[196:203], v[42:45]
	v_mfma_f32_16x16x128_f8f6f4 v[38:41], v[2:9], v[204:211], v[38:41]
	v_mfma_f32_16x16x128_f8f6f4 v[34:37], v[10:17], v[204:211], v[34:37]
	s_setprio 0
	s_barrier
.Lmid6:
	v_add_u32_e32 v14, 0x18000, v173
	v_add_u32_e32 v30, 0x1c000, v173
	ds_read_b128 v[2:5], v14
	ds_read_b128 v[6:9], v14 offset:1024
	ds_read_b128 v[10:13], v14 offset:2048
	ds_read_b128 v[14:17], v14 offset:3072
	ds_read_b128 v[18:21], v30
	ds_read_b128 v[22:25], v30 offset:1024
	ds_read_b128 v[26:29], v30 offset:2048
	ds_read_b128 v[30:33], v30 offset:3072
	ds_read_b128 v[180:183], v174 offset:32768
	ds_read_b128 v[184:187], v174 offset:33792
	ds_read_b128 v[188:191], v174 offset:34816
	ds_read_b128 v[192:195], v174 offset:35840
	ds_read_b128 v[196:199], v174 offset:36864
	ds_read_b128 v[200:203], v174 offset:37888
	ds_read_b128 v[204:207], v174 offset:38912
	ds_read_b128 v[208:211], v174 offset:39936
	s_mov_b32 s33, m0
	s_mov_b32 m0, s80
	s_nop 2
	global_load_lds_dwordx4 v169, s[54:55]
	s_mov_b32 m0, s33
	s_mov_b32 s33, m0
	s_mov_b32 m0, s81
	s_nop 2
	global_load_lds_dwordx4 v175, s[54:55]
	s_mov_b32 m0, s33
	s_waitcnt vmcnt(8)
	s_waitcnt lgkmcnt(0)
	s_barrier
	s_setprio 1
	v_mfma_f32_16x16x128_f8f6f4 v[158:161], v[2:9], v[180:187], v[158:161]
	v_mfma_f32_16x16x128_f8f6f4 v[154:157], v[10:17], v[180:187], v[154:157]
	v_mfma_f32_16x16x128_f8f6f4 v[150:153], v[2:9], v[188:195], v[150:153]
	v_mfma_f32_16x16x128_f8f6f4 v[146:149], v[10:17], v[188:195], v[146:149]
	v_mfma_f32_16x16x128_f8f6f4 v[142:145], v[2:9], v[196:203], v[142:145]
	v_mfma_f32_16x16x128_f8f6f4 v[138:141], v[10:17], v[196:203], v[138:141]
	v_mfma_f32_16x16x128_f8f6f4 v[134:137], v[2:9], v[204:211], v[134:137]
	v_mfma_f32_16x16x128_f8f6f4 v[130:133], v[10:17], v[204:211], v[130:133]
	v_mfma_f32_16x16x128_f8f6f4 v[126:129], v[18:25], v[180:187], v[126:129]
	v_mfma_f32_16x16x128_f8f6f4 v[122:125], v[26:33], v[180:187], v[122:125]
	v_mfma_f32_16x16x128_f8f6f4 v[118:121], v[18:25], v[188:195], v[118:121]
	v_mfma_f32_16x16x128_f8f6f4 v[114:117], v[26:33], v[188:195], v[114:117]
	v_mfma_f32_16x16x128_f8f6f4 v[110:113], v[18:25], v[196:203], v[110:113]
	v_mfma_f32_16x16x128_f8f6f4 v[106:109], v[26:33], v[196:203], v[106:109]
	v_mfma_f32_16x16x128_f8f6f4 v[102:105], v[18:25], v[204:211], v[102:105]
	v_mfma_f32_16x16x128_f8f6f4 v[98:101], v[26:33], v[204:211], v[98:101]
	s_setprio 0
	s_barrier
	ds_read_b128 v[180:183], v174 offset:49152
	ds_read_b128 v[184:187], v174 offset:50176
	ds_read_b128 v[188:191], v174 offset:51200
	ds_read_b128 v[192:195], v174 offset:52224
	ds_read_b128 v[196:199], v174 offset:53248
	ds_read_b128 v[200:203], v174 offset:54272
	ds_read_b128 v[204:207], v174 offset:55296
	ds_read_b128 v[208:211], v174 offset:56320
	s_mov_b32 s33, m0
	s_mov_b32 m0, s84
	s_nop 2
	global_load_lds_dwordx4 v1, s[52:53]
	s_mov_b32 m0, s33
	s_add_u32 s42, s42, 0x20080
	s_mov_b32 s33, m0
	s_mov_b32 m0, s85
	s_nop 2
	global_load_lds_dwordx4 v163, s[52:53]
	s_mov_b32 m0, s33
	s_addc_u32 s43, s43, 0
	s_mov_b32 s33, m0
	s_mov_b32 m0, s91
	s_nop 2
	global_load_lds_dwordx4 v1, s[42:43]
	s_mov_b32 m0, s33
	s_mov_b32 s33, m0
	s_mov_b32 m0, s92
	s_nop 2
	global_load_lds_dwordx4 v163, s[42:43]
	s_mov_b32 m0, s33
	s_mov_b32 s33, m0
	s_mov_b32 m0, s86
	s_nop 2
	global_load_lds_dwordx4 v168, s[44:45]
	s_mov_b32 m0, s33
	s_mov_b32 s33, m0
	s_mov_b32 m0, s87
	s_nop 2
	global_load_lds_dwordx4 v172, s[44:45]
	s_mov_b32 m0, s33
	s_waitcnt vmcnt(8)
	s_waitcnt lgkmcnt(0)
	s_barrier
	s_setprio 1
	v_mfma_f32_16x16x128_f8f6f4 v[94:97], v[2:9], v[180:187], v[94:97]
	v_mfma_f32_16x16x128_f8f6f4 v[90:93], v[10:17], v[180:187], v[90:93]
	v_mfma_f32_16x16x128_f8f6f4 v[86:89], v[2:9], v[188:195], v[86:89]
	v_mfma_f32_16x16x128_f8f6f4 v[82:85], v[10:17], v[188:195], v[82:85]
	v_mfma_f32_16x16x128_f8f6f4 v[78:81], v[2:9], v[196:203], v[78:81]
	v_mfma_f32_16x16x128_f8f6f4 v[74:77], v[10:17], v[196:203], v[74:77]
	v_mfma_f32_16x16x128_f8f6f4 v[70:73], v[2:9], v[204:211], v[70:73]
	v_mfma_f32_16x16x128_f8f6f4 v[66:69], v[10:17], v[204:211], v[66:69]
	v_mfma_f32_16x16x128_f8f6f4 v[62:65], v[18:25], v[180:187], v[62:65]
	v_mfma_f32_16x16x128_f8f6f4 v[58:61], v[26:33], v[180:187], v[58:61]
	v_mfma_f32_16x16x128_f8f6f4 v[54:57], v[18:25], v[188:195], v[54:57]
	v_mfma_f32_16x16x128_f8f6f4 v[50:53], v[26:33], v[188:195], v[50:53]
	v_mfma_f32_16x16x128_f8f6f4 v[46:49], v[18:25], v[196:203], v[46:49]
	v_mfma_f32_16x16x128_f8f6f4 v[42:45], v[26:33], v[196:203], v[42:45]
	v_mfma_f32_16x16x128_f8f6f4 v[38:41], v[18:25], v[204:211], v[38:41]
	v_mfma_f32_16x16x128_f8f6f4 v[34:37], v[26:33], v[204:211], v[34:37]
	s_setprio 0
	s_cmp_lt_i32 s9, 4
	s_cbranch_scc1 .Lkb6_do
	s_cmp_lg_u64 s[16:17], 0
	s_cbranch_scc0 .Lkb6_skip

.Lpeel6:
	s_add_u32 s33, s74, s40
	s_addc_u32 s44, s75, s41
	s_add_u32 s56, s33, 0x1d800080
	s_addc_u32 s57, s44, 0
	s_add_u32 s33, s33, 0x1d800100
	s_addc_u32 s52, s44, 0
	v_add_u32_e32 v2, 0x10000, v173
	v_add_u32_e32 v14, 0x14000, v173
	s_and_b64 s[44:45], s[42:43], exec
	ds_read_b128 v[18:21], v2
	ds_read_b128 v[22:25], v2 offset:1024
	ds_read_b128 v[26:29], v2 offset:2048
	ds_read_b128 v[30:33], v2 offset:3072
	ds_read_b128 v[2:5], v14
	ds_read_b128 v[6:9], v14 offset:1024
	ds_read_b128 v[10:13], v14 offset:2048
	ds_read_b128 v[14:17], v14 offset:3072
	s_cselect_b32 s55, s11, s52
	s_cselect_b32 s54, s10, s33
	s_add_u32 s33, s2, s40
	s_addc_u32 s44, s23, s41
	s_and_b64 s[42:43], s[42:43], exec
	s_cselect_b32 s43, s39, s44
	s_cselect_b32 s42, s38, s33
	s_add_u32 s44, s54, 0x80
	s_addc_u32 s45, s55, 0
	s_add_u32 s52, s42, 0x80
	s_addc_u32 s53, s43, 0
	ds_read_b128 v[180:183], v174
	ds_read_b128 v[184:187], v174 offset:1024
	ds_read_b128 v[188:191], v174 offset:2048
	ds_read_b128 v[192:195], v174 offset:3072
	ds_read_b128 v[196:199], v174 offset:4096
	ds_read_b128 v[200:203], v174 offset:5120
	ds_read_b128 v[204:207], v174 offset:6144
	ds_read_b128 v[208:211], v174 offset:7168
	s_mov_b32 s33, m0
	s_mov_b32 m0, s93
	s_nop 2
	global_load_lds_dwordx4 v178, s[56:57]
	s_mov_b32 m0, s33
	s_mov_b32 s33, m0
	s_mov_b32 m0, s94
	s_nop 2
	global_load_lds_dwordx4 v177, s[56:57]
	s_mov_b32 m0, s33
	s_waitcnt vmcnt(8)
	s_waitcnt lgkmcnt(0)
	s_barrier
	s_setprio 1
	v_mfma_f32_16x16x128_f8f6f4 v[158:161], v[18:25], v[180:187], 0
	v_mfma_f32_16x16x128_f8f6f4 v[154:157], v[26:33], v[180:187], 0
	v_mfma_f32_16x16x128_f8f6f4 v[150:153], v[18:25], v[188:195], 0
	v_mfma_f32_16x16x128_f8f6f4 v[146:149], v[26:33], v[188:195], 0
	v_mfma_f32_16x16x128_f8f6f4 v[142:145], v[18:25], v[196:203], 0
	v_mfma_f32_16x16x128_f8f6f4 v[138:141], v[26:33], v[196:203], 0
	v_mfma_f32_16x16x128_f8f6f4 v[134:137], v[18:25], v[204:211], 0
	v_mfma_f32_16x16x128_f8f6f4 v[130:133], v[26:33], v[204:211], 0
	v_mfma_f32_16x16x128_f8f6f4 v[126:129], v[2:9], v[180:187], 0
	v_mfma_f32_16x16x128_f8f6f4 v[122:125], v[10:17], v[180:187], 0
	v_mfma_f32_16x16x128_f8f6f4 v[118:121], v[2:9], v[188:195], 0
	v_mfma_f32_16x16x128_f8f6f4 v[114:117], v[10:17], v[188:195], 0
	v_mfma_f32_16x16x128_f8f6f4 v[110:113], v[2:9], v[196:203], 0
	v_mfma_f32_16x16x128_f8f6f4 v[106:109], v[10:17], v[196:203], 0
	v_mfma_f32_16x16x128_f8f6f4 v[102:105], v[2:9], v[204:211], 0
	v_mfma_f32_16x16x128_f8f6f4 v[98:101], v[10:17], v[204:211], 0
	s_setprio 0
	s_barrier
	ds_read_b128 v[180:183], v174 offset:16384
	ds_read_b128 v[184:187], v174 offset:17408
	ds_read_b128 v[188:191], v174 offset:18432
	ds_read_b128 v[192:195], v174 offset:19456
	ds_read_b128 v[196:199], v174 offset:20480
	ds_read_b128 v[200:203], v174 offset:21504
	ds_read_b128 v[204:207], v174 offset:22528
	ds_read_b128 v[208:211], v174 offset:23552
	s_mov_b32 s33, m0
	s_mov_b32 m0, s67
	s_nop 2
	global_load_lds_dwordx4 v1, s[42:43]
	s_mov_b32 m0, s33
	s_add_u32 s56, s42, 0x20000
	s_mov_b32 s33, m0
	s_mov_b32 m0, s68
	s_nop 2
	global_load_lds_dwordx4 v163, s[42:43]
	s_mov_b32 m0, s33
	s_addc_u32 s57, s43, 0
	s_mov_b32 s33, m0
	s_mov_b32 m0, s69
	s_nop 2
	global_load_lds_dwordx4 v1, s[56:57]
	s_mov_b32 m0, s33
	s_mov_b32 s33, m0
	s_mov_b32 m0, s76
	s_nop 2
	global_load_lds_dwordx4 v163, s[56:57]
	s_mov_b32 m0, s33
	s_mov_b32 s33, m0
	s_mov_b32 m0, s15
	s_nop 2
	global_load_lds_dwordx4 v168, s[54:55]
	s_mov_b32 m0, s33
	s_mov_b32 s33, m0
	s_mov_b32 m0, s79
	s_nop 2
	global_load_lds_dwordx4 v172, s[54:55]
	s_mov_b32 m0, s33
	s_waitcnt vmcnt(8)
	s_waitcnt lgkmcnt(0)
	s_barrier
	s_setprio 1
	v_mfma_f32_16x16x128_f8f6f4 v[94:97], v[18:25], v[180:187], 0
	v_mfma_f32_16x16x128_f8f6f4 v[90:93], v[26:33], v[180:187], 0
	v_mfma_f32_16x16x128_f8f6f4 v[86:89], v[18:25], v[188:195], 0
	v_mfma_f32_16x16x128_f8f6f4 v[82:85], v[26:33], v[188:195], 0
	v_mfma_f32_16x16x128_f8f6f4 v[78:81], v[18:25], v[196:203], 0
	v_mfma_f32_16x16x128_f8f6f4 v[74:77], v[26:33], v[196:203], 0
	v_mfma_f32_16x16x128_f8f6f4 v[70:73], v[18:25], v[204:211], 0
	v_mfma_f32_16x16x128_f8f6f4 v[66:69], v[26:33], v[204:211], 0
	v_mfma_f32_16x16x128_f8f6f4 v[62:65], v[2:9], v[180:187], 0
	v_mfma_f32_16x16x128_f8f6f4 v[58:61], v[10:17], v[180:187], 0
	v_mfma_f32_16x16x128_f8f6f4 v[54:57], v[2:9], v[188:195], 0
	v_mfma_f32_16x16x128_f8f6f4 v[50:53], v[10:17], v[188:195], 0
	v_mfma_f32_16x16x128_f8f6f4 v[46:49], v[2:9], v[196:203], 0
	v_mfma_f32_16x16x128_f8f6f4 v[42:45], v[10:17], v[196:203], 0
	v_mfma_f32_16x16x128_f8f6f4 v[38:41], v[2:9], v[204:211], 0
	v_mfma_f32_16x16x128_f8f6f4 v[34:37], v[10:17], v[204:211], 0
	s_setprio 0
	s_barrier
	s_branch .Lmid6

.LBB0_1943:
	s_add_u32 s54, s38, 0x80
	s_addc_u32 s55, s39, 0
	v_add_u32_e32 v2, 0x10000, v174
	v_add_u32_e32 v14, 0x14000, v174
	s_add_u32 s38, s38, 0x100
	ds_read_b128 v[18:21], v2
	ds_read_b128 v[22:25], v2 offset:1024
	ds_read_b128 v[26:29], v2 offset:2048
	ds_read_b128 v[30:33], v2 offset:3072
	ds_read_b128 v[2:5], v14
	ds_read_b128 v[6:9], v14 offset:1024
	ds_read_b128 v[10:13], v14 offset:2048
	ds_read_b128 v[14:17], v14 offset:3072
	s_addc_u32 s39, s39, 0
	s_and_b64 s[40:41], s[40:41], exec
	s_cselect_b32 s52, s10, s38
	s_cselect_b32 s53, s11, s39
	s_cselect_b32 s41, s1, s87
	s_cselect_b32 s40, s0, s86
	s_add_u32 s42, s52, 0x80
	s_addc_u32 s43, s53, 0
	s_add_u32 s44, s40, 0x80
	s_addc_u32 s45, s41, 0
	ds_read_b128 v[180:183], v175
	ds_read_b128 v[184:187], v175 offset:1024
	ds_read_b128 v[188:191], v175 offset:2048
	ds_read_b128 v[192:195], v175 offset:3072
	ds_read_b128 v[196:199], v175 offset:4096
	ds_read_b128 v[200:203], v175 offset:5120
	ds_read_b128 v[204:207], v175 offset:6144
	ds_read_b128 v[208:211], v175 offset:7168
	s_mov_b32 s33, m0
	s_mov_b32 m0, s78
	s_nop 2
	global_load_lds_dwordx4 v164, s[54:55]
	s_mov_b32 m0, s33
	s_mov_b32 s33, m0
	s_mov_b32 m0, s79
	s_nop 2
	global_load_lds_dwordx4 v166, s[54:55]
	s_mov_b32 m0, s33
	s_waitcnt vmcnt(8)
	s_waitcnt lgkmcnt(0)
	s_barrier
	s_setprio 1
	v_mfma_f32_16x16x128_f8f6f4 v[158:161], v[18:25], v[180:187], v[158:161]
	v_mfma_f32_16x16x128_f8f6f4 v[150:153], v[26:33], v[180:187], v[150:153]
	v_mfma_f32_16x16x128_f8f6f4 v[142:145], v[18:25], v[188:195], v[142:145]
	v_mfma_f32_16x16x128_f8f6f4 v[134:137], v[26:33], v[188:195], v[134:137]
	v_mfma_f32_16x16x128_f8f6f4 v[126:129], v[18:25], v[196:203], v[126:129]
	v_mfma_f32_16x16x128_f8f6f4 v[118:121], v[26:33], v[196:203], v[118:121]
	v_mfma_f32_16x16x128_f8f6f4 v[110:113], v[18:25], v[204:211], v[110:113]
	v_mfma_f32_16x16x128_f8f6f4 v[102:105], v[26:33], v[204:211], v[102:105]
	v_mfma_f32_16x16x128_f8f6f4 v[154:157], v[2:9], v[180:187], v[154:157]
	v_mfma_f32_16x16x128_f8f6f4 v[146:149], v[10:17], v[180:187], v[146:149]
	v_mfma_f32_16x16x128_f8f6f4 v[138:141], v[2:9], v[188:195], v[138:141]
	v_mfma_f32_16x16x128_f8f6f4 v[130:133], v[10:17], v[188:195], v[130:133]
	v_mfma_f32_16x16x128_f8f6f4 v[122:125], v[2:9], v[196:203], v[122:125]
	v_mfma_f32_16x16x128_f8f6f4 v[114:117], v[10:17], v[196:203], v[114:117]
	v_mfma_f32_16x16x128_f8f6f4 v[106:109], v[2:9], v[204:211], v[106:109]
	v_mfma_f32_16x16x128_f8f6f4 v[98:101], v[10:17], v[204:211], v[98:101]
	s_setprio 0
	s_barrier
	ds_read_b128 v[180:183], v175 offset:16384
	ds_read_b128 v[184:187], v175 offset:17408
	ds_read_b128 v[188:191], v175 offset:18432
	ds_read_b128 v[192:195], v175 offset:19456
	ds_read_b128 v[196:199], v175 offset:20480
	ds_read_b128 v[200:203], v175 offset:21504
	ds_read_b128 v[204:207], v175 offset:22528
	ds_read_b128 v[208:211], v175 offset:23552
	s_mov_b32 s33, m0
	s_mov_b32 m0, s34
	s_nop 2
	global_load_lds_dwordx4 v165, s[40:41]
	s_mov_b32 m0, s33
	s_add_u32 s54, s40, 0x20000
	s_mov_b32 s33, m0
	s_mov_b32 m0, s35
	s_nop 2
	global_load_lds_dwordx4 v167, s[40:41]
	s_mov_b32 m0, s33
	s_addc_u32 s55, s41, 0
	s_mov_b32 s33, m0
	s_mov_b32 m0, s36
	s_nop 2
	global_load_lds_dwordx4 v165, s[54:55]
	s_mov_b32 m0, s33
	s_mov_b32 s33, m0
	s_mov_b32 m0, s37
	s_nop 2
	global_load_lds_dwordx4 v167, s[54:55]
	s_mov_b32 m0, s33
	s_mov_b32 s33, m0
	s_mov_b32 m0, s31
	s_nop 2
	global_load_lds_dwordx4 v171, s[52:53]
	s_mov_b32 m0, s33
	s_mov_b32 s33, m0
	s_mov_b32 m0, s56
	s_nop 2
	global_load_lds_dwordx4 v173, s[52:53]
	s_mov_b32 m0, s33
	s_waitcnt vmcnt(8)
	s_waitcnt lgkmcnt(0)
	s_barrier
	s_setprio 1
	v_mfma_f32_16x16x128_f8f6f4 v[94:97], v[18:25], v[180:187], v[94:97]
	v_mfma_f32_16x16x128_f8f6f4 v[86:89], v[26:33], v[180:187], v[86:89]
	v_mfma_f32_16x16x128_f8f6f4 v[78:81], v[18:25], v[188:195], v[78:81]
	v_mfma_f32_16x16x128_f8f6f4 v[70:73], v[26:33], v[188:195], v[70:73]
	v_mfma_f32_16x16x128_f8f6f4 v[62:65], v[18:25], v[196:203], v[62:65]
	v_mfma_f32_16x16x128_f8f6f4 v[54:57], v[26:33], v[196:203], v[54:57]
	v_mfma_f32_16x16x128_f8f6f4 v[46:49], v[18:25], v[204:211], v[46:49]
	v_mfma_f32_16x16x128_f8f6f4 v[38:41], v[26:33], v[204:211], v[38:41]
	v_mfma_f32_16x16x128_f8f6f4 v[90:93], v[2:9], v[180:187], v[90:93]
	v_mfma_f32_16x16x128_f8f6f4 v[82:85], v[10:17], v[180:187], v[82:85]
	v_mfma_f32_16x16x128_f8f6f4 v[74:77], v[2:9], v[188:195], v[74:77]
	v_mfma_f32_16x16x128_f8f6f4 v[66:69], v[10:17], v[188:195], v[66:69]
	v_mfma_f32_16x16x128_f8f6f4 v[58:61], v[2:9], v[196:203], v[58:61]
	v_mfma_f32_16x16x128_f8f6f4 v[50:53], v[10:17], v[196:203], v[50:53]
	v_mfma_f32_16x16x128_f8f6f4 v[42:45], v[2:9], v[204:211], v[42:45]
	v_mfma_f32_16x16x128_f8f6f4 v[34:37], v[10:17], v[204:211], v[34:37]
	s_setprio 0
	s_barrier
	v_add_u32_e32 v14, 0x18000, v174
	v_add_u32_e32 v30, 0x1c000, v174
	ds_read_b128 v[2:5], v14
	ds_read_b128 v[6:9], v14 offset:1024
	ds_read_b128 v[10:13], v14 offset:2048
	ds_read_b128 v[14:17], v14 offset:3072
	ds_read_b128 v[18:21], v30
	ds_read_b128 v[22:25], v30 offset:1024
	ds_read_b128 v[26:29], v30 offset:2048
	ds_read_b128 v[30:33], v30 offset:3072
	ds_read_b128 v[180:183], v175 offset:32768
	ds_read_b128 v[184:187], v175 offset:33792
	ds_read_b128 v[188:191], v175 offset:34816
	ds_read_b128 v[192:195], v175 offset:35840
	ds_read_b128 v[196:199], v175 offset:36864
	ds_read_b128 v[200:203], v175 offset:37888
	ds_read_b128 v[204:207], v175 offset:38912
	ds_read_b128 v[208:211], v175 offset:39936
	s_mov_b32 s33, m0
	s_mov_b32 m0, s57
	s_nop 2
	global_load_lds_dwordx4 v177, s[52:53]
	s_mov_b32 m0, s33
	s_mov_b32 s33, m0
	s_mov_b32 m0, s63
	s_nop 2
	global_load_lds_dwordx4 v178, s[52:53]
	s_mov_b32 m0, s33
	s_waitcnt vmcnt(8)
	s_waitcnt lgkmcnt(0)
	s_barrier
	s_setprio 1
	v_mfma_f32_16x16x128_f8f6f4 v[158:161], v[2:9], v[180:187], v[158:161]
	v_mfma_f32_16x16x128_f8f6f4 v[150:153], v[10:17], v[180:187], v[150:153]
	v_mfma_f32_16x16x128_f8f6f4 v[142:145], v[2:9], v[188:195], v[142:145]
	v_mfma_f32_16x16x128_f8f6f4 v[134:137], v[10:17], v[188:195], v[134:137]
	v_mfma_f32_16x16x128_f8f6f4 v[126:129], v[2:9], v[196:203], v[126:129]
	v_mfma_f32_16x16x128_f8f6f4 v[118:121], v[10:17], v[196:203], v[118:121]
	v_mfma_f32_16x16x128_f8f6f4 v[110:113], v[2:9], v[204:211], v[110:113]
	v_mfma_f32_16x16x128_f8f6f4 v[102:105], v[10:17], v[204:211], v[102:105]
	v_mfma_f32_16x16x128_f8f6f4 v[154:157], v[18:25], v[180:187], v[154:157]
	v_mfma_f32_16x16x128_f8f6f4 v[146:149], v[26:33], v[180:187], v[146:149]
	v_mfma_f32_16x16x128_f8f6f4 v[138:141], v[18:25], v[188:195], v[138:141]
	v_mfma_f32_16x16x128_f8f6f4 v[130:133], v[26:33], v[188:195], v[130:133]
	v_mfma_f32_16x16x128_f8f6f4 v[122:125], v[18:25], v[196:203], v[122:125]
	v_mfma_f32_16x16x128_f8f6f4 v[114:117], v[26:33], v[196:203], v[114:117]
	v_mfma_f32_16x16x128_f8f6f4 v[106:109], v[18:25], v[204:211], v[106:109]
	v_mfma_f32_16x16x128_f8f6f4 v[98:101], v[26:33], v[204:211], v[98:101]
	s_setprio 0
	s_barrier
	ds_read_b128 v[180:183], v175 offset:49152
	ds_read_b128 v[184:187], v175 offset:50176
	ds_read_b128 v[188:191], v175 offset:51200
	ds_read_b128 v[192:195], v175 offset:52224
	ds_read_b128 v[196:199], v175 offset:53248
	ds_read_b128 v[200:203], v175 offset:54272
	ds_read_b128 v[204:207], v175 offset:55296
	ds_read_b128 v[208:211], v175 offset:56320
	s_mov_b32 s33, m0
	s_mov_b32 m0, s66
	s_nop 2
	global_load_lds_dwordx4 v165, s[44:45]
	s_mov_b32 m0, s33
	s_add_u32 s40, s40, 0x20080
	s_mov_b32 s33, m0
	s_mov_b32 m0, s67
	s_nop 2
	global_load_lds_dwordx4 v167, s[44:45]
	s_mov_b32 m0, s33
	s_addc_u32 s41, s41, 0
	s_mov_b32 s33, m0
	s_mov_b32 m0, s76
	s_nop 2
	global_load_lds_dwordx4 v165, s[40:41]
	s_mov_b32 m0, s33
	s_mov_b32 s33, m0
	s_mov_b32 m0, s77
	s_nop 2
	global_load_lds_dwordx4 v167, s[40:41]
	s_mov_b32 m0, s33
	s_mov_b32 s33, m0
	s_mov_b32 m0, s68
	s_nop 2
	global_load_lds_dwordx4 v171, s[42:43]
	s_mov_b32 m0, s33
	s_mov_b32 s33, m0
	s_mov_b32 m0, s69
	s_nop 2
	global_load_lds_dwordx4 v173, s[42:43]
	s_mov_b32 m0, s33
	s_waitcnt vmcnt(8)
	s_waitcnt lgkmcnt(0)
	s_barrier
	s_setprio 1
	v_mfma_f32_16x16x128_f8f6f4 v[94:97], v[2:9], v[180:187], v[94:97]
	v_mfma_f32_16x16x128_f8f6f4 v[86:89], v[10:17], v[180:187], v[86:89]
	v_mfma_f32_16x16x128_f8f6f4 v[78:81], v[2:9], v[188:195], v[78:81]
	v_mfma_f32_16x16x128_f8f6f4 v[70:73], v[10:17], v[188:195], v[70:73]
	v_mfma_f32_16x16x128_f8f6f4 v[62:65], v[2:9], v[196:203], v[62:65]
	v_mfma_f32_16x16x128_f8f6f4 v[54:57], v[10:17], v[196:203], v[54:57]
	v_mfma_f32_16x16x128_f8f6f4 v[46:49], v[2:9], v[204:211], v[46:49]
	v_mfma_f32_16x16x128_f8f6f4 v[38:41], v[10:17], v[204:211], v[38:41]
	v_mfma_f32_16x16x128_f8f6f4 v[90:93], v[18:25], v[180:187], v[90:93]
	v_mfma_f32_16x16x128_f8f6f4 v[82:85], v[26:33], v[180:187], v[82:85]
	v_mfma_f32_16x16x128_f8f6f4 v[74:77], v[18:25], v[188:195], v[74:77]
	v_mfma_f32_16x16x128_f8f6f4 v[66:69], v[26:33], v[188:195], v[66:69]
	v_mfma_f32_16x16x128_f8f6f4 v[58:61], v[18:25], v[196:203], v[58:61]
	v_mfma_f32_16x16x128_f8f6f4 v[50:53], v[26:33], v[196:203], v[50:53]
	v_mfma_f32_16x16x128_f8f6f4 v[42:45], v[18:25], v[204:211], v[42:45]
	v_mfma_f32_16x16x128_f8f6f4 v[34:37], v[26:33], v[204:211], v[34:37]
	s_setprio 0
	s_barrier
	s_add_i32 s88, s88, 2
	s_add_u32 s86, s86, 0x100
	s_addc_u32 s87, s87, 0
	s_cmp_gt_u32 s88, 5
	s_cbranch_scc1 .LBB0_1957

.LBB0_2092:
	s_cmp_eq_u32 s91, 0
	s_cbranch_scc1 .Lpeel7
	s_lshl_b32 s33, s91, 7
	s_add_u32 s52, s36, s33
	s_addc_u32 s53, s37, 0
	s_add_u32 s46, s52, 0x100
	s_addc_u32 s47, s53, 0
	s_and_b64 s[44:45], s[42:43], exec
	s_cselect_b32 s49, s15, s47
	s_cselect_b32 s48, s17, s46
	s_add_u32 s33, s26, s33
	v_add_u32_e32 v2, 0x10000, v171
	v_add_u32_e32 v14, 0x14000, v171
	s_addc_u32 s44, s27, 0
	ds_read_b128 v[18:21], v2
	ds_read_b128 v[22:25], v2 offset:1024
	ds_read_b128 v[26:29], v2 offset:2048
	ds_read_b128 v[30:33], v2 offset:3072
	ds_read_b128 v[2:5], v14
	ds_read_b128 v[6:9], v14 offset:1024
	ds_read_b128 v[10:13], v14 offset:2048
	ds_read_b128 v[14:17], v14 offset:3072
	s_add_u32 s33, s33, 0x100
	s_addc_u32 s44, s44, 0
	s_and_b64 s[42:43], s[42:43], exec
	s_cselect_b32 s43, s19, s44
	s_cselect_b32 s42, s18, s33
	s_add_u32 s44, s48, 0x80
	s_addc_u32 s45, s49, 0
	s_add_u32 s46, s42, 0x80
	s_addc_u32 s47, s43, 0
	ds_read_b128 v[176:179], v172
	ds_read_b128 v[180:183], v172 offset:1024
	ds_read_b128 v[184:187], v172 offset:2048
	ds_read_b128 v[188:191], v172 offset:3072
	ds_read_b128 v[192:195], v172 offset:4096
	ds_read_b128 v[196:199], v172 offset:5120
	ds_read_b128 v[200:203], v172 offset:6144
	ds_read_b128 v[204:207], v172 offset:7168
	s_add_u32 s52, s52, 0x20080
	s_addc_u32 s53, s53, 0
	s_mov_b32 s33, m0
	s_mov_b32 m0, s79
	s_nop 2
	global_load_lds_dwordx4 v163, s[52:53]
	s_mov_b32 m0, s33
	s_mov_b32 s33, m0
	s_mov_b32 m0, s80
	s_nop 2
	global_load_lds_dwordx4 v164, s[52:53]
	s_mov_b32 m0, s33
	s_waitcnt vmcnt(8)
	s_waitcnt lgkmcnt(0)
	s_barrier
	s_setprio 1
	v_mfma_f32_16x16x128_f8f6f4 v[158:161], v[18:25], v[176:183], v[158:161]
	v_mfma_f32_16x16x128_f8f6f4 v[154:157], v[26:33], v[176:183], v[154:157]
	v_mfma_f32_16x16x128_f8f6f4 v[142:145], v[18:25], v[184:191], v[142:145]
	v_mfma_f32_16x16x128_f8f6f4 v[138:141], v[26:33], v[184:191], v[138:141]
	v_mfma_f32_16x16x128_f8f6f4 v[126:129], v[18:25], v[192:199], v[126:129]
	v_mfma_f32_16x16x128_f8f6f4 v[122:125], v[26:33], v[192:199], v[122:125]
	v_mfma_f32_16x16x128_f8f6f4 v[110:113], v[18:25], v[200:207], v[110:113]
	v_mfma_f32_16x16x128_f8f6f4 v[106:109], v[26:33], v[200:207], v[106:109]
	v_mfma_f32_16x16x128_f8f6f4 v[150:153], v[2:9], v[176:183], v[150:153]
	v_mfma_f32_16x16x128_f8f6f4 v[146:149], v[10:17], v[176:183], v[146:149]
	v_mfma_f32_16x16x128_f8f6f4 v[134:137], v[2:9], v[184:191], v[134:137]
	v_mfma_f32_16x16x128_f8f6f4 v[130:133], v[10:17], v[184:191], v[130:133]
	v_mfma_f32_16x16x128_f8f6f4 v[118:121], v[2:9], v[192:199], v[118:121]
	v_mfma_f32_16x16x128_f8f6f4 v[114:117], v[10:17], v[192:199], v[114:117]
	v_mfma_f32_16x16x128_f8f6f4 v[102:105], v[2:9], v[200:207], v[102:105]
	v_mfma_f32_16x16x128_f8f6f4 v[98:101], v[10:17], v[200:207], v[98:101]
	s_setprio 0
	s_barrier
	ds_read_b128 v[176:179], v172 offset:16384
	ds_read_b128 v[180:183], v172 offset:17408
	ds_read_b128 v[184:187], v172 offset:18432
	ds_read_b128 v[188:191], v172 offset:19456
	ds_read_b128 v[192:195], v172 offset:20480
	ds_read_b128 v[196:199], v172 offset:21504
	ds_read_b128 v[200:203], v172 offset:22528
	ds_read_b128 v[204:207], v172 offset:23552
	s_mov_b32 s33, m0
	s_mov_b32 m0, s64
	s_nop 2
	global_load_lds_dwordx4 v1, s[42:43]
	s_mov_b32 m0, s33
	s_add_u32 s52, s42, 0x20000
	s_mov_b32 s33, m0
	s_mov_b32 m0, s65
	s_nop 2
	global_load_lds_dwordx4 v162, s[42:43]
	s_mov_b32 m0, s33
	s_addc_u32 s53, s43, 0
	s_mov_b32 s33, m0
	s_mov_b32 m0, s24
	s_nop 2
	global_load_lds_dwordx4 v1, s[52:53]
	s_mov_b32 m0, s33
	s_mov_b32 s33, m0
	s_mov_b32 m0, s25
	s_nop 2
	global_load_lds_dwordx4 v162, s[52:53]
	s_mov_b32 m0, s33
	s_mov_b32 s33, m0
	s_mov_b32 m0, s63
	s_nop 2
	global_load_lds_dwordx4 v163, s[48:49]
	s_mov_b32 m0, s33
	s_mov_b32 s33, m0
	s_mov_b32 m0, s2
	s_nop 2
	global_load_lds_dwordx4 v164, s[48:49]
	s_mov_b32 m0, s33
	s_waitcnt vmcnt(8)
	s_waitcnt lgkmcnt(0)
	s_barrier
	s_setprio 1
	v_mfma_f32_16x16x128_f8f6f4 v[94:97], v[18:25], v[176:183], v[94:97]
	v_mfma_f32_16x16x128_f8f6f4 v[90:93], v[26:33], v[176:183], v[90:93]
	v_mfma_f32_16x16x128_f8f6f4 v[78:81], v[18:25], v[184:191], v[78:81]
	v_mfma_f32_16x16x128_f8f6f4 v[74:77], v[26:33], v[184:191], v[74:77]
	v_mfma_f32_16x16x128_f8f6f4 v[62:65], v[18:25], v[192:199], v[62:65]
	v_mfma_f32_16x16x128_f8f6f4 v[58:61], v[26:33], v[192:199], v[58:61]
	v_mfma_f32_16x16x128_f8f6f4 v[46:49], v[18:25], v[200:207], v[46:49]
	v_mfma_f32_16x16x128_f8f6f4 v[42:45], v[26:33], v[200:207], v[42:45]
	v_mfma_f32_16x16x128_f8f6f4 v[86:89], v[2:9], v[176:183], v[86:89]
	v_mfma_f32_16x16x128_f8f6f4 v[82:85], v[10:17], v[176:183], v[82:85]
	v_mfma_f32_16x16x128_f8f6f4 v[70:73], v[2:9], v[184:191], v[70:73]
	v_mfma_f32_16x16x128_f8f6f4 v[66:69], v[10:17], v[184:191], v[66:69]
	v_mfma_f32_16x16x128_f8f6f4 v[54:57], v[2:9], v[192:199], v[54:57]
	v_mfma_f32_16x16x128_f8f6f4 v[50:53], v[10:17], v[192:199], v[50:53]
	v_mfma_f32_16x16x128_f8f6f4 v[38:41], v[2:9], v[200:207], v[38:41]
	v_mfma_f32_16x16x128_f8f6f4 v[34:37], v[10:17], v[200:207], v[34:37]
	s_setprio 0
	s_barrier
.Lmid7:
	v_add_u32_e32 v14, 0x18000, v171
	v_add_u32_e32 v30, 0x1c000, v171
	ds_read_b128 v[2:5], v14
	ds_read_b128 v[6:9], v14 offset:1024
	ds_read_b128 v[10:13], v14 offset:2048
	ds_read_b128 v[14:17], v14 offset:3072
	ds_read_b128 v[18:21], v30
	ds_read_b128 v[22:25], v30 offset:1024
	ds_read_b128 v[26:29], v30 offset:2048
	ds_read_b128 v[30:33], v30 offset:3072
	ds_read_b128 v[176:179], v172 offset:32768
	ds_read_b128 v[180:183], v172 offset:33792
	ds_read_b128 v[184:187], v172 offset:34816
	ds_read_b128 v[188:191], v172 offset:35840
	ds_read_b128 v[192:195], v172 offset:36864
	ds_read_b128 v[196:199], v172 offset:37888
	ds_read_b128 v[200:203], v172 offset:38912
	ds_read_b128 v[204:207], v172 offset:39936
	s_add_u32 s48, s48, 0x20000
	s_addc_u32 s49, s49, 0
	s_mov_b32 s33, m0
	s_mov_b32 m0, s23
	s_nop 2
	global_load_lds_dwordx4 v163, s[48:49]
	s_mov_b32 m0, s33
	s_mov_b32 s33, m0
	s_mov_b32 m0, s28
	s_nop 2
	global_load_lds_dwordx4 v164, s[48:49]
	s_mov_b32 m0, s33
	s_waitcnt vmcnt(8)
	s_waitcnt lgkmcnt(0)
	s_barrier
	s_setprio 1
	v_mfma_f32_16x16x128_f8f6f4 v[158:161], v[2:9], v[176:183], v[158:161]
	v_mfma_f32_16x16x128_f8f6f4 v[154:157], v[10:17], v[176:183], v[154:157]
	v_mfma_f32_16x16x128_f8f6f4 v[142:145], v[2:9], v[184:191], v[142:145]
	v_mfma_f32_16x16x128_f8f6f4 v[138:141], v[10:17], v[184:191], v[138:141]
	v_mfma_f32_16x16x128_f8f6f4 v[126:129], v[2:9], v[192:199], v[126:129]
	v_mfma_f32_16x16x128_f8f6f4 v[122:125], v[10:17], v[192:199], v[122:125]
	v_mfma_f32_16x16x128_f8f6f4 v[110:113], v[2:9], v[200:207], v[110:113]
	v_mfma_f32_16x16x128_f8f6f4 v[106:109], v[10:17], v[200:207], v[106:109]
	v_mfma_f32_16x16x128_f8f6f4 v[150:153], v[18:25], v[176:183], v[150:153]
	v_mfma_f32_16x16x128_f8f6f4 v[146:149], v[26:33], v[176:183], v[146:149]
	v_mfma_f32_16x16x128_f8f6f4 v[134:137], v[18:25], v[184:191], v[134:137]
	v_mfma_f32_16x16x128_f8f6f4 v[130:133], v[26:33], v[184:191], v[130:133]
	v_mfma_f32_16x16x128_f8f6f4 v[118:121], v[18:25], v[192:199], v[118:121]
	v_mfma_f32_16x16x128_f8f6f4 v[114:117], v[26:33], v[192:199], v[114:117]
	v_mfma_f32_16x16x128_f8f6f4 v[102:105], v[18:25], v[200:207], v[102:105]
	v_mfma_f32_16x16x128_f8f6f4 v[98:101], v[26:33], v[200:207], v[98:101]
	s_setprio 0
	s_barrier
	ds_read_b128 v[176:179], v172 offset:49152
	ds_read_b128 v[180:183], v172 offset:50176
	ds_read_b128 v[184:187], v172 offset:51200
	ds_read_b128 v[188:191], v172 offset:52224
	ds_read_b128 v[192:195], v172 offset:53248
	ds_read_b128 v[196:199], v172 offset:54272
	ds_read_b128 v[200:203], v172 offset:55296
	ds_read_b128 v[204:207], v172 offset:56320
	s_mov_b32 s33, m0
	s_mov_b32 m0, s67
	s_nop 2
	global_load_lds_dwordx4 v1, s[46:47]
	s_mov_b32 m0, s33
	s_add_u32 s42, s42, 0x20080
	s_mov_b32 s33, m0
	s_mov_b32 m0, s68
	s_nop 2
	global_load_lds_dwordx4 v162, s[46:47]
	s_mov_b32 m0, s33
	s_addc_u32 s43, s43, 0
	s_mov_b32 s33, m0
	s_mov_b32 m0, s77
	s_nop 2
	global_load_lds_dwordx4 v1, s[42:43]
	s_mov_b32 m0, s33
	s_mov_b32 s33, m0
	s_mov_b32 m0, s78
	s_nop 2
	global_load_lds_dwordx4 v162, s[42:43]
	s_mov_b32 m0, s33
	s_mov_b32 s33, m0
	s_mov_b32 m0, s69
	s_nop 2
	global_load_lds_dwordx4 v163, s[44:45]
	s_mov_b32 m0, s33
	s_mov_b32 s33, m0
	s_mov_b32 m0, s76
	s_nop 2
	global_load_lds_dwordx4 v164, s[44:45]
	s_mov_b32 m0, s33
	s_waitcnt vmcnt(8)
	s_waitcnt lgkmcnt(0)
	s_barrier
	s_setprio 1
	v_mfma_f32_16x16x128_f8f6f4 v[94:97], v[2:9], v[176:183], v[94:97]
	v_mfma_f32_16x16x128_f8f6f4 v[90:93], v[10:17], v[176:183], v[90:93]
	v_mfma_f32_16x16x128_f8f6f4 v[78:81], v[2:9], v[184:191], v[78:81]
	v_mfma_f32_16x16x128_f8f6f4 v[74:77], v[10:17], v[184:191], v[74:77]
	v_mfma_f32_16x16x128_f8f6f4 v[62:65], v[2:9], v[192:199], v[62:65]
	v_mfma_f32_16x16x128_f8f6f4 v[58:61], v[10:17], v[192:199], v[58:61]
	v_mfma_f32_16x16x128_f8f6f4 v[46:49], v[2:9], v[200:207], v[46:49]
	v_mfma_f32_16x16x128_f8f6f4 v[42:45], v[10:17], v[200:207], v[42:45]
	v_mfma_f32_16x16x128_f8f6f4 v[86:89], v[18:25], v[176:183], v[86:89]
	v_mfma_f32_16x16x128_f8f6f4 v[82:85], v[26:33], v[176:183], v[82:85]
	v_mfma_f32_16x16x128_f8f6f4 v[70:73], v[18:25], v[184:191], v[70:73]
	v_mfma_f32_16x16x128_f8f6f4 v[66:69], v[26:33], v[184:191], v[66:69]
	v_mfma_f32_16x16x128_f8f6f4 v[54:57], v[18:25], v[192:199], v[54:57]
	v_mfma_f32_16x16x128_f8f6f4 v[50:53], v[26:33], v[192:199], v[50:53]
	v_mfma_f32_16x16x128_f8f6f4 v[38:41], v[18:25], v[200:207], v[38:41]
	v_mfma_f32_16x16x128_f8f6f4 v[34:37], v[26:33], v[200:207], v[34:37]
	s_setprio 0
	s_cmp_lt_u32 s91, 6
	s_cbranch_scc1 .Lkb7_do
	s_cmp_lg_u64 s[12:13], 0
	s_cbranch_scc0 .Lkb7_skip

.Lpeel7:
	s_lshl_b32 s33, s91, 7
	s_add_u32 s52, s36, s33
	s_addc_u32 s53, s37, 0
	s_add_u32 s46, s52, 0x100
	s_addc_u32 s47, s53, 0
	s_and_b64 s[44:45], s[42:43], exec
	s_cselect_b32 s49, s15, s47
	s_cselect_b32 s48, s17, s46
	s_add_u32 s33, s26, s33
	v_add_u32_e32 v2, 0x10000, v171
	v_add_u32_e32 v14, 0x14000, v171
	s_addc_u32 s44, s27, 0
	ds_read_b128 v[18:21], v2
	ds_read_b128 v[22:25], v2 offset:1024
	ds_read_b128 v[26:29], v2 offset:2048
	ds_read_b128 v[30:33], v2 offset:3072
	ds_read_b128 v[2:5], v14
	ds_read_b128 v[6:9], v14 offset:1024
	ds_read_b128 v[10:13], v14 offset:2048
	ds_read_b128 v[14:17], v14 offset:3072
	s_add_u32 s33, s33, 0x100
	s_addc_u32 s44, s44, 0
	s_and_b64 s[42:43], s[42:43], exec
	s_cselect_b32 s43, s19, s44
	s_cselect_b32 s42, s18, s33
	s_add_u32 s44, s48, 0x80
	s_addc_u32 s45, s49, 0
	s_add_u32 s46, s42, 0x80
	s_addc_u32 s47, s43, 0
	ds_read_b128 v[176:179], v172
	ds_read_b128 v[180:183], v172 offset:1024
	ds_read_b128 v[184:187], v172 offset:2048
	ds_read_b128 v[188:191], v172 offset:3072
	ds_read_b128 v[192:195], v172 offset:4096
	ds_read_b128 v[196:199], v172 offset:5120
	ds_read_b128 v[200:203], v172 offset:6144
	ds_read_b128 v[204:207], v172 offset:7168
	s_add_u32 s52, s52, 0x20080
	s_addc_u32 s53, s53, 0
	s_mov_b32 s33, m0
	s_mov_b32 m0, s79
	s_nop 2
	global_load_lds_dwordx4 v163, s[52:53]
	s_mov_b32 m0, s33
	s_mov_b32 s33, m0
	s_mov_b32 m0, s80
	s_nop 2
	global_load_lds_dwordx4 v164, s[52:53]
	s_mov_b32 m0, s33
	s_waitcnt vmcnt(8)
	s_waitcnt lgkmcnt(0)
	s_barrier
	s_setprio 1
	v_mfma_f32_16x16x128_f8f6f4 v[158:161], v[18:25], v[176:183], 0
	v_mfma_f32_16x16x128_f8f6f4 v[154:157], v[26:33], v[176:183], 0
	v_mfma_f32_16x16x128_f8f6f4 v[142:145], v[18:25], v[184:191], 0
	v_mfma_f32_16x16x128_f8f6f4 v[138:141], v[26:33], v[184:191], 0
	v_mfma_f32_16x16x128_f8f6f4 v[126:129], v[18:25], v[192:199], 0
	v_mfma_f32_16x16x128_f8f6f4 v[122:125], v[26:33], v[192:199], 0
	v_mfma_f32_16x16x128_f8f6f4 v[110:113], v[18:25], v[200:207], 0
	v_mfma_f32_16x16x128_f8f6f4 v[106:109], v[26:33], v[200:207], 0
	v_mfma_f32_16x16x128_f8f6f4 v[150:153], v[2:9], v[176:183], 0
	v_mfma_f32_16x16x128_f8f6f4 v[146:149], v[10:17], v[176:183], 0
	v_mfma_f32_16x16x128_f8f6f4 v[134:137], v[2:9], v[184:191], 0
	v_mfma_f32_16x16x128_f8f6f4 v[130:133], v[10:17], v[184:191], 0
	v_mfma_f32_16x16x128_f8f6f4 v[118:121], v[2:9], v[192:199], 0
	v_mfma_f32_16x16x128_f8f6f4 v[114:117], v[10:17], v[192:199], 0
	v_mfma_f32_16x16x128_f8f6f4 v[102:105], v[2:9], v[200:207], 0
	v_mfma_f32_16x16x128_f8f6f4 v[98:101], v[10:17], v[200:207], 0
	s_setprio 0
	s_barrier
	ds_read_b128 v[176:179], v172 offset:16384
	ds_read_b128 v[180:183], v172 offset:17408
	ds_read_b128 v[184:187], v172 offset:18432
	ds_read_b128 v[188:191], v172 offset:19456
	ds_read_b128 v[192:195], v172 offset:20480
	ds_read_b128 v[196:199], v172 offset:21504
	ds_read_b128 v[200:203], v172 offset:22528
	ds_read_b128 v[204:207], v172 offset:23552
	s_mov_b32 s33, m0
	s_mov_b32 m0, s64
	s_nop 2
	global_load_lds_dwordx4 v1, s[42:43]
	s_mov_b32 m0, s33
	s_add_u32 s52, s42, 0x20000
	s_mov_b32 s33, m0
	s_mov_b32 m0, s65
	s_nop 2
	global_load_lds_dwordx4 v162, s[42:43]
	s_mov_b32 m0, s33
	s_addc_u32 s53, s43, 0
	s_mov_b32 s33, m0
	s_mov_b32 m0, s24
	s_nop 2
	global_load_lds_dwordx4 v1, s[52:53]
	s_mov_b32 m0, s33
	s_mov_b32 s33, m0
	s_mov_b32 m0, s25
	s_nop 2
	global_load_lds_dwordx4 v162, s[52:53]
	s_mov_b32 m0, s33
	s_mov_b32 s33, m0
	s_mov_b32 m0, s63
	s_nop 2
	global_load_lds_dwordx4 v163, s[48:49]
	s_mov_b32 m0, s33
	s_mov_b32 s33, m0
	s_mov_b32 m0, s2
	s_nop 2
	global_load_lds_dwordx4 v164, s[48:49]
	s_mov_b32 m0, s33
	s_waitcnt vmcnt(8)
	s_waitcnt lgkmcnt(0)
	s_barrier
	s_setprio 1
	v_mfma_f32_16x16x128_f8f6f4 v[94:97], v[18:25], v[176:183], 0
	v_mfma_f32_16x16x128_f8f6f4 v[90:93], v[26:33], v[176:183], 0
	v_mfma_f32_16x16x128_f8f6f4 v[78:81], v[18:25], v[184:191], 0
	v_mfma_f32_16x16x128_f8f6f4 v[74:77], v[26:33], v[184:191], 0
	v_mfma_f32_16x16x128_f8f6f4 v[62:65], v[18:25], v[192:199], 0
	v_mfma_f32_16x16x128_f8f6f4 v[58:61], v[26:33], v[192:199], 0
	v_mfma_f32_16x16x128_f8f6f4 v[46:49], v[18:25], v[200:207], 0
	v_mfma_f32_16x16x128_f8f6f4 v[42:45], v[26:33], v[200:207], 0
	v_mfma_f32_16x16x128_f8f6f4 v[86:89], v[2:9], v[176:183], 0
	v_mfma_f32_16x16x128_f8f6f4 v[82:85], v[10:17], v[176:183], 0
	v_mfma_f32_16x16x128_f8f6f4 v[70:73], v[2:9], v[184:191], 0
	v_mfma_f32_16x16x128_f8f6f4 v[66:69], v[10:17], v[184:191], 0
	v_mfma_f32_16x16x128_f8f6f4 v[54:57], v[2:9], v[192:199], 0
	v_mfma_f32_16x16x128_f8f6f4 v[50:53], v[10:17], v[192:199], 0
	v_mfma_f32_16x16x128_f8f6f4 v[38:41], v[2:9], v[200:207], 0
	v_mfma_f32_16x16x128_f8f6f4 v[34:37], v[10:17], v[200:207], 0
	s_setprio 0
	s_barrier
	s_branch .Lmid7

.LBB0_2128:
	v_add_u32_e32 v0, 0x10000, v169
	v_add_u32_e32 v12, 0x14000, v169
	s_add_u32 s26, s22, 0x100
	ds_read_b128 v[16:19], v0
	ds_read_b128 v[20:23], v0 offset:1024
	ds_read_b128 v[24:27], v0 offset:2048
	ds_read_b128 v[28:31], v0 offset:3072
	ds_read_b128 v[0:3], v12
	ds_read_b128 v[4:7], v12 offset:1024
	ds_read_b128 v[8:11], v12 offset:2048
	ds_read_b128 v[12:15], v12 offset:3072
	s_addc_u32 s27, s23, 0
	s_cmp_eq_u32 s83, 4
	s_cselect_b32 s42, s15, s26
	s_cselect_b32 s43, s13, s27
	s_cselect_b32 s37, s17, s82
	s_cselect_b32 s36, s16, s81
	s_add_u32 s38, s42, 0x80
	s_addc_u32 s39, s43, 0
	s_add_u32 s40, s36, 0x80
	s_addc_u32 s41, s37, 0
	ds_read_b128 v[172:175], v170
	ds_read_b128 v[176:179], v170 offset:1024
	ds_read_b128 v[180:183], v170 offset:2048
	ds_read_b128 v[184:187], v170 offset:3072
	ds_read_b128 v[188:191], v170 offset:4096
	ds_read_b128 v[192:195], v170 offset:5120
	ds_read_b128 v[196:199], v170 offset:6144
	ds_read_b128 v[200:203], v170 offset:7168
	s_add_u32 s22, s22, 0x20080
	s_addc_u32 s23, s23, 0
	s_mov_b32 s33, m0
	s_mov_b32 m0, s64
	s_nop 2
	global_load_lds_dwordx4 v162, s[22:23]
	s_mov_b32 m0, s33
	s_mov_b32 s33, m0
	s_mov_b32 m0, s65
	s_nop 2
	global_load_lds_dwordx4 v164, s[22:23]
	s_mov_b32 m0, s33
	s_waitcnt vmcnt(8)
	s_waitcnt lgkmcnt(0)
	s_barrier
	s_setprio 1
	v_mfma_f32_16x16x128_f8f6f4 v[156:159], v[16:23], v[172:179], v[156:159]
	v_mfma_f32_16x16x128_f8f6f4 v[152:155], v[24:31], v[172:179], v[152:155]
	v_mfma_f32_16x16x128_f8f6f4 v[140:143], v[16:23], v[180:187], v[140:143]
	v_mfma_f32_16x16x128_f8f6f4 v[136:139], v[24:31], v[180:187], v[136:139]
	v_mfma_f32_16x16x128_f8f6f4 v[124:127], v[16:23], v[188:195], v[124:127]
	v_mfma_f32_16x16x128_f8f6f4 v[120:123], v[24:31], v[188:195], v[120:123]
	v_mfma_f32_16x16x128_f8f6f4 v[108:111], v[16:23], v[196:203], v[108:111]
	v_mfma_f32_16x16x128_f8f6f4 v[104:107], v[24:31], v[196:203], v[104:107]
	v_mfma_f32_16x16x128_f8f6f4 v[148:151], v[0:7], v[172:179], v[148:151]
	v_mfma_f32_16x16x128_f8f6f4 v[144:147], v[8:15], v[172:179], v[144:147]
	v_mfma_f32_16x16x128_f8f6f4 v[132:135], v[0:7], v[180:187], v[132:135]
	v_mfma_f32_16x16x128_f8f6f4 v[128:131], v[8:15], v[180:187], v[128:131]
	v_mfma_f32_16x16x128_f8f6f4 v[116:119], v[0:7], v[188:195], v[116:119]
	v_mfma_f32_16x16x128_f8f6f4 v[112:115], v[8:15], v[188:195], v[112:115]
	v_mfma_f32_16x16x128_f8f6f4 v[100:103], v[0:7], v[196:203], v[100:103]
	v_mfma_f32_16x16x128_f8f6f4 v[96:99], v[8:15], v[196:203], v[96:99]
	s_setprio 0
	s_barrier
	ds_read_b128 v[172:175], v170 offset:16384
	ds_read_b128 v[176:179], v170 offset:17408
	ds_read_b128 v[180:183], v170 offset:18432
	ds_read_b128 v[184:187], v170 offset:19456
	ds_read_b128 v[188:191], v170 offset:20480
	ds_read_b128 v[192:195], v170 offset:21504
	ds_read_b128 v[196:199], v170 offset:22528
	ds_read_b128 v[200:203], v170 offset:23552
	s_mov_b32 s22, m0
	s_mov_b32 m0, s31
	s_nop 2
	global_load_lds_dwordx4 v163, s[36:37]
	s_mov_b32 m0, s22
	s_mov_b32 s22, m0
	s_mov_b32 m0, s44
	s_nop 2
	global_load_lds_dwordx4 v165, s[36:37]
	s_mov_b32 m0, s22
	s_add_u32 s22, s36, 0x20000
	s_addc_u32 s23, s37, 0
	s_mov_b32 s33, m0
	s_mov_b32 m0, s45
	s_nop 2
	global_load_lds_dwordx4 v163, s[22:23]
	s_mov_b32 m0, s33
	s_mov_b32 s33, m0
	s_mov_b32 m0, s46
	s_nop 2
	global_load_lds_dwordx4 v165, s[22:23]
	s_mov_b32 m0, s33
	s_mov_b32 s22, m0
	s_mov_b32 m0, s21
	s_nop 2
	global_load_lds_dwordx4 v162, s[42:43]
	s_mov_b32 m0, s22
	s_mov_b32 s22, m0
	s_mov_b32 m0, s47
	s_nop 2
	global_load_lds_dwordx4 v164, s[42:43]
	s_mov_b32 m0, s22
	s_waitcnt vmcnt(8)
	s_waitcnt lgkmcnt(0)
	s_barrier
	s_setprio 1
	v_mfma_f32_16x16x128_f8f6f4 v[92:95], v[16:23], v[172:179], v[92:95]
	v_mfma_f32_16x16x128_f8f6f4 v[88:91], v[24:31], v[172:179], v[88:91]
	v_mfma_f32_16x16x128_f8f6f4 v[76:79], v[16:23], v[180:187], v[76:79]
	v_mfma_f32_16x16x128_f8f6f4 v[72:75], v[24:31], v[180:187], v[72:75]
	v_mfma_f32_16x16x128_f8f6f4 v[60:63], v[16:23], v[188:195], v[60:63]
	v_mfma_f32_16x16x128_f8f6f4 v[56:59], v[24:31], v[188:195], v[56:59]
	v_mfma_f32_16x16x128_f8f6f4 v[44:47], v[16:23], v[196:203], v[44:47]
	v_mfma_f32_16x16x128_f8f6f4 v[40:43], v[24:31], v[196:203], v[40:43]
	v_mfma_f32_16x16x128_f8f6f4 v[84:87], v[0:7], v[172:179], v[84:87]
	v_mfma_f32_16x16x128_f8f6f4 v[80:83], v[8:15], v[172:179], v[80:83]
	v_mfma_f32_16x16x128_f8f6f4 v[68:71], v[0:7], v[180:187], v[68:71]
	v_mfma_f32_16x16x128_f8f6f4 v[64:67], v[8:15], v[180:187], v[64:67]
	v_mfma_f32_16x16x128_f8f6f4 v[52:55], v[0:7], v[188:195], v[52:55]
	v_mfma_f32_16x16x128_f8f6f4 v[48:51], v[8:15], v[188:195], v[48:51]
	v_mfma_f32_16x16x128_f8f6f4 v[36:39], v[0:7], v[196:203], v[36:39]
	v_mfma_f32_16x16x128_f8f6f4 v[32:35], v[8:15], v[196:203], v[32:35]
	s_setprio 0
	s_barrier
	v_add_u32_e32 v12, 0x18000, v169
	v_add_u32_e32 v28, 0x1c000, v169
	ds_read_b128 v[0:3], v12
	ds_read_b128 v[4:7], v12 offset:1024
	ds_read_b128 v[8:11], v12 offset:2048
	ds_read_b128 v[12:15], v12 offset:3072
	ds_read_b128 v[16:19], v28
	ds_read_b128 v[20:23], v28 offset:1024
	ds_read_b128 v[24:27], v28 offset:2048
	ds_read_b128 v[28:31], v28 offset:3072
	ds_read_b128 v[172:175], v170 offset:32768
	ds_read_b128 v[176:179], v170 offset:33792
	ds_read_b128 v[180:183], v170 offset:34816
	ds_read_b128 v[184:187], v170 offset:35840
	ds_read_b128 v[188:191], v170 offset:36864
	ds_read_b128 v[192:195], v170 offset:37888
	ds_read_b128 v[196:199], v170 offset:38912
	ds_read_b128 v[200:203], v170 offset:39936
	s_add_u32 s22, s42, 0x20000
	s_addc_u32 s23, s43, 0
	s_mov_b32 s33, m0
	s_mov_b32 m0, s48
	s_nop 2
	global_load_lds_dwordx4 v162, s[22:23]
	s_mov_b32 m0, s33
	s_mov_b32 s33, m0
	s_mov_b32 m0, s49
	s_nop 2
	global_load_lds_dwordx4 v164, s[22:23]
	s_mov_b32 m0, s33
	s_waitcnt vmcnt(8)
	s_waitcnt lgkmcnt(0)
	s_barrier
	s_setprio 1
	v_mfma_f32_16x16x128_f8f6f4 v[156:159], v[0:7], v[172:179], v[156:159]
	v_mfma_f32_16x16x128_f8f6f4 v[152:155], v[8:15], v[172:179], v[152:155]
	v_mfma_f32_16x16x128_f8f6f4 v[140:143], v[0:7], v[180:187], v[140:143]
	v_mfma_f32_16x16x128_f8f6f4 v[136:139], v[8:15], v[180:187], v[136:139]
	v_mfma_f32_16x16x128_f8f6f4 v[124:127], v[0:7], v[188:195], v[124:127]
	v_mfma_f32_16x16x128_f8f6f4 v[120:123], v[8:15], v[188:195], v[120:123]
	v_mfma_f32_16x16x128_f8f6f4 v[108:111], v[0:7], v[196:203], v[108:111]
	v_mfma_f32_16x16x128_f8f6f4 v[104:107], v[8:15], v[196:203], v[104:107]
	v_mfma_f32_16x16x128_f8f6f4 v[148:151], v[16:23], v[172:179], v[148:151]
	v_mfma_f32_16x16x128_f8f6f4 v[144:147], v[24:31], v[172:179], v[144:147]
	v_mfma_f32_16x16x128_f8f6f4 v[132:135], v[16:23], v[180:187], v[132:135]
	v_mfma_f32_16x16x128_f8f6f4 v[128:131], v[24:31], v[180:187], v[128:131]
	v_mfma_f32_16x16x128_f8f6f4 v[116:119], v[16:23], v[188:195], v[116:119]
	v_mfma_f32_16x16x128_f8f6f4 v[112:115], v[24:31], v[188:195], v[112:115]
	v_mfma_f32_16x16x128_f8f6f4 v[100:103], v[16:23], v[196:203], v[100:103]
	v_mfma_f32_16x16x128_f8f6f4 v[96:99], v[24:31], v[196:203], v[96:99]
	s_setprio 0
	s_barrier
	ds_read_b128 v[172:175], v170 offset:49152
	ds_read_b128 v[176:179], v170 offset:50176
	ds_read_b128 v[180:183], v170 offset:51200
	ds_read_b128 v[184:187], v170 offset:52224
	ds_read_b128 v[188:191], v170 offset:53248
	ds_read_b128 v[192:195], v170 offset:54272
	ds_read_b128 v[196:199], v170 offset:55296
	ds_read_b128 v[200:203], v170 offset:56320
	s_mov_b32 s22, m0
	s_mov_b32 m0, s58
	s_nop 2
	global_load_lds_dwordx4 v163, s[40:41]
	s_mov_b32 m0, s22
	s_mov_b32 s22, m0
	s_mov_b32 m0, s59
	s_nop 2
	global_load_lds_dwordx4 v165, s[40:41]
	s_mov_b32 m0, s22
	s_add_u32 s22, s36, 0x20080
	s_addc_u32 s23, s37, 0
	s_mov_b32 s33, m0
	s_mov_b32 m0, s62
	s_nop 2
	global_load_lds_dwordx4 v163, s[22:23]
	s_mov_b32 m0, s33
	s_mov_b32 s33, m0
	s_mov_b32 m0, s63
	s_nop 2
	global_load_lds_dwordx4 v165, s[22:23]
	s_mov_b32 m0, s33
	s_mov_b32 s22, m0
	s_mov_b32 m0, s60
	s_nop 2
	global_load_lds_dwordx4 v162, s[38:39]
	s_mov_b32 m0, s22
	s_mov_b32 s22, m0
	s_mov_b32 m0, s61
	s_nop 2
	global_load_lds_dwordx4 v164, s[38:39]
	s_mov_b32 m0, s22
	s_waitcnt vmcnt(8)
	s_waitcnt lgkmcnt(0)
	s_barrier
	s_setprio 1
	v_mfma_f32_16x16x128_f8f6f4 v[92:95], v[0:7], v[172:179], v[92:95]
	v_mfma_f32_16x16x128_f8f6f4 v[88:91], v[8:15], v[172:179], v[88:91]
	v_mfma_f32_16x16x128_f8f6f4 v[76:79], v[0:7], v[180:187], v[76:79]
	v_mfma_f32_16x16x128_f8f6f4 v[72:75], v[8:15], v[180:187], v[72:75]
	v_mfma_f32_16x16x128_f8f6f4 v[60:63], v[0:7], v[188:195], v[60:63]
	v_mfma_f32_16x16x128_f8f6f4 v[56:59], v[8:15], v[188:195], v[56:59]
	v_mfma_f32_16x16x128_f8f6f4 v[44:47], v[0:7], v[196:203], v[44:47]
	v_mfma_f32_16x16x128_f8f6f4 v[40:43], v[8:15], v[196:203], v[40:43]
	v_mfma_f32_16x16x128_f8f6f4 v[84:87], v[16:23], v[172:179], v[84:87]
	v_mfma_f32_16x16x128_f8f6f4 v[80:83], v[24:31], v[172:179], v[80:83]
	v_mfma_f32_16x16x128_f8f6f4 v[68:71], v[16:23], v[180:187], v[68:71]
	v_mfma_f32_16x16x128_f8f6f4 v[64:67], v[24:31], v[180:187], v[64:67]
	v_mfma_f32_16x16x128_f8f6f4 v[52:55], v[16:23], v[188:195], v[52:55]
	v_mfma_f32_16x16x128_f8f6f4 v[48:51], v[24:31], v[188:195], v[48:51]
	v_mfma_f32_16x16x128_f8f6f4 v[36:39], v[16:23], v[196:203], v[36:39]
	v_mfma_f32_16x16x128_f8f6f4 v[32:35], v[24:31], v[196:203], v[32:35]
	s_setprio 0
	s_barrier
	s_add_i32 s83, s83, 2
	s_add_u32 s81, s81, 0x100
	s_addc_u32 s82, s82, 0
	s_cmp_gt_u32 s83, 5
	s_cbranch_scc1 .LBB0_2130
	s_mov_b64 s[22:23], s[26:27]
	s_cmp_lg_u32 s83, -2
	s_cbranch_scc0 .LBB0_2121
	s_branch .LBB0_2128
